# baseline (speedup 1.0000x reference)
_Z9finish6_kPKDF16_PKfS2_S2_S2_S2_Pf:
	s_load_dwordx8 s[4:11], s[0:1], 0x0
	s_load_dwordx4 s[12:15], s[0:1], 0x20
	s_load_dwordx2 s[16:17], s[0:1], 0x30
	v_lshl_or_b32 v1, s2, 8, v0
	v_and_b32_e32 v50, 7, v0
	v_ashrrev_i32_e32 v0, 3, v1
	v_ashrrev_i32_e32 v1, 31, v0
	v_lshlrev_b64 v[2:3], 7, v[0:1]
	s_waitcnt lgkmcnt(0)
	s_load_dword s18, s[12:13], 0x0
	s_load_dword s19, s[14:15], 0x0
	v_lshl_add_u64 v[2:3], s[4:5], 0, v[2:3]
	v_lshlrev_b32_e32 v4, 4, v50
	v_mov_b32_e32 v5, 0
	v_lshl_add_u64 v[14:15], v[2:3], 0, v[4:5]
	s_mov_b32 s2, 0x201000
	v_add_co_u32_e32 v10, vcc, s2, v14
	s_mov_b32 s2, 0x402000
	s_nop 0
	v_addc_co_u32_e32 v11, vcc, 0, v15, vcc
	global_load_dwordx4 v[2:5], v[14:15], off nt
	global_load_dwordx4 v[6:9], v[10:11], off offset:256 nt
	v_add_co_u32_e32 v10, vcc, s2, v14
	s_mov_b32 s2, 0x603000
	s_nop 0
	v_addc_co_u32_e32 v11, vcc, 0, v15, vcc
	v_add_co_u32_e32 v14, vcc, s2, v14
	global_load_dwordx4 v[10:13], v[10:11], off offset:512 nt
	s_nop 0
	v_addc_co_u32_e32 v15, vcc, 0, v15, vcc
	global_load_dwordx4 v[14:17], v[14:15], off offset:768 nt
	v_lshlrev_b32_e32 v34, 5, v50
	global_load_dwordx4 v[18:21], v34, s[6:7]
	global_load_dwordx4 v[22:25], v34, s[6:7] offset:16
	global_load_dwordx4 v[26:29], v34, s[10:11]
	global_load_dwordx4 v[30:33], v34, s[10:11] offset:16
	s_load_dword s2, s[8:9], 0x0
	s_waitcnt vmcnt(7)
	v_cvt_f32_f16_e32 v34, v2
	v_cvt_f32_f16_sdwa v35, v2 dst_sel:DWORD dst_unused:UNUSED_PAD src0_sel:WORD_1
	v_cvt_f32_f16_e32 v2, v3
	v_cvt_f32_f16_sdwa v3, v3 dst_sel:DWORD dst_unused:UNUSED_PAD src0_sel:WORD_1
	s_waitcnt vmcnt(6)
	v_cvt_f32_f16_e32 v38, v6
	v_cvt_f32_f16_sdwa v39, v6 dst_sel:DWORD dst_unused:UNUSED_PAD src0_sel:WORD_1
	v_cvt_f32_f16_e32 v6, v7
	v_cvt_f32_f16_sdwa v7, v7 dst_sel:DWORD dst_unused:UNUSED_PAD src0_sel:WORD_1
	v_cvt_f32_f16_e32 v36, v4
	s_waitcnt vmcnt(5)
	v_cvt_f32_f16_e32 v40, v10
	v_cvt_f32_f16_sdwa v41, v10 dst_sel:DWORD dst_unused:UNUSED_PAD src0_sel:WORD_1
	v_cvt_f32_f16_e32 v10, v11
	s_waitcnt vmcnt(4)
	v_cvt_f32_f16_e32 v42, v14
	v_cvt_f32_f16_sdwa v43, v14 dst_sel:DWORD dst_unused:UNUSED_PAD src0_sel:WORD_1
	v_cvt_f32_f16_sdwa v11, v11 dst_sel:DWORD dst_unused:UNUSED_PAD src0_sel:WORD_1
	v_cvt_f32_f16_sdwa v37, v4 dst_sel:DWORD dst_unused:UNUSED_PAD src0_sel:WORD_1
	v_pk_add_f32 v[34:35], v[34:35], 0 op_sel_hi:[1,0]
	v_cvt_f32_f16_e32 v14, v15
	v_cvt_f32_f16_sdwa v15, v15 dst_sel:DWORD dst_unused:UNUSED_PAD src0_sel:WORD_1
	v_cvt_f32_f16_e32 v44, v8
	v_cvt_f32_f16_sdwa v45, v8 dst_sel:DWORD dst_unused:UNUSED_PAD src0_sel:WORD_1
	v_pk_add_f32 v[2:3], v[2:3], 0 op_sel_hi:[1,0]
	v_pk_add_f32 v[34:35], v[34:35], v[38:39]
	v_cvt_f32_f16_e32 v46, v12
	v_cvt_f32_f16_sdwa v47, v12 dst_sel:DWORD dst_unused:UNUSED_PAD src0_sel:WORD_1
	v_pk_add_f32 v[2:3], v[2:3], v[6:7]
	v_pk_add_f32 v[34:35], v[34:35], v[40:41]
	v_cvt_f32_f16_e32 v48, v16
	v_cvt_f32_f16_sdwa v49, v16 dst_sel:DWORD dst_unused:UNUSED_PAD src0_sel:WORD_1
	v_pk_add_f32 v[2:3], v[2:3], v[10:11]
	v_pk_add_f32 v[10:11], v[34:35], v[42:43]
	v_pk_add_f32 v[36:37], v[36:37], 0 op_sel_hi:[1,0]
	s_waitcnt vmcnt(3)
	v_pk_add_f32 v[10:11], v[10:11], v[18:19]
	v_pk_add_f32 v[6:7], v[36:37], v[44:45]
	v_pk_add_f32 v[2:3], v[2:3], v[14:15]
	s_waitcnt lgkmcnt(0)
	v_mul_f32_e32 v12, s2, v10
	v_cmp_le_f32_e32 vcc, 0, v10
	v_pk_add_f32 v[6:7], v[6:7], v[46:47]
	v_pk_add_f32 v[2:3], v[2:3], v[20:21]
	v_mul_f32_e32 v14, s2, v11
	v_cndmask_b32_e32 v10, v12, v10, vcc
	v_cmp_le_f32_e32 vcc, 0, v11
	v_pk_add_f32 v[6:7], v[6:7], v[48:49]
	v_mul_f32_e32 v15, s2, v2
	v_cndmask_b32_e32 v11, v14, v11, vcc
	v_cmp_le_f32_e32 vcc, 0, v2
	s_waitcnt vmcnt(1)
	v_fma_f32 v10, v26, v10, 0
	v_pk_add_f32 v[6:7], v[6:7], v[22:23]
	v_mul_f32_e32 v16, s2, v3
	v_cndmask_b32_e32 v2, v15, v2, vcc
	v_cmp_le_f32_e32 vcc, 0, v3
	v_fmac_f32_e32 v10, v27, v11
	v_cvt_f32_f16_e32 v4, v5
	v_cvt_f32_f16_sdwa v5, v5 dst_sel:DWORD dst_unused:UNUSED_PAD src0_sel:WORD_1
	v_mul_f32_e32 v18, s2, v6
	v_cndmask_b32_e32 v3, v16, v3, vcc
	v_cmp_le_f32_e32 vcc, 0, v6
	v_fmac_f32_e32 v10, v28, v2
	v_cvt_f32_f16_e32 v8, v9
	v_cvt_f32_f16_sdwa v9, v9 dst_sel:DWORD dst_unused:UNUSED_PAD src0_sel:WORD_1
	v_mul_f32_e32 v19, s2, v7
	v_cndmask_b32_e32 v6, v18, v6, vcc
	v_cmp_le_f32_e32 vcc, 0, v7
	v_fmac_f32_e32 v10, v29, v3
	s_waitcnt vmcnt(0)
	v_fmac_f32_e32 v10, v30, v6
	v_cndmask_b32_e32 v7, v19, v7, vcc
	v_cvt_f32_f16_e32 v2, v13
	v_cvt_f32_f16_sdwa v3, v13 dst_sel:DWORD dst_unused:UNUSED_PAD src0_sel:WORD_1
	v_fmac_f32_e32 v10, v31, v7
	v_cvt_f32_f16_e32 v6, v17
	v_cvt_f32_f16_sdwa v7, v17 dst_sel:DWORD dst_unused:UNUSED_PAD src0_sel:WORD_1
	v_pk_add_f32 v[4:5], v[4:5], 0 op_sel_hi:[1,0]
	s_nop 0
	v_pk_add_f32 v[4:5], v[4:5], v[8:9]
	s_nop 0
	v_pk_add_f32 v[2:3], v[4:5], v[2:3]
	s_nop 0
	v_pk_add_f32 v[2:3], v[2:3], v[6:7]
	s_nop 0
	v_pk_add_f32 v[2:3], v[2:3], v[24:25]
	s_nop 0
	v_mul_f32_e32 v4, s2, v2
	v_cmp_le_f32_e32 vcc, 0, v2
	s_nop 1
	v_cndmask_b32_e32 v2, v4, v2, vcc
	v_fmac_f32_e32 v10, v32, v2
	v_mul_f32_e32 v2, s2, v3
	v_cmp_le_f32_e32 vcc, 0, v3
	s_nop 1
	v_cndmask_b32_e32 v2, v2, v3, vcc
	v_fmac_f32_e32 v10, v33, v2
	v_mbcnt_lo_u32_b32 v2, -1, 0
	v_mbcnt_hi_u32_b32 v3, -1, v2
	v_and_b32_e32 v4, 64, v3
	v_xor_b32_e32 v2, 4, v3
	v_add_u32_e32 v4, 64, v4
	v_cmp_lt_i32_e32 vcc, v2, v4
	v_xor_b32_e32 v5, 2, v3
	s_nop 0
	v_cndmask_b32_e32 v2, v3, v2, vcc
	v_lshlrev_b32_e32 v2, 2, v2
	ds_bpermute_b32 v2, v2, v10
	v_cmp_lt_i32_e32 vcc, v5, v4
	s_waitcnt lgkmcnt(0)
	v_add_f32_e32 v2, v10, v2
	v_cndmask_b32_e32 v5, v3, v5, vcc
	v_lshlrev_b32_e32 v5, 2, v5
	ds_bpermute_b32 v5, v5, v2
	s_waitcnt lgkmcnt(0)
	v_add_f32_e32 v2, v2, v5
	v_xor_b32_e32 v5, 1, v3
	v_cmp_lt_i32_e32 vcc, v5, v4
	s_nop 1
	v_cndmask_b32_e32 v3, v3, v5, vcc
	v_lshlrev_b32_e32 v3, 2, v3
	ds_bpermute_b32 v3, v3, v2
	v_cmp_eq_u32_e32 vcc, 0, v50
	s_and_saveexec_b64 s[2:3], vcc
	s_cbranch_execz .LBB1_2
	s_waitcnt lgkmcnt(0)
	v_add_f32_e32 v2, v2, v3
	v_lshl_add_u64 v[0:1], v[0:1], 2, s[16:17]
	v_add_f32_e32 v2, s18, v2
	v_mul_f32_e32 v3, s19, v2
	v_cmp_le_f32_e32 vcc, 0, v2
	s_nop 1
	v_cndmask_b32_e32 v2, v3, v2, vcc
	global_store_dword v[0:1], v2, off

	.amdhsa_kernel _Z9finish6_kPKDF16_PKfS2_S2_S2_S2_Pf
		.amdhsa_group_segment_fixed_size 0
		.amdhsa_private_segment_fixed_size 0
		.amdhsa_kernarg_size 56
		.amdhsa_user_sgpr_count 2
		.amdhsa_user_sgpr_dispatch_ptr 0
		.amdhsa_user_sgpr_queue_ptr 0
		.amdhsa_user_sgpr_kernarg_segment_ptr 1
		.amdhsa_user_sgpr_dispatch_id 0
		.amdhsa_user_sgpr_kernarg_preload_length 0
		.amdhsa_user_sgpr_kernarg_preload_offset 0
		.amdhsa_user_sgpr_private_segment_size 0
		.amdhsa_uses_dynamic_stack 0
		.amdhsa_enable_private_segment 0
		.amdhsa_system_sgpr_workgroup_id_x 1
		.amdhsa_system_sgpr_workgroup_id_y 0
		.amdhsa_system_sgpr_workgroup_id_z 0
		.amdhsa_system_sgpr_workgroup_info 0
		.amdhsa_system_vgpr_workitem_id 0
		.amdhsa_next_free_vgpr 51
		.amdhsa_next_free_sgpr 20
		.amdhsa_accum_offset 52
		.amdhsa_reserve_vcc 1
		.amdhsa_float_round_mode_32 0
		.amdhsa_float_round_mode_16_64 0
		.amdhsa_float_denorm_mode_32 3
		.amdhsa_float_denorm_mode_16_64 3
		.amdhsa_dx10_clamp 1
		.amdhsa_ieee_mode 1
		.amdhsa_fp16_overflow 0
		.amdhsa_tg_split 0
		.amdhsa_exception_fp_ieee_invalid_op 0
		.amdhsa_exception_fp_denorm_src 0
		.amdhsa_exception_fp_ieee_div_zero 0
		.amdhsa_exception_fp_ieee_overflow 0
		.amdhsa_exception_fp_ieee_underflow 0
		.amdhsa_exception_fp_ieee_inexact 0
		.amdhsa_exception_int_div_zero 0
	.end_amdhsa_kernel

_Z6conv_kILi64ELi128ELi20ELi128ELi4ELi4ELb1EEvPKDF16_S1_PKfS3_PDF16_S4_S1_fS3_S3_S3_S3_:
	s_load_dwordx2 s[22:23], s[0:1], 0x8
	s_load_dword s88, s[0:1], 0x38
	s_load_dwordx8 s[24:31], s[0:1], 0x40
	v_readfirstlane_b32 s34, v0
	s_lshr_b32 s35, s34, 6
	v_lshlrev_b32_e32 v1, 3, v0
	v_and_b32_e32 v2, 48, v0
	s_and_b32 s33, s2, 3
	v_bitop3_b32 v2, v1, v2, 56 bitop3:0x6c
	s_lshl_b32 s5, s35, 10
	v_and_b32_e32 v1, 0x1c0, v1
	s_and_b32 s4, s2, 56
	v_or3_b32 v18, s5, v1, v2
	v_and_b32_e32 v1, 7, v0
	s_mul_i32 s5, s33, 5
	v_or_b32_e32 v97, 0x200, v0
	s_lshl_b32 s3, s2, 3
	v_lshlrev_b32_e32 v19, 5, v1
	s_add_i32 s4, s4, s5
	v_mul_u32_u24_e32 v23, 0x283, v97
	s_and_b32 s3, s3, 32
	s_waitcnt lgkmcnt(0)
	global_load_dwordx4 v[2:5], v19, s[26:27] offset:16
	global_load_dwordx4 v[6:9], v19, s[28:29] offset:16
	global_load_dwordx4 v[10:13], v19, s[26:27]
	global_load_dwordx4 v[14:17], v19, s[28:29]
	s_add_i32 s20, s4, -9
	v_mul_u32_u24_e32 v19, 0xa1, v0
	s_movk_i32 s4, 0xffcd
	v_lshrrev_b32_e32 v23, 18, v23
	s_add_i32 s21, s3, -9
	v_lshrrev_b32_e32 v37, 3, v0
	v_mul_i32_i24_sdwa v20, v19, s4 dst_sel:DWORD dst_unused:UNUSED_PAD src0_sel:WORD_1 src1_sel:DWORD
	v_lshrrev_b32_e32 v50, 3, v97
	v_mul_i32_i24_e32 v24, 0xffffffcd, v23
	v_add_u32_sdwa v19, s20, v19 dst_sel:DWORD dst_unused:UNUSED_PAD src0_sel:DWORD src1_sel:WORD_1
	v_add3_u32 v20, s21, v37, v20
	v_add_u32_e32 v23, s20, v23
	v_add3_u32 v24, s21, v50, v24
	v_max_u32_e32 v21, v19, v20
	v_max_u32_e32 v25, v23, v24
	v_cmp_gt_u32_e64 s[16:17], 64, v21
	v_cmp_lt_u32_e64 s[14:15], 63, v25
	s_and_b32 s28, s2, 0xffffffc0
	v_cndmask_b32_e64 v19, 0, v19, s[16:17]
	v_cndmask_b32_e64 v23, v23, 0, s[14:15]
	v_or_b32_e32 v19, s28, v19
	v_cndmask_b32_e64 v20, 0, v20, s[16:17]
	v_or_b32_e32 v23, s28, v23
	v_cndmask_b32_e64 v24, v24, 0, s[14:15]
	v_lshl_add_u32 v20, v19, 6, v20
	v_cndmask_b32_e64 v19, 0, 1, s[16:17]
	v_lshl_add_u32 v24, v23, 6, v24
	v_cndmask_b32_e64 v23, 2, 0, s[14:15]
	v_or_b32_e32 v102, 0x400, v0
	v_or_b32_e32 v19, v23, v19
	v_mul_u32_u24_e32 v23, 0xa0b, v102
	v_lshrrev_b32_e32 v23, 20, v23
	v_lshrrev_b32_e32 v51, 3, v102
	v_mul_i32_i24_e32 v26, 0xffffffcd, v23
	v_add_u32_e32 v23, s20, v23
	v_add3_u32 v26, s21, v51, v26
	v_max_u32_e32 v27, v23, v26
	v_cmp_lt_u32_e64 s[12:13], 63, v27
	v_or_b32_e32 v103, 0x600, v0
	v_lshrrev_b32_e32 v52, 3, v103
	v_cndmask_b32_e64 v23, v23, 0, s[12:13]
	v_or_b32_e32 v23, s28, v23
	v_cndmask_b32_e64 v26, v26, 0, s[12:13]
	v_lshl_add_u32 v26, v23, 6, v26
	v_ashrrev_i32_e32 v27, 31, v26
	v_lshl_add_u64 v[38:39], v[26:27], 2, s[24:25]
	v_mul_u32_u24_e32 v26, 0xa0b, v103
	v_lshrrev_b32_e32 v26, 20, v26
	v_mul_i32_i24_e32 v27, 0xffffffcd, v26
	v_add_u32_e32 v26, s20, v26
	v_add3_u32 v27, s21, v52, v27
	v_max_u32_e32 v28, v26, v27
	v_cmp_lt_u32_e64 s[10:11], 63, v28
	v_cndmask_b32_e64 v23, 4, 0, s[12:13]
	v_or_b32_e32 v104, 0x800, v0
	v_cndmask_b32_e64 v26, v26, 0, s[10:11]
	v_or_b32_e32 v26, s28, v26
	v_cndmask_b32_e64 v27, v27, 0, s[10:11]
	v_lshl_add_u32 v26, v26, 6, v27
	v_ashrrev_i32_e32 v27, 31, v26
	v_lshl_add_u64 v[40:41], v[26:27], 2, s[24:25]
	v_cndmask_b32_e64 v26, 8, 0, s[10:11]
	v_or3_b32 v19, v19, v23, v26
	v_mul_u32_u24_e32 v23, 0x1415, v104
	v_lshrrev_b32_e32 v23, 21, v23
	v_lshrrev_b32_e32 v35, 3, v104
	v_mul_i32_i24_e32 v26, 0xffffffcd, v23
	v_add_u32_e32 v23, s20, v23
	v_add3_u32 v26, s21, v35, v26
	v_max_u32_e32 v27, v23, v26
	v_cmp_lt_u32_e64 s[8:9], 63, v27
	v_or_b32_e32 v105, 0xa00, v0
	v_lshrrev_b32_e32 v33, 3, v105
	v_cndmask_b32_e64 v23, v23, 0, s[8:9]
	v_or_b32_e32 v23, s28, v23
	v_cndmask_b32_e64 v26, v26, 0, s[8:9]
	v_lshl_add_u32 v26, v23, 6, v26
	v_ashrrev_i32_e32 v27, 31, v26
	v_lshl_add_u64 v[42:43], v[26:27], 2, s[24:25]
	v_mul_u32_u24_e32 v26, 0x1415, v105
	v_lshrrev_b32_e32 v26, 21, v26
	v_mul_i32_i24_e32 v27, 0xffffffcd, v26
	v_add_u32_e32 v26, s20, v26
	v_add3_u32 v27, s21, v33, v27
	v_max_u32_e32 v28, v26, v27
	v_cmp_lt_u32_e64 s[6:7], 63, v28
	v_cndmask_b32_e64 v23, 16, 0, s[8:9]
	v_or_b32_e32 v106, 0xc00, v0
	v_cndmask_b32_e64 v26, v26, 0, s[6:7]
	v_or_b32_e32 v26, s28, v26
	v_cndmask_b32_e64 v27, v27, 0, s[6:7]
	v_lshl_add_u32 v26, v26, 6, v27
	v_ashrrev_i32_e32 v27, 31, v26
	v_lshl_add_u64 v[44:45], v[26:27], 2, s[24:25]
	v_cndmask_b32_e64 v26, 32, 0, s[6:7]
	v_or3_b32 v30, v19, v23, v26
	v_mul_u32_u24_e32 v19, 0x1415, v106
	v_lshrrev_b32_e32 v19, 21, v19
	v_lshrrev_b32_e32 v31, 3, v106
	v_mul_i32_i24_e32 v23, 0xffffffcd, v19
	v_add_u32_e32 v19, s20, v19
	v_add3_u32 v23, s21, v31, v23
	v_max_u32_e32 v26, v19, v23
	v_cmp_gt_u32_e32 vcc, 64, v26
	v_or_b32_e32 v107, 0xe00, v0
	v_ashrrev_i32_e32 v21, 31, v20
	v_cndmask_b32_e32 v19, 0, v19, vcc
	v_or_b32_e32 v19, s28, v19
	v_cndmask_b32_e32 v23, 0, v23, vcc
	v_lshl_add_u32 v26, v19, 6, v23
	v_mul_u32_u24_e32 v23, 0x1415, v107
	v_ashrrev_i32_e32 v27, 31, v26
	v_lshrrev_b32_e32 v23, 21, v23
	v_lshl_add_u64 v[46:47], v[26:27], 2, s[24:25]
	v_lshrrev_b32_e32 v26, 3, v107
	v_mul_i32_i24_e32 v27, 0xffffffcd, v23
	v_add_u32_e32 v23, s20, v23
	v_add3_u32 v27, s21, v26, v27
	v_max_u32_e32 v28, v23, v27
	v_cndmask_b32_e64 v19, 0, 64, vcc
	v_cmp_gt_u32_e32 vcc, 64, v28
	v_lshl_add_u64 v[20:21], v[20:21], 2, s[24:25]
	v_ashrrev_i32_e32 v25, 31, v24
	v_cndmask_b32_e32 v23, 0, v23, vcc
	v_or_b32_e32 v23, s28, v23
	v_cndmask_b32_e32 v27, 0, v27, vcc
	v_lshl_add_u32 v28, v23, 6, v27
	v_ashrrev_i32_e32 v29, 31, v28
	s_load_dword s26, s[30:31], 0x0
	v_lshl_add_u64 v[24:25], v[24:25], 2, s[24:25]
	v_lshl_add_u64 v[48:49], v[28:29], 2, s[24:25]
	global_load_dword v53, v[20:21], off
	global_load_dword v54, v[24:25], off
	global_load_dword v55, v[38:39], off
	global_load_dword v56, v[40:41], off
	global_load_dword v57, v[42:43], off
	global_load_dword v36, v[44:45], off
	global_load_dword v34, v[46:47], off
	global_load_dword v29, v[48:49], off
	v_mov_b32_e32 v20, 0x80
	v_cndmask_b32_e32 v20, 0, v20, vcc
	v_or_b32_e32 v32, v19, v20
	v_or_b32_e32 v20, 0x1000, v0
	v_mul_u32_u24_e32 v21, 0x2829, v20
	v_lshrrev_b32_e32 v21, 22, v21
	v_lshrrev_b32_e32 v24, 3, v20
	v_mul_i32_i24_e32 v23, 0xffffffcd, v21
	v_add_u32_e32 v28, s20, v21
	s_movk_i32 s4, 0x1320
	v_add3_u32 v27, s21, v24, v23
	v_cmp_gt_u32_e64 s[4:5], s4, v20
	v_cmp_gt_u32_e32 vcc, 64, v28
	s_and_b64 s[18:19], s[4:5], vcc
	v_cmp_gt_u32_e32 vcc, 64, v27
	v_mov_b32_e32 v20, 0x100
	s_and_b64 s[18:19], s[18:19], vcc
	v_cndmask_b32_e64 v23, 0, v20, s[18:19]
	v_or_b32_e32 v20, 0x1200, v0
	v_lshrrev_b32_e32 v21, 3, v20
	v_mul_u32_u24_e32 v20, 0x2829, v20
	v_lshrrev_b32_e32 v20, 22, v20
	v_mul_i32_i24_e32 v25, 0xffffffcd, v20
	v_add_u32_e32 v20, s20, v20
	s_movk_i32 s20, 0x120
	v_add3_u32 v25, s21, v21, v25
	v_cmp_gt_u32_e32 vcc, s20, v0
	v_cmp_gt_u32_e64 s[20:21], 64, v20
	s_and_b64 s[30:31], vcc, s[20:21]
	v_cmp_gt_u32_e64 s[20:21], 64, v25
	s_and_b64 s[20:21], s[30:31], s[20:21]
	s_lshl_b32 s36, s35, 11
	v_cndmask_b32_e64 v20, 0, v20, s[20:21]
	v_or_b32_e32 v20, s28, v20
	v_cndmask_b32_e64 v25, 0, v25, s[20:21]
	v_lshl_add_u32 v38, v20, 6, v25
	v_mov_b32_e32 v25, 0x200
	v_or_b32_e32 v19, v32, v30
	v_ashrrev_i32_e32 v39, 31, v38
	v_cndmask_b32_e64 v25, 0, v25, s[20:21]
	s_add_i32 s27, s36, 0x14000
	s_mul_i32 s20, s33, 0x190000
	v_lshl_add_u64 v[38:39], v[38:39], 2, s[24:25]
	v_or3_b32 v25, v23, v25, v19
	v_mov_b32_e32 v19, 0
	s_add_u32 s20, s22, s20
	global_load_dword v20, v[38:39], off
	s_addc_u32 s21, s23, 0
	v_lshlrev_b64 v[38:39], 1, v[18:19]
	v_lshl_add_u64 v[40:41], s[20:21], 0, v[38:39]
	s_mov_b32 m0, s27
	s_mov_b64 s[30:31], 0x400
	global_load_lds_dwordx4 v[40:41], off
	s_add_i32 m0, s36, 0x14400
	v_lshl_add_u64 v[40:41], v[40:41], 0, s[30:31]
	s_add_u32 s30, s20, 0x50000
	s_addc_u32 s31, s21, 0
	global_load_lds_dwordx4 v[40:41], off
	s_add_i32 m0, s36, 0x18000
	v_lshl_add_u64 v[40:41], s[30:31], 0, v[38:39]
	v_or_b32_e32 v22, 0x200, v18
	v_mov_b32_e32 v23, v19
	global_load_lds_dwordx4 v[40:41], off
	s_add_i32 m0, s36, 0x18400
	v_lshlrev_b64 v[22:23], 1, v[22:23]
	s_add_u32 s20, s20, 0xa0000
	v_lshl_add_u64 v[40:41], s[30:31], 0, v[22:23]
	s_addc_u32 s21, s21, 0
	global_load_lds_dwordx4 v[40:41], off
	s_add_i32 m0, s36, 0x1c000
	v_lshl_add_u64 v[38:39], s[20:21], 0, v[38:39]
	global_load_lds_dwordx4 v[38:39], off
	v_lshl_add_u64 v[22:23], s[20:21], 0, v[22:23]
	s_add_i32 m0, s36, 0x1c400
	s_movk_i32 s29, 0x80
	global_load_lds_dwordx4 v[22:23], off
	s_waitcnt vmcnt(6)
	v_fma_f32 v22, v53, v10, v14
	s_waitcnt lgkmcnt(0)
	v_mul_f32_e32 v23, s26, v22
	v_cmp_le_f32_e64 s[20:21], 0, v22
	s_nop 1
	v_cndmask_b32_e64 v22, v23, v22, s[20:21]
	v_fma_f32 v23, v53, v11, v15
	v_mul_f32_e32 v38, s26, v23
	v_cmp_le_f32_e64 s[20:21], 0, v23
	v_cvt_f16_f32_e32 v22, v22
	v_cndmask_b32_e64 v22, 0, v22, s[16:17]
	v_cndmask_b32_e64 v23, v38, v23, s[20:21]
	v_fma_f32 v38, v53, v12, v16
	v_mul_f32_e32 v39, s26, v38
	v_cmp_le_f32_e64 s[20:21], 0, v38
	v_cvt_f16_f32_e32 v23, v23
	v_cndmask_b32_e64 v23, 0, v23, s[16:17]
	v_cndmask_b32_e64 v38, v39, v38, s[20:21]
	v_fma_f32 v39, v53, v13, v17
	v_mul_f32_e32 v40, s26, v39
	v_cmp_le_f32_e64 s[20:21], 0, v39
	v_cvt_f16_f32_e32 v38, v38
	v_cndmask_b32_e64 v38, 0, v38, s[16:17]
	v_cndmask_b32_e64 v39, v40, v39, s[20:21]
	v_fma_f32 v40, v53, v2, v6
	v_mul_f32_e32 v41, s26, v40
	v_cmp_le_f32_e64 s[20:21], 0, v40
	v_cvt_f16_f32_e32 v39, v39
	v_cndmask_b32_e64 v39, 0, v39, s[16:17]
	v_cndmask_b32_e64 v40, v41, v40, s[20:21]
	v_fma_f32 v41, v53, v3, v7
	v_mul_f32_e32 v42, s26, v41
	v_cmp_le_f32_e64 s[20:21], 0, v41
	v_cvt_f16_f32_e32 v40, v40
	v_pack_b32_f16 v39, v38, v39
	v_cndmask_b32_e64 v41, v42, v41, s[20:21]
	v_fma_f32 v42, v53, v4, v8
	v_mul_f32_e32 v43, s26, v42
	v_cmp_le_f32_e64 s[20:21], 0, v42
	v_cvt_f16_f32_e32 v41, v41
	v_pack_b32_f16 v38, v22, v23
	v_cndmask_b32_e64 v42, v43, v42, s[20:21]
	v_fma_f32 v43, v53, v5, v9
	v_mul_f32_e32 v44, s26, v43
	v_cmp_le_f32_e64 s[20:21], 0, v43
	v_cvt_f16_f32_e32 v42, v42
	v_bitop3_b32 v22, v37, v1, 6 bitop3:0x6c
	v_cndmask_b32_e64 v43, v44, v43, s[20:21]
	v_cvt_f16_f32_e32 v43, v43
	v_cndmask_b32_e64 v40, 0, v40, s[16:17]
	v_cndmask_b32_e64 v44, 0, v41, s[16:17]
	v_cndmask_b32_e64 v41, 0, v42, s[16:17]
	v_cndmask_b32_e64 v42, 0, v43, s[16:17]
	v_lshlrev_b32_e32 v22, 4, v22
	v_pack_b32_f16 v41, v41, v42
	v_pack_b32_f16 v40, v40, v44
	v_lshl_or_b32 v22, v37, 7, v22
	ds_write_b128 v22, v[38:41]
	v_fma_f32 v22, v54, v10, v14
	v_mul_f32_e32 v23, s26, v22
	v_cmp_le_f32_e64 s[16:17], 0, v22
	s_nop 1
	v_cndmask_b32_e64 v22, v23, v22, s[16:17]
	v_fma_f32 v23, v54, v11, v15
	v_mul_f32_e32 v37, s26, v23
	v_cmp_le_f32_e64 s[16:17], 0, v23
	v_cvt_f16_f32_e32 v22, v22
	v_cndmask_b32_e64 v22, v22, 0, s[14:15]
	v_cndmask_b32_e64 v23, v37, v23, s[16:17]
	v_fma_f32 v37, v54, v12, v16
	v_mul_f32_e32 v38, s26, v37
	v_cmp_le_f32_e64 s[16:17], 0, v37
	v_cvt_f16_f32_e32 v23, v23
	v_cndmask_b32_e64 v23, v23, 0, s[14:15]
	v_cndmask_b32_e64 v37, v38, v37, s[16:17]
	v_fma_f32 v38, v54, v13, v17
	v_mul_f32_e32 v39, s26, v38
	v_cmp_le_f32_e64 s[16:17], 0, v38
	v_cvt_f16_f32_e32 v37, v37
	v_cndmask_b32_e64 v37, v37, 0, s[14:15]
	v_cndmask_b32_e64 v38, v39, v38, s[16:17]
	v_fma_f32 v39, v54, v2, v6
	v_mul_f32_e32 v40, s26, v39
	v_cmp_le_f32_e64 s[16:17], 0, v39
	v_cvt_f16_f32_e32 v38, v38
	v_cndmask_b32_e64 v38, v38, 0, s[14:15]
	v_cndmask_b32_e64 v39, v40, v39, s[16:17]
	v_fma_f32 v40, v54, v3, v7
	v_mul_f32_e32 v41, s26, v40
	v_cmp_le_f32_e64 s[16:17], 0, v40
	v_cvt_f16_f32_e32 v39, v39
	v_cndmask_b32_e64 v39, v39, 0, s[14:15]
	v_cndmask_b32_e64 v40, v41, v40, s[16:17]
	v_fma_f32 v41, v54, v4, v8
	v_mul_f32_e32 v42, s26, v41
	v_cmp_le_f32_e64 s[16:17], 0, v41
	v_cvt_f16_f32_e32 v40, v40
	v_cndmask_b32_e64 v40, v40, 0, s[14:15]
	v_cndmask_b32_e64 v41, v42, v41, s[16:17]
	v_fma_f32 v42, v54, v5, v9
	v_mul_f32_e32 v43, s26, v42
	v_cmp_le_f32_e64 s[16:17], 0, v42
	v_cvt_f16_f32_e32 v41, v41
	v_pack_b32_f16 v40, v39, v40
	v_cndmask_b32_e64 v42, v43, v42, s[16:17]
	v_cvt_f16_f32_e32 v42, v42
	v_pack_b32_f16 v39, v37, v38
	v_pack_b32_f16 v38, v22, v23
	v_bitop3_b32 v22, v50, v1, 6 bitop3:0x6c
	v_cndmask_b32_e64 v41, v41, 0, s[14:15]
	v_cndmask_b32_e64 v42, v42, 0, s[14:15]
	v_lshlrev_b32_e32 v22, 4, v22
	v_pack_b32_f16 v41, v41, v42
	v_lshl_or_b32 v22, v50, 7, v22
	ds_write_b128 v22, v[38:41]
	v_fma_f32 v22, v55, v10, v14
	v_mul_f32_e32 v23, s26, v22
	v_cmp_le_f32_e64 s[14:15], 0, v22
	s_nop 1
	v_cndmask_b32_e64 v22, v23, v22, s[14:15]
	v_fma_f32 v23, v55, v11, v15
	v_mul_f32_e32 v37, s26, v23
	v_cmp_le_f32_e64 s[14:15], 0, v23
	v_cvt_f16_f32_e32 v22, v22
	v_cndmask_b32_e64 v22, v22, 0, s[12:13]
	v_cndmask_b32_e64 v23, v37, v23, s[14:15]
	v_fma_f32 v37, v55, v12, v16
	v_mul_f32_e32 v38, s26, v37
	v_cmp_le_f32_e64 s[14:15], 0, v37
	v_cvt_f16_f32_e32 v23, v23
	v_cndmask_b32_e64 v23, v23, 0, s[12:13]
	v_cndmask_b32_e64 v37, v38, v37, s[14:15]
	v_fma_f32 v38, v55, v13, v17
	v_mul_f32_e32 v39, s26, v38
	v_cmp_le_f32_e64 s[14:15], 0, v38
	v_cvt_f16_f32_e32 v37, v37
	v_cndmask_b32_e64 v37, v37, 0, s[12:13]
	v_cndmask_b32_e64 v38, v39, v38, s[14:15]
	v_fma_f32 v39, v55, v2, v6
	v_mul_f32_e32 v40, s26, v39
	v_cmp_le_f32_e64 s[14:15], 0, v39
	v_cvt_f16_f32_e32 v38, v38
	v_cndmask_b32_e64 v38, v38, 0, s[12:13]
	v_cndmask_b32_e64 v39, v40, v39, s[14:15]
	v_fma_f32 v40, v55, v3, v7
	v_mul_f32_e32 v41, s26, v40
	v_cmp_le_f32_e64 s[14:15], 0, v40
	v_cvt_f16_f32_e32 v39, v39
	v_cndmask_b32_e64 v39, v39, 0, s[12:13]
	v_cndmask_b32_e64 v40, v41, v40, s[14:15]
	v_fma_f32 v41, v55, v4, v8
	v_mul_f32_e32 v42, s26, v41
	v_cmp_le_f32_e64 s[14:15], 0, v41
	v_cvt_f16_f32_e32 v40, v40
	v_cndmask_b32_e64 v40, v40, 0, s[12:13]
	v_cndmask_b32_e64 v41, v42, v41, s[14:15]
	v_fma_f32 v42, v55, v5, v9
	v_mul_f32_e32 v43, s26, v42
	v_cmp_le_f32_e64 s[14:15], 0, v42
	v_cvt_f16_f32_e32 v41, v41
	v_pack_b32_f16 v40, v39, v40
	v_cndmask_b32_e64 v42, v43, v42, s[14:15]
	v_cvt_f16_f32_e32 v42, v42
	v_pack_b32_f16 v39, v37, v38
	v_pack_b32_f16 v38, v22, v23
	v_bitop3_b32 v22, v51, v1, 6 bitop3:0x6c
	v_cndmask_b32_e64 v41, v41, 0, s[12:13]
	v_cndmask_b32_e64 v42, v42, 0, s[12:13]
	v_lshlrev_b32_e32 v22, 4, v22
	v_pack_b32_f16 v41, v41, v42
	v_lshl_or_b32 v22, v51, 7, v22
	ds_write_b128 v22, v[38:41]
	v_fma_f32 v22, v56, v10, v14
	v_mul_f32_e32 v23, s26, v22
	v_cmp_le_f32_e64 s[12:13], 0, v22
	s_nop 1
	v_cndmask_b32_e64 v22, v23, v22, s[12:13]
	v_fma_f32 v23, v56, v11, v15
	v_mul_f32_e32 v37, s26, v23
	v_cmp_le_f32_e64 s[12:13], 0, v23
	v_cvt_f16_f32_e32 v22, v22
	v_cndmask_b32_e64 v22, v22, 0, s[10:11]
	v_cndmask_b32_e64 v23, v37, v23, s[12:13]
	v_fma_f32 v37, v56, v12, v16
	v_mul_f32_e32 v38, s26, v37
	v_cmp_le_f32_e64 s[12:13], 0, v37
	v_cvt_f16_f32_e32 v23, v23
	v_cndmask_b32_e64 v23, v23, 0, s[10:11]
	v_cndmask_b32_e64 v37, v38, v37, s[12:13]
	v_fma_f32 v38, v56, v13, v17
	v_mul_f32_e32 v39, s26, v38
	v_cmp_le_f32_e64 s[12:13], 0, v38
	v_cvt_f16_f32_e32 v37, v37
	v_cndmask_b32_e64 v37, v37, 0, s[10:11]
	v_cndmask_b32_e64 v38, v39, v38, s[12:13]
	v_fma_f32 v39, v56, v2, v6
	v_mul_f32_e32 v40, s26, v39
	v_cmp_le_f32_e64 s[12:13], 0, v39
	v_cvt_f16_f32_e32 v38, v38
	v_cndmask_b32_e64 v38, v38, 0, s[10:11]
	v_cndmask_b32_e64 v39, v40, v39, s[12:13]
	v_fma_f32 v40, v56, v3, v7
	v_mul_f32_e32 v41, s26, v40
	v_cmp_le_f32_e64 s[12:13], 0, v40
	v_cvt_f16_f32_e32 v39, v39
	v_cndmask_b32_e64 v39, v39, 0, s[10:11]
	v_cndmask_b32_e64 v40, v41, v40, s[12:13]
	v_fma_f32 v41, v56, v4, v8
	v_mul_f32_e32 v42, s26, v41
	v_cmp_le_f32_e64 s[12:13], 0, v41
	v_cvt_f16_f32_e32 v40, v40
	v_cndmask_b32_e64 v40, v40, 0, s[10:11]
	v_cndmask_b32_e64 v41, v42, v41, s[12:13]
	v_fma_f32 v42, v56, v5, v9
	v_mul_f32_e32 v43, s26, v42
	v_cmp_le_f32_e64 s[12:13], 0, v42
	v_cvt_f16_f32_e32 v41, v41
	v_pack_b32_f16 v40, v39, v40
	v_cndmask_b32_e64 v42, v43, v42, s[12:13]
	v_cvt_f16_f32_e32 v42, v42
	v_pack_b32_f16 v39, v37, v38
	v_pack_b32_f16 v38, v22, v23
	v_bitop3_b32 v22, v52, v1, 6 bitop3:0x6c
	v_cndmask_b32_e64 v41, v41, 0, s[10:11]
	v_cndmask_b32_e64 v42, v42, 0, s[10:11]
	v_lshlrev_b32_e32 v22, 4, v22
	v_pack_b32_f16 v41, v41, v42
	v_lshl_or_b32 v22, v52, 7, v22
	ds_write_b128 v22, v[38:41]
	v_fma_f32 v22, v57, v10, v14
	v_mul_f32_e32 v23, s26, v22
	v_cmp_le_f32_e64 s[10:11], 0, v22
	s_nop 1
	v_cndmask_b32_e64 v22, v23, v22, s[10:11]
	v_fma_f32 v23, v57, v11, v15
	v_mul_f32_e32 v37, s26, v23
	v_cmp_le_f32_e64 s[10:11], 0, v23
	v_cvt_f16_f32_e32 v22, v22
	v_cndmask_b32_e64 v22, v22, 0, s[8:9]
	v_cndmask_b32_e64 v23, v37, v23, s[10:11]
	v_fma_f32 v37, v57, v12, v16
	v_mul_f32_e32 v38, s26, v37
	v_cmp_le_f32_e64 s[10:11], 0, v37
	v_cvt_f16_f32_e32 v23, v23
	v_cndmask_b32_e64 v23, v23, 0, s[8:9]
	v_cndmask_b32_e64 v37, v38, v37, s[10:11]
	v_fma_f32 v38, v57, v13, v17
	v_mul_f32_e32 v39, s26, v38
	v_cmp_le_f32_e64 s[10:11], 0, v38
	v_cvt_f16_f32_e32 v37, v37
	v_cndmask_b32_e64 v37, v37, 0, s[8:9]
	v_cndmask_b32_e64 v38, v39, v38, s[10:11]
	v_fma_f32 v39, v57, v2, v6
	v_mul_f32_e32 v40, s26, v39
	v_cmp_le_f32_e64 s[10:11], 0, v39
	v_cvt_f16_f32_e32 v38, v38
	v_cndmask_b32_e64 v38, v38, 0, s[8:9]
	v_cndmask_b32_e64 v39, v40, v39, s[10:11]
	v_fma_f32 v40, v57, v3, v7
	v_mul_f32_e32 v41, s26, v40
	v_cmp_le_f32_e64 s[10:11], 0, v40
	v_cvt_f16_f32_e32 v39, v39
	v_cndmask_b32_e64 v39, v39, 0, s[8:9]
	v_cndmask_b32_e64 v40, v41, v40, s[10:11]
	v_fma_f32 v41, v57, v4, v8
	v_mul_f32_e32 v42, s26, v41
	v_cmp_le_f32_e64 s[10:11], 0, v41
	v_cvt_f16_f32_e32 v40, v40
	v_cndmask_b32_e64 v40, v40, 0, s[8:9]
	v_cndmask_b32_e64 v41, v42, v41, s[10:11]
	v_fma_f32 v42, v57, v5, v9
	v_mul_f32_e32 v43, s26, v42
	v_cmp_le_f32_e64 s[10:11], 0, v42
	v_cvt_f16_f32_e32 v41, v41
	v_pack_b32_f16 v40, v39, v40
	v_cndmask_b32_e64 v42, v43, v42, s[10:11]
	v_cvt_f16_f32_e32 v42, v42
	v_pack_b32_f16 v39, v37, v38
	v_pack_b32_f16 v38, v22, v23
	v_bitop3_b32 v22, v35, v1, 6 bitop3:0x6c
	v_cndmask_b32_e64 v41, v41, 0, s[8:9]
	v_cndmask_b32_e64 v42, v42, 0, s[8:9]
	v_lshlrev_b32_e32 v22, 4, v22
	v_pack_b32_f16 v41, v41, v42
	v_lshl_or_b32 v22, v35, 7, v22
	ds_write_b128 v22, v[38:41]
	v_fma_f32 v22, v36, v10, v14
	v_mul_f32_e32 v23, s26, v22
	v_cmp_le_f32_e64 s[8:9], 0, v22
	s_nop 1
	v_cndmask_b32_e64 v22, v23, v22, s[8:9]
	v_fma_f32 v23, v36, v11, v15
	v_mul_f32_e32 v35, s26, v23
	v_cmp_le_f32_e64 s[8:9], 0, v23
	v_cvt_f16_f32_e32 v22, v22
	v_cndmask_b32_e64 v22, v22, 0, s[6:7]
	v_cndmask_b32_e64 v23, v35, v23, s[8:9]
	v_fma_f32 v35, v36, v12, v16
	v_mul_f32_e32 v37, s26, v35
	v_cmp_le_f32_e64 s[8:9], 0, v35
	v_cvt_f16_f32_e32 v23, v23
	v_cndmask_b32_e64 v23, v23, 0, s[6:7]
	v_cndmask_b32_e64 v35, v37, v35, s[8:9]
	v_fma_f32 v37, v36, v13, v17
	v_mul_f32_e32 v38, s26, v37
	v_cmp_le_f32_e64 s[8:9], 0, v37
	v_cvt_f16_f32_e32 v35, v35
	v_cndmask_b32_e64 v35, v35, 0, s[6:7]
	v_cndmask_b32_e64 v37, v38, v37, s[8:9]
	v_fma_f32 v38, v36, v2, v6
	v_mul_f32_e32 v39, s26, v38
	v_cmp_le_f32_e64 s[8:9], 0, v38
	v_cvt_f16_f32_e32 v37, v37
	v_cndmask_b32_e64 v37, v37, 0, s[6:7]
	v_cndmask_b32_e64 v38, v39, v38, s[8:9]
	v_fma_f32 v39, v36, v3, v7
	v_mul_f32_e32 v40, s26, v39
	v_cmp_le_f32_e64 s[8:9], 0, v39
	v_cvt_f16_f32_e32 v38, v38
	v_pack_b32_f16 v37, v35, v37
	v_cndmask_b32_e64 v39, v40, v39, s[8:9]
	v_fma_f32 v40, v36, v4, v8
	v_mul_f32_e32 v41, s26, v40
	v_cmp_le_f32_e64 s[8:9], 0, v40
	v_fma_f32 v36, v36, v5, v9
	v_cvt_f16_f32_e32 v39, v39
	v_cndmask_b32_e64 v40, v41, v40, s[8:9]
	v_mul_f32_e32 v41, s26, v36
	v_cmp_le_f32_e64 s[8:9], 0, v36
	v_cvt_f16_f32_e32 v40, v40
	v_cndmask_b32_e64 v38, v38, 0, s[6:7]
	v_cndmask_b32_e64 v36, v41, v36, s[8:9]
	v_cvt_f16_f32_e32 v36, v36
	v_cndmask_b32_e64 v41, v39, 0, s[6:7]
	v_cndmask_b32_e64 v39, v40, 0, s[6:7]
	v_pack_b32_f16 v38, v38, v41
	v_cndmask_b32_e64 v36, v36, 0, s[6:7]
	v_pack_b32_f16 v39, v39, v36
	v_pack_b32_f16 v36, v22, v23
	v_bitop3_b32 v22, v33, v1, 6 bitop3:0x6c
	v_lshlrev_b32_e32 v22, 4, v22
	v_fma_f32 v23, v34, v10, v14
	v_lshl_or_b32 v22, v33, 7, v22
	v_mul_f32_e32 v33, s26, v23
	v_cmp_le_f32_e64 s[6:7], 0, v23
	ds_write_b128 v22, v[36:39]
	v_bitop3_b32 v22, v32, 64, v30 bitop3:0xc8
	v_cndmask_b32_e64 v23, v33, v23, s[6:7]
	v_fma_f32 v33, v34, v11, v15
	v_mul_f32_e32 v35, s26, v33
	v_cmp_le_f32_e64 s[6:7], 0, v33
	v_cvt_f16_f32_e32 v23, v23
	s_nop 0
	v_cndmask_b32_e64 v33, v35, v33, s[6:7]
	v_fma_f32 v35, v34, v12, v16
	v_mul_f32_e32 v36, s26, v35
	v_cmp_le_f32_e64 s[6:7], 0, v35
	v_cvt_f16_f32_e32 v33, v33
	s_nop 0
	v_cndmask_b32_e64 v35, v36, v35, s[6:7]
	v_fma_f32 v36, v34, v13, v17
	v_mul_f32_e32 v37, s26, v36
	v_cmp_le_f32_e64 s[6:7], 0, v36
	v_cvt_f16_f32_e32 v35, v35
	s_nop 0
	v_cndmask_b32_e64 v36, v37, v36, s[6:7]
	v_cvt_f16_f32_e32 v36, v36
	v_cmp_eq_u32_e64 s[6:7], 0, v22
	s_nop 1
	v_cndmask_b32_e64 v22, v23, 0, s[6:7]
	v_cndmask_b32_e64 v23, v33, 0, s[6:7]
	v_cndmask_b32_e64 v33, v35, 0, s[6:7]
	v_cndmask_b32_e64 v35, v36, 0, s[6:7]
	v_fma_f32 v36, v34, v2, v6
	v_mul_f32_e32 v37, s26, v36
	v_cmp_le_f32_e64 s[8:9], 0, v36
	v_pack_b32_f16 v35, v33, v35
	s_nop 0
	v_cndmask_b32_e64 v36, v37, v36, s[8:9]
	v_fma_f32 v37, v34, v3, v7
	v_mul_f32_e32 v38, s26, v37
	v_cmp_le_f32_e64 s[8:9], 0, v37
	v_cvt_f16_f32_e32 v36, v36
	v_cndmask_b32_e64 v36, v36, 0, s[6:7]
	v_cndmask_b32_e64 v37, v38, v37, s[8:9]
	v_fma_f32 v38, v34, v4, v8
	v_mul_f32_e32 v39, s26, v38
	v_cmp_le_f32_e64 s[8:9], 0, v38
	v_fma_f32 v34, v34, v5, v9
	v_cvt_f16_f32_e32 v37, v37
	v_cndmask_b32_e64 v38, v39, v38, s[8:9]
	v_mul_f32_e32 v39, s26, v34
	v_cmp_le_f32_e64 s[8:9], 0, v34
	v_cvt_f16_f32_e32 v38, v38
	s_nop 0
	v_cndmask_b32_e64 v34, v39, v34, s[8:9]
	v_cvt_f16_f32_e32 v34, v34
	v_cndmask_b32_e64 v39, v37, 0, s[6:7]
	v_cndmask_b32_e64 v37, v38, 0, s[6:7]
	v_pack_b32_f16 v36, v36, v39
	v_cndmask_b32_e64 v34, v34, 0, s[6:7]
	v_pack_b32_f16 v37, v37, v34
	v_pack_b32_f16 v34, v22, v23
	v_bitop3_b32 v22, v31, v1, 6 bitop3:0x6c
	v_lshlrev_b32_e32 v22, 4, v22
	v_lshl_or_b32 v22, v31, 7, v22
	v_fma_f32 v23, v29, v10, v14
	ds_write_b128 v22, v[34:37]
	v_bitop3_b32 v22, v32, s29, v30 bitop3:0xc8
	v_mul_f32_e32 v30, s26, v23
	v_cmp_le_f32_e64 s[6:7], 0, v23
	s_nop 1
	v_cndmask_b32_e64 v23, v30, v23, s[6:7]
	v_fma_f32 v30, v29, v11, v15
	v_mul_f32_e32 v31, s26, v30
	v_cmp_le_f32_e64 s[6:7], 0, v30
	v_cvt_f16_f32_e32 v23, v23
	s_nop 0
	v_cndmask_b32_e64 v30, v31, v30, s[6:7]
	v_fma_f32 v31, v29, v12, v16
	v_mul_f32_e32 v32, s26, v31
	v_cmp_le_f32_e64 s[6:7], 0, v31
	v_cvt_f16_f32_e32 v30, v30
	s_nop 0
	v_cndmask_b32_e64 v31, v32, v31, s[6:7]
	v_fma_f32 v32, v29, v13, v17
	v_mul_f32_e32 v33, s26, v32
	v_cmp_le_f32_e64 s[6:7], 0, v32
	v_cvt_f16_f32_e32 v31, v31
	s_nop 0
	v_cndmask_b32_e64 v32, v33, v32, s[6:7]
	v_cvt_f16_f32_e32 v32, v32
	v_cmp_eq_u32_e64 s[6:7], 0, v22
	s_nop 1
	v_cndmask_b32_e64 v22, v23, 0, s[6:7]
	v_cndmask_b32_e64 v23, v30, 0, s[6:7]
	v_cndmask_b32_e64 v30, v31, 0, s[6:7]
	v_cndmask_b32_e64 v31, v32, 0, s[6:7]
	v_fma_f32 v32, v29, v2, v6
	v_mul_f32_e32 v33, s26, v32
	v_cmp_le_f32_e64 s[8:9], 0, v32
	v_pack_b32_f16 v31, v30, v31
	v_pack_b32_f16 v30, v22, v23
	v_cndmask_b32_e64 v32, v33, v32, s[8:9]
	v_fma_f32 v33, v29, v3, v7
	v_mul_f32_e32 v34, s26, v33
	v_cmp_le_f32_e64 s[8:9], 0, v33
	v_cvt_f16_f32_e32 v32, v32
	v_bitop3_b32 v22, v26, v1, 6 bitop3:0x6c
	v_cndmask_b32_e64 v33, v34, v33, s[8:9]
	v_fma_f32 v34, v29, v4, v8
	v_mul_f32_e32 v35, s26, v34
	v_cmp_le_f32_e64 s[8:9], 0, v34
	v_fma_f32 v29, v29, v5, v9
	v_cvt_f16_f32_e32 v33, v33
	v_cndmask_b32_e64 v34, v35, v34, s[8:9]
	v_mul_f32_e32 v35, s26, v29
	v_cmp_le_f32_e64 s[8:9], 0, v29
	v_cvt_f16_f32_e32 v34, v34
	v_cndmask_b32_e64 v32, v32, 0, s[6:7]
	v_cndmask_b32_e64 v29, v35, v29, s[8:9]
	v_cvt_f16_f32_e32 v29, v29
	v_cndmask_b32_e64 v35, v33, 0, s[6:7]
	v_cndmask_b32_e64 v33, v34, 0, s[6:7]
	v_lshlrev_b32_e32 v22, 4, v22
	v_cndmask_b32_e64 v29, v29, 0, s[6:7]
	v_pack_b32_f16 v33, v33, v29
	v_pack_b32_f16 v32, v32, v35
	v_lshl_or_b32 v22, v26, 7, v22
	ds_write_b128 v22, v[30:33]
	s_and_saveexec_b64 s[6:7], s[4:5]
	s_cbranch_execz .LBB3_2
	v_cndmask_b32_e64 v22, 0, v28, s[18:19]
	v_or_b32_e32 v22, s28, v22
	v_cndmask_b32_e64 v23, 0, v27, s[18:19]
	v_lshl_add_u32 v22, v22, 6, v23
	v_ashrrev_i32_e32 v23, 31, v22
	v_lshl_add_u64 v[22:23], v[22:23], 2, s[24:25]
	global_load_dword v22, v[22:23], off
	v_bitop3_b32 v26, v24, v1, 6 bitop3:0x6c
	v_lshlrev_b32_e32 v30, 4, v26
	v_and_b32_e32 v23, 0x100, v25
	s_waitcnt vmcnt(0)
	v_fma_f32 v26, v22, v10, v14
	v_fma_f32 v27, v22, v11, v15
	v_mul_f32_e32 v34, s26, v26
	v_cmp_le_f32_e64 s[4:5], 0, v26
	v_fma_f32 v28, v22, v12, v16
	v_mul_f32_e32 v35, s26, v27
	v_cndmask_b32_e64 v26, v34, v26, s[4:5]
	v_cmp_le_f32_e64 s[4:5], 0, v27
	v_fma_f32 v29, v22, v13, v17
	v_mul_f32_e32 v36, s26, v28
	v_cndmask_b32_e64 v27, v35, v27, s[4:5]
	v_cmp_le_f32_e64 s[4:5], 0, v28
	v_fma_f32 v31, v22, v2, v6
	v_mul_f32_e32 v37, s26, v29
	v_cndmask_b32_e64 v28, v36, v28, s[4:5]
	v_cmp_le_f32_e64 s[4:5], 0, v29
	v_fma_f32 v32, v22, v3, v7
	v_mul_f32_e32 v38, s26, v31
	v_cndmask_b32_e64 v29, v37, v29, s[4:5]
	v_cmp_le_f32_e64 s[4:5], 0, v31
	v_fma_f32 v33, v22, v4, v8
	v_mul_f32_e32 v39, s26, v32
	v_cndmask_b32_e64 v31, v38, v31, s[4:5]
	v_cmp_le_f32_e64 s[4:5], 0, v32
	v_fma_f32 v22, v22, v5, v9
	v_mul_f32_e32 v40, s26, v33
	v_cndmask_b32_e64 v32, v39, v32, s[4:5]
	v_cmp_le_f32_e64 s[4:5], 0, v33
	v_mul_f32_e32 v41, s26, v22
	v_cvt_f16_f32_e32 v26, v26
	v_cndmask_b32_e64 v33, v40, v33, s[4:5]
	v_cmp_le_f32_e64 s[4:5], 0, v22
	v_cvt_f16_f32_e32 v27, v27
	v_cvt_f16_f32_e32 v28, v28
	v_cndmask_b32_e64 v22, v41, v22, s[4:5]
	v_cvt_f16_f32_e32 v29, v29
	v_cvt_f16_f32_e32 v31, v31
	v_cvt_f16_f32_e32 v32, v32
	v_cvt_f16_f32_e32 v33, v33
	v_cvt_f16_f32_e32 v22, v22
	v_cmp_eq_u32_e64 s[4:5], 0, v23
	s_nop 1
	v_cndmask_b32_e64 v23, v26, 0, s[4:5]
	v_cndmask_b32_e64 v26, v27, 0, s[4:5]
	v_cndmask_b32_e64 v27, v28, 0, s[4:5]
	v_cndmask_b32_e64 v34, v29, 0, s[4:5]
	v_cndmask_b32_e64 v28, v31, 0, s[4:5]
	v_cndmask_b32_e64 v31, v32, 0, s[4:5]
	v_cndmask_b32_e64 v29, v33, 0, s[4:5]
	v_cndmask_b32_e64 v22, v22, 0, s[4:5]
	v_pack_b32_f16 v29, v29, v22
	v_pack_b32_f16 v28, v28, v31
	v_pack_b32_f16 v27, v27, v34
	v_pack_b32_f16 v26, v23, v26
	v_lshl_or_b32 v22, v24, 7, v30
	ds_write_b128 v22, v[26:29]

.Lc1_loop:
	s_waitcnt vmcnt(2)
	s_barrier
	s_waitcnt lgkmcnt(3)
	v_mfma_f32_16x16x32_f16 v[92:95], v[40:43], v[56:59], v[92:95]
	ds_read_b128 v[116:119], v115
	v_mfma_f32_16x16x32_f16 v[88:91], v[48:51], v[56:59], v[88:91]
	v_xor_b32_e32 v153, 64, v114
	s_add_i32 s4, s45, 60
	s_add_i32 s4, s4, s12
	s_lshl_b32 s4, s4, 14
	s_waitcnt lgkmcnt(3)
	v_mfma_f32_16x16x32_f16 v[60:63], v[40:43], v[52:55], v[60:63]
	ds_read_b128 v[120:123], v115 offset:2048
	v_lshl_add_u64 v[148:149], v[100:101], 0, s[4:5]
	s_and_b32 s42, s13, 0xc000
	s_add_i32 s42, s42, s27
	v_mfma_f32_16x16x32_f16 v[44:47], v[48:51], v[52:55], v[44:47]
	v_xor_b32_e32 v152, 64, v113
	s_mov_b32 m0, s42
	s_add_i32 s16, s13, 0xffff8000
	global_load_lds_dwordx4 v[148:149], off
	v_mfma_f32_16x16x32_f16 v[28:31], v[40:43], v[64:67], v[28:31]
	ds_read_b128 v[132:135], v153
	v_mfma_f32_16x16x32_f16 v[24:27], v[48:51], v[64:67], v[24:27]
	s_and_b32 s16, s16, 0xc000
	s_add_i32 s43, s42, 0x400
	v_lshl_add_u64 v[150:151], v[148:149], 0, s[8:9]
	v_mfma_f32_16x16x32_f16 v[12:15], v[40:43], v[68:71], v[12:15]
	ds_read_b128 v[136:139], v153 offset:2048
	v_mfma_f32_16x16x32_f16 v[8:11], v[48:51], v[68:71], v[8:11]
	v_add_u32_e32 v154, s16, v110
	s_add_i32 s44, s45, 102
	s_waitcnt lgkmcnt(5)
	v_mfma_f32_16x16x32_f16 v[84:87], v[76:79], v[56:59], v[84:87]
	ds_read_b128 v[124:127], v152
	s_waitcnt lgkmcnt(5)
	v_mfma_f32_16x16x32_f16 v[72:75], v[80:83], v[56:59], v[72:75]
	v_mfma_f32_16x16x32_f16 v[36:39], v[76:79], v[52:55], v[36:39]
	ds_read_b128 v[128:131], v152 offset:2048
	v_mfma_f32_16x16x32_f16 v[32:35], v[80:83], v[52:55], v[32:35]
	v_add_u32_e32 v155, s44, v98
	v_mfma_f32_16x16x32_f16 v[20:23], v[76:79], v[64:67], v[20:23]
	ds_read_b128 v[140:143], v115 offset:4096
	v_mfma_f32_16x16x32_f16 v[16:19], v[80:83], v[64:67], v[16:19]
	v_lshlrev_b32_e32 v156, 7, v155
	v_bitop3_b32 v155, v155, v99, 6 bitop3:0x6c
	v_mfma_f32_16x16x32_f16 v[4:7], v[76:79], v[68:71], v[4:7]
	ds_read_b128 v[144:147], v115 offset:6144
	v_mfma_f32_16x16x32_f16 v[0:3], v[80:83], v[68:71], v[0:3]
	v_lshl_or_b32 v114, v155, 4, v156
	v_add_u32_e32 v115, s16, v111
	s_waitcnt lgkmcnt(3)
	v_mfma_f32_16x16x32_f16 v[92:95], v[116:119], v[124:127], v[92:95]
	ds_read_b128 v[40:43], v154
	v_mfma_f32_16x16x32_f16 v[88:91], v[120:123], v[124:127], v[88:91]
	s_mov_b32 m0, s43
	s_addk_i32 s13, 0x4000
	global_load_lds_dwordx4 v[150:151], off
	s_waitcnt lgkmcnt(3)
	v_mfma_f32_16x16x32_f16 v[60:63], v[116:119], v[128:131], v[60:63]
	ds_read_b128 v[48:51], v154 offset:2048
	v_mfma_f32_16x16x32_f16 v[44:47], v[120:123], v[128:131], v[44:47]
	v_mfma_f32_16x16x32_f16 v[28:31], v[116:119], v[132:135], v[28:31]
	ds_read_b128 v[56:59], v114
	v_mfma_f32_16x16x32_f16 v[24:27], v[120:123], v[132:135], v[24:27]
	v_mfma_f32_16x16x32_f16 v[12:15], v[116:119], v[136:139], v[12:15]
	ds_read_b128 v[52:55], v114 offset:2048
	v_mfma_f32_16x16x32_f16 v[8:11], v[120:123], v[136:139], v[8:11]
	s_waitcnt lgkmcnt(5)
	v_mfma_f32_16x16x32_f16 v[84:87], v[140:143], v[124:127], v[84:87]
	s_waitcnt lgkmcnt(4)
	v_mfma_f32_16x16x32_f16 v[72:75], v[144:147], v[124:127], v[72:75]
	v_mfma_f32_16x16x32_f16 v[36:39], v[140:143], v[128:131], v[36:39]
	v_mfma_f32_16x16x32_f16 v[32:35], v[144:147], v[128:131], v[32:35]
	v_mfma_f32_16x16x32_f16 v[20:23], v[140:143], v[132:135], v[20:23]
	ds_read_b128 v[76:79], v154 offset:4096
	v_mfma_f32_16x16x32_f16 v[16:19], v[144:147], v[132:135], v[16:19]
	v_mfma_f32_16x16x32_f16 v[4:7], v[140:143], v[136:139], v[4:7]
	ds_read_b128 v[80:83], v154 offset:6144
	v_mfma_f32_16x16x32_f16 v[0:3], v[144:147], v[136:139], v[0:3]
	s_waitcnt vmcnt(2)
	s_barrier
	s_waitcnt lgkmcnt(5)
	v_mfma_f32_16x16x32_f16 v[92:95], v[40:43], v[64:67], v[92:95]
	ds_read_b128 v[116:119], v115
	s_waitcnt lgkmcnt(5)
	v_mfma_f32_16x16x32_f16 v[88:91], v[48:51], v[64:67], v[88:91]
	v_xor_b32_e32 v153, 64, v114
	s_add_i32 s4, s45, 80
	s_add_i32 s4, s4, s12
	s_lshl_b32 s4, s4, 14
	v_mfma_f32_16x16x32_f16 v[60:63], v[40:43], v[68:71], v[60:63]
	ds_read_b128 v[120:123], v115 offset:2048
	v_lshl_add_u64 v[148:149], v[100:101], 0, s[4:5]
	s_and_b32 s42, s13, 0xc000
	s_add_i32 s42, s42, s27
	v_mfma_f32_16x16x32_f16 v[44:47], v[48:51], v[68:71], v[44:47]
	s_mov_b32 m0, s42
	s_add_i32 s16, s13, 0xffff8000
	global_load_lds_dwordx4 v[148:149], off
	s_waitcnt lgkmcnt(5)
	v_mfma_f32_16x16x32_f16 v[28:31], v[40:43], v[56:59], v[28:31]
	ds_read_b128 v[124:127], v153
	v_mfma_f32_16x16x32_f16 v[24:27], v[48:51], v[56:59], v[24:27]
	s_and_b32 s16, s16, 0xc000
	s_add_i32 s43, s42, 0x400
	v_lshl_add_u64 v[150:151], v[148:149], 0, s[8:9]
	s_waitcnt lgkmcnt(5)
	v_mfma_f32_16x16x32_f16 v[12:15], v[40:43], v[52:55], v[12:15]
	ds_read_b128 v[128:131], v153 offset:2048
	v_mfma_f32_16x16x32_f16 v[8:11], v[48:51], v[52:55], v[8:11]
	v_add_u32_e32 v154, s16, v110
	s_add_i32 s44, s45, 153
	s_waitcnt lgkmcnt(5)
	v_mfma_f32_16x16x32_f16 v[84:87], v[76:79], v[64:67], v[84:87]
	s_waitcnt lgkmcnt(4)
	v_mfma_f32_16x16x32_f16 v[72:75], v[80:83], v[64:67], v[72:75]
	v_mfma_f32_16x16x32_f16 v[36:39], v[76:79], v[68:71], v[36:39]
	v_mfma_f32_16x16x32_f16 v[32:35], v[80:83], v[68:71], v[32:35]
	v_add_u32_e32 v155, s44, v98
	v_mfma_f32_16x16x32_f16 v[20:23], v[76:79], v[56:59], v[20:23]
	ds_read_b128 v[140:143], v115 offset:4096
	v_mfma_f32_16x16x32_f16 v[16:19], v[80:83], v[56:59], v[16:19]
	v_lshlrev_b32_e32 v156, 7, v155
	v_bitop3_b32 v155, v155, v99, 6 bitop3:0x6c
	v_mfma_f32_16x16x32_f16 v[4:7], v[76:79], v[52:55], v[4:7]
	ds_read_b128 v[144:147], v115 offset:6144
	v_mfma_f32_16x16x32_f16 v[0:3], v[80:83], v[52:55], v[0:3]
	v_lshl_or_b32 v114, v155, 4, v156
	v_add_u32_e32 v115, s16, v111
	s_waitcnt lgkmcnt(5)
	v_mfma_f32_16x16x32_f16 v[92:95], v[116:119], v[132:135], v[92:95]
	ds_read_b128 v[40:43], v154
	s_waitcnt lgkmcnt(5)
	v_mfma_f32_16x16x32_f16 v[88:91], v[120:123], v[132:135], v[88:91]
	s_mov_b32 m0, s43
	s_addk_i32 s13, 0x4000
	global_load_lds_dwordx4 v[150:151], off
	v_mfma_f32_16x16x32_f16 v[60:63], v[116:119], v[136:139], v[60:63]
	ds_read_b128 v[48:51], v154 offset:2048
	v_mfma_f32_16x16x32_f16 v[44:47], v[120:123], v[136:139], v[44:47]
	s_waitcnt lgkmcnt(5)
	v_mfma_f32_16x16x32_f16 v[28:31], v[116:119], v[124:127], v[28:31]
	ds_read_b128 v[64:67], v114
	v_mfma_f32_16x16x32_f16 v[24:27], v[120:123], v[124:127], v[24:27]
	s_waitcnt lgkmcnt(5)
	v_mfma_f32_16x16x32_f16 v[12:15], v[116:119], v[128:131], v[12:15]
	ds_read_b128 v[68:71], v114 offset:2048
	v_mfma_f32_16x16x32_f16 v[8:11], v[120:123], v[128:131], v[8:11]
	s_waitcnt lgkmcnt(5)
	v_mfma_f32_16x16x32_f16 v[84:87], v[140:143], v[132:135], v[84:87]
	s_waitcnt lgkmcnt(4)
	v_mfma_f32_16x16x32_f16 v[72:75], v[144:147], v[132:135], v[72:75]
	v_mfma_f32_16x16x32_f16 v[36:39], v[140:143], v[136:139], v[36:39]
	v_mfma_f32_16x16x32_f16 v[32:35], v[144:147], v[136:139], v[32:35]
	v_mfma_f32_16x16x32_f16 v[20:23], v[140:143], v[124:127], v[20:23]
	ds_read_b128 v[76:79], v154 offset:4096
	v_mfma_f32_16x16x32_f16 v[16:19], v[144:147], v[124:127], v[16:19]
	v_mfma_f32_16x16x32_f16 v[4:7], v[140:143], v[128:131], v[4:7]
	ds_read_b128 v[80:83], v154 offset:6144
	v_mfma_f32_16x16x32_f16 v[0:3], v[144:147], v[128:131], v[0:3]
	s_waitcnt vmcnt(2)
	s_barrier
	s_waitcnt lgkmcnt(5)
	v_mfma_f32_16x16x32_f16 v[92:95], v[40:43], v[56:59], v[92:95]
	ds_read_b128 v[116:119], v115
	s_waitcnt lgkmcnt(5)
	v_mfma_f32_16x16x32_f16 v[88:91], v[48:51], v[56:59], v[88:91]
	v_xor_b32_e32 v153, 64, v114
	s_add_i32 s4, s45, 1
	s_add_i32 s4, s4, s12
	s_lshl_b32 s4, s4, 14
	v_mfma_f32_16x16x32_f16 v[60:63], v[40:43], v[52:55], v[60:63]
	ds_read_b128 v[120:123], v115 offset:2048
	v_lshl_add_u64 v[148:149], v[100:101], 0, s[4:5]
	s_and_b32 s42, s13, 0xc000
	s_add_i32 s42, s42, s27
	v_mfma_f32_16x16x32_f16 v[44:47], v[48:51], v[52:55], v[44:47]
	s_mov_b32 m0, s42
	s_add_i32 s16, s13, 0xffff8000
	global_load_lds_dwordx4 v[148:149], off
	s_waitcnt lgkmcnt(5)
	v_mfma_f32_16x16x32_f16 v[28:31], v[40:43], v[64:67], v[28:31]
	ds_read_b128 v[132:135], v153
	v_mfma_f32_16x16x32_f16 v[24:27], v[48:51], v[64:67], v[24:27]
	s_and_b32 s16, s16, 0xc000
	s_add_i32 s43, s42, 0x400
	v_lshl_add_u64 v[150:151], v[148:149], 0, s[8:9]
	s_waitcnt lgkmcnt(5)
	v_mfma_f32_16x16x32_f16 v[12:15], v[40:43], v[68:71], v[12:15]
	ds_read_b128 v[136:139], v153 offset:2048
	v_mfma_f32_16x16x32_f16 v[8:11], v[48:51], v[68:71], v[8:11]
	v_add_u32_e32 v154, s16, v110
	s_add_i32 s44, s45, 204
	s_waitcnt lgkmcnt(5)
	v_mfma_f32_16x16x32_f16 v[84:87], v[76:79], v[56:59], v[84:87]
	s_waitcnt lgkmcnt(4)
	v_mfma_f32_16x16x32_f16 v[72:75], v[80:83], v[56:59], v[72:75]
	v_mfma_f32_16x16x32_f16 v[36:39], v[76:79], v[52:55], v[36:39]
	v_mfma_f32_16x16x32_f16 v[32:35], v[80:83], v[52:55], v[32:35]
	v_add_u32_e32 v155, s44, v98
	v_mfma_f32_16x16x32_f16 v[20:23], v[76:79], v[64:67], v[20:23]
	ds_read_b128 v[140:143], v115 offset:4096
	v_mfma_f32_16x16x32_f16 v[16:19], v[80:83], v[64:67], v[16:19]
	v_lshlrev_b32_e32 v156, 7, v155
	v_bitop3_b32 v155, v155, v99, 6 bitop3:0x6c
	v_mfma_f32_16x16x32_f16 v[4:7], v[76:79], v[68:71], v[4:7]
	ds_read_b128 v[144:147], v115 offset:6144
	v_mfma_f32_16x16x32_f16 v[0:3], v[80:83], v[68:71], v[0:3]
	v_lshl_or_b32 v114, v155, 4, v156
	v_add_u32_e32 v115, s16, v111
	s_waitcnt lgkmcnt(5)
	v_mfma_f32_16x16x32_f16 v[92:95], v[116:119], v[124:127], v[92:95]
	ds_read_b128 v[40:43], v154
	s_waitcnt lgkmcnt(5)
	v_mfma_f32_16x16x32_f16 v[88:91], v[120:123], v[124:127], v[88:91]
	s_mov_b32 m0, s43
	s_addk_i32 s13, 0x4000
	global_load_lds_dwordx4 v[150:151], off
	v_mfma_f32_16x16x32_f16 v[60:63], v[116:119], v[128:131], v[60:63]
	ds_read_b128 v[48:51], v154 offset:2048
	v_mfma_f32_16x16x32_f16 v[44:47], v[120:123], v[128:131], v[44:47]
	s_waitcnt lgkmcnt(5)
	v_mfma_f32_16x16x32_f16 v[28:31], v[116:119], v[132:135], v[28:31]
	ds_read_b128 v[56:59], v114
	v_mfma_f32_16x16x32_f16 v[24:27], v[120:123], v[132:135], v[24:27]
	s_waitcnt lgkmcnt(5)
	v_mfma_f32_16x16x32_f16 v[12:15], v[116:119], v[136:139], v[12:15]
	ds_read_b128 v[52:55], v114 offset:2048
	v_mfma_f32_16x16x32_f16 v[8:11], v[120:123], v[136:139], v[8:11]
	s_waitcnt lgkmcnt(5)
	v_mfma_f32_16x16x32_f16 v[84:87], v[140:143], v[124:127], v[84:87]
	s_waitcnt lgkmcnt(4)
	v_mfma_f32_16x16x32_f16 v[72:75], v[144:147], v[124:127], v[72:75]
	v_mfma_f32_16x16x32_f16 v[36:39], v[140:143], v[128:131], v[36:39]
	v_mfma_f32_16x16x32_f16 v[32:35], v[144:147], v[128:131], v[32:35]
	v_mfma_f32_16x16x32_f16 v[20:23], v[140:143], v[132:135], v[20:23]
	ds_read_b128 v[76:79], v154 offset:4096
	v_mfma_f32_16x16x32_f16 v[16:19], v[144:147], v[132:135], v[16:19]
	v_mfma_f32_16x16x32_f16 v[4:7], v[140:143], v[136:139], v[4:7]
	ds_read_b128 v[80:83], v154 offset:6144
	v_mfma_f32_16x16x32_f16 v[0:3], v[144:147], v[136:139], v[0:3]
	s_waitcnt vmcnt(2)
	s_barrier
	s_waitcnt lgkmcnt(5)
	v_mfma_f32_16x16x32_f16 v[92:95], v[40:43], v[64:67], v[92:95]
	ds_read_b128 v[116:119], v115
	s_waitcnt lgkmcnt(5)
	v_mfma_f32_16x16x32_f16 v[88:91], v[48:51], v[64:67], v[88:91]
	v_xor_b32_e32 v153, 64, v114
	s_add_i32 s4, s45, 21
	s_add_i32 s4, s4, s12
	s_lshl_b32 s4, s4, 14
	v_mfma_f32_16x16x32_f16 v[60:63], v[40:43], v[68:71], v[60:63]
	ds_read_b128 v[120:123], v115 offset:2048
	v_lshl_add_u64 v[148:149], v[100:101], 0, s[4:5]
	s_and_b32 s42, s13, 0xc000
	s_add_i32 s42, s42, s27
	v_mfma_f32_16x16x32_f16 v[44:47], v[48:51], v[68:71], v[44:47]
	s_mov_b32 m0, s42
	s_add_i32 s16, s13, 0xffff8000
	global_load_lds_dwordx4 v[148:149], off
	s_waitcnt lgkmcnt(5)
	v_mfma_f32_16x16x32_f16 v[28:31], v[40:43], v[56:59], v[28:31]
	ds_read_b128 v[124:127], v153
	v_mfma_f32_16x16x32_f16 v[24:27], v[48:51], v[56:59], v[24:27]
	s_and_b32 s16, s16, 0xc000
	s_add_i32 s43, s42, 0x400
	v_lshl_add_u64 v[150:151], v[148:149], 0, s[8:9]
	s_waitcnt lgkmcnt(5)
	v_mfma_f32_16x16x32_f16 v[12:15], v[40:43], v[52:55], v[12:15]
	ds_read_b128 v[128:131], v153 offset:2048
	v_mfma_f32_16x16x32_f16 v[8:11], v[48:51], v[52:55], v[8:11]
	v_add_u32_e32 v154, s16, v110
	s_add_i32 s44, s45, 255
	s_waitcnt lgkmcnt(5)
	v_mfma_f32_16x16x32_f16 v[84:87], v[76:79], v[64:67], v[84:87]
	s_waitcnt lgkmcnt(4)
	v_mfma_f32_16x16x32_f16 v[72:75], v[80:83], v[64:67], v[72:75]
	v_mfma_f32_16x16x32_f16 v[36:39], v[76:79], v[68:71], v[36:39]
	v_mfma_f32_16x16x32_f16 v[32:35], v[80:83], v[68:71], v[32:35]
	v_add_u32_e32 v155, s44, v98
	v_mfma_f32_16x16x32_f16 v[20:23], v[76:79], v[56:59], v[20:23]
	ds_read_b128 v[140:143], v115 offset:4096
	v_mfma_f32_16x16x32_f16 v[16:19], v[80:83], v[56:59], v[16:19]
	v_lshlrev_b32_e32 v156, 7, v155
	v_bitop3_b32 v155, v155, v99, 6 bitop3:0x6c
	v_mfma_f32_16x16x32_f16 v[4:7], v[76:79], v[52:55], v[4:7]
	ds_read_b128 v[144:147], v115 offset:6144
	v_mfma_f32_16x16x32_f16 v[0:3], v[80:83], v[52:55], v[0:3]
	v_lshl_or_b32 v114, v155, 4, v156
	v_add_u32_e32 v115, s16, v111
	s_waitcnt lgkmcnt(5)
	v_mfma_f32_16x16x32_f16 v[92:95], v[116:119], v[132:135], v[92:95]
	ds_read_b128 v[40:43], v154
	s_waitcnt lgkmcnt(5)
	v_mfma_f32_16x16x32_f16 v[88:91], v[120:123], v[132:135], v[88:91]
	s_mov_b32 m0, s43
	s_addk_i32 s13, 0x4000
	global_load_lds_dwordx4 v[150:151], off
	v_mfma_f32_16x16x32_f16 v[60:63], v[116:119], v[136:139], v[60:63]
	ds_read_b128 v[48:51], v154 offset:2048
	v_mfma_f32_16x16x32_f16 v[44:47], v[120:123], v[136:139], v[44:47]
	s_waitcnt lgkmcnt(5)
	v_mfma_f32_16x16x32_f16 v[28:31], v[116:119], v[124:127], v[28:31]
	ds_read_b128 v[64:67], v114
	v_mfma_f32_16x16x32_f16 v[24:27], v[120:123], v[124:127], v[24:27]
	s_waitcnt lgkmcnt(5)
	v_mfma_f32_16x16x32_f16 v[12:15], v[116:119], v[128:131], v[12:15]
	ds_read_b128 v[68:71], v114 offset:2048
	v_mfma_f32_16x16x32_f16 v[8:11], v[120:123], v[128:131], v[8:11]
	s_waitcnt lgkmcnt(5)
	v_mfma_f32_16x16x32_f16 v[84:87], v[140:143], v[132:135], v[84:87]
	s_waitcnt lgkmcnt(4)
	v_mfma_f32_16x16x32_f16 v[72:75], v[144:147], v[132:135], v[72:75]
	v_mfma_f32_16x16x32_f16 v[36:39], v[140:143], v[136:139], v[36:39]
	v_mfma_f32_16x16x32_f16 v[32:35], v[144:147], v[136:139], v[32:35]
	v_mfma_f32_16x16x32_f16 v[20:23], v[140:143], v[124:127], v[20:23]
	ds_read_b128 v[76:79], v154 offset:4096
	v_mfma_f32_16x16x32_f16 v[16:19], v[144:147], v[124:127], v[16:19]
	v_mfma_f32_16x16x32_f16 v[4:7], v[140:143], v[128:131], v[4:7]
	ds_read_b128 v[80:83], v154 offset:6144
	v_mfma_f32_16x16x32_f16 v[0:3], v[144:147], v[128:131], v[0:3]
	s_waitcnt vmcnt(2)
	s_barrier
	s_waitcnt lgkmcnt(5)
	v_mfma_f32_16x16x32_f16 v[92:95], v[40:43], v[56:59], v[92:95]
	ds_read_b128 v[116:119], v115
	s_waitcnt lgkmcnt(5)
	v_mfma_f32_16x16x32_f16 v[88:91], v[48:51], v[56:59], v[88:91]
	v_xor_b32_e32 v153, 64, v114
	s_add_i32 s4, s45, 41
	s_add_i32 s4, s4, s12
	s_lshl_b32 s4, s4, 14
	v_mfma_f32_16x16x32_f16 v[60:63], v[40:43], v[52:55], v[60:63]
	ds_read_b128 v[120:123], v115 offset:2048
	v_lshl_add_u64 v[148:149], v[100:101], 0, s[4:5]
	s_and_b32 s42, s13, 0xc000
	s_add_i32 s42, s42, s27
	v_mfma_f32_16x16x32_f16 v[44:47], v[48:51], v[52:55], v[44:47]
	s_mov_b32 m0, s42
	s_add_i32 s16, s13, 0xffff8000
	global_load_lds_dwordx4 v[148:149], off
	s_waitcnt lgkmcnt(5)
	v_mfma_f32_16x16x32_f16 v[28:31], v[40:43], v[64:67], v[28:31]
	ds_read_b128 v[132:135], v153
	v_mfma_f32_16x16x32_f16 v[24:27], v[48:51], v[64:67], v[24:27]
	s_and_b32 s16, s16, 0xc000
	s_add_i32 s43, s42, 0x400
	v_lshl_add_u64 v[150:151], v[148:149], 0, s[8:9]
	s_waitcnt lgkmcnt(5)
	v_mfma_f32_16x16x32_f16 v[12:15], v[40:43], v[68:71], v[12:15]
	ds_read_b128 v[136:139], v153 offset:2048
	v_mfma_f32_16x16x32_f16 v[8:11], v[48:51], v[68:71], v[8:11]
	v_add_u32_e32 v154, s16, v110
	s_add_i32 s44, s45, 52
	s_waitcnt lgkmcnt(5)
	v_mfma_f32_16x16x32_f16 v[84:87], v[76:79], v[56:59], v[84:87]
	s_waitcnt lgkmcnt(4)
	v_mfma_f32_16x16x32_f16 v[72:75], v[80:83], v[56:59], v[72:75]
	v_mfma_f32_16x16x32_f16 v[36:39], v[76:79], v[52:55], v[36:39]
	v_mfma_f32_16x16x32_f16 v[32:35], v[80:83], v[52:55], v[32:35]
	v_add_u32_e32 v155, s44, v98
	v_mfma_f32_16x16x32_f16 v[20:23], v[76:79], v[64:67], v[20:23]
	ds_read_b128 v[140:143], v115 offset:4096
	v_mfma_f32_16x16x32_f16 v[16:19], v[80:83], v[64:67], v[16:19]
	v_lshlrev_b32_e32 v156, 7, v155
	v_bitop3_b32 v155, v155, v99, 6 bitop3:0x6c
	v_mfma_f32_16x16x32_f16 v[4:7], v[76:79], v[68:71], v[4:7]
	ds_read_b128 v[144:147], v115 offset:6144
	v_mfma_f32_16x16x32_f16 v[0:3], v[80:83], v[68:71], v[0:3]
	v_lshl_or_b32 v114, v155, 4, v156
	v_add_u32_e32 v115, s16, v111
	s_waitcnt lgkmcnt(5)
	v_mfma_f32_16x16x32_f16 v[92:95], v[116:119], v[124:127], v[92:95]
	ds_read_b128 v[40:43], v154
	s_waitcnt lgkmcnt(5)
	v_mfma_f32_16x16x32_f16 v[88:91], v[120:123], v[124:127], v[88:91]
	s_mov_b32 m0, s43
	s_addk_i32 s13, 0x4000
	global_load_lds_dwordx4 v[150:151], off
	v_mfma_f32_16x16x32_f16 v[60:63], v[116:119], v[128:131], v[60:63]
	ds_read_b128 v[48:51], v154 offset:2048
	v_mfma_f32_16x16x32_f16 v[44:47], v[120:123], v[128:131], v[44:47]
	s_sub_i32 s44, s44, 51
	v_add_u32_e32 v155, s44, v98
	s_waitcnt lgkmcnt(5)
	v_mfma_f32_16x16x32_f16 v[28:31], v[116:119], v[132:135], v[28:31]
	ds_read_b128 v[56:59], v114
	v_mfma_f32_16x16x32_f16 v[24:27], v[120:123], v[132:135], v[24:27]
	v_lshlrev_b32_e32 v156, 7, v155
	v_bitop3_b32 v155, v155, v99, 6 bitop3:0x6c
	s_waitcnt lgkmcnt(5)
	v_mfma_f32_16x16x32_f16 v[12:15], v[116:119], v[136:139], v[12:15]
	ds_read_b128 v[52:55], v114 offset:2048
	v_mfma_f32_16x16x32_f16 v[8:11], v[120:123], v[136:139], v[8:11]
	v_lshl_or_b32 v113, v155, 4, v156
	s_waitcnt lgkmcnt(5)
	v_mfma_f32_16x16x32_f16 v[84:87], v[140:143], v[124:127], v[84:87]
	ds_read_b128 v[64:67], v113
	s_waitcnt lgkmcnt(5)
	v_mfma_f32_16x16x32_f16 v[72:75], v[144:147], v[124:127], v[72:75]
	v_mfma_f32_16x16x32_f16 v[36:39], v[140:143], v[128:131], v[36:39]
	ds_read_b128 v[68:71], v113 offset:2048
	v_mfma_f32_16x16x32_f16 v[32:35], v[144:147], v[128:131], v[32:35]
	v_mfma_f32_16x16x32_f16 v[20:23], v[140:143], v[132:135], v[20:23]
	ds_read_b128 v[76:79], v154 offset:4096
	v_mfma_f32_16x16x32_f16 v[16:19], v[144:147], v[132:135], v[16:19]
	v_mfma_f32_16x16x32_f16 v[4:7], v[140:143], v[136:139], v[4:7]
	ds_read_b128 v[80:83], v154 offset:6144
	v_mfma_f32_16x16x32_f16 v[0:3], v[144:147], v[136:139], v[0:3]
	s_waitcnt vmcnt(2)
	s_barrier
	s_waitcnt lgkmcnt(3)
	v_mfma_f32_16x16x32_f16 v[92:95], v[40:43], v[64:67], v[92:95]
	ds_read_b128 v[116:119], v115
	v_mfma_f32_16x16x32_f16 v[88:91], v[48:51], v[64:67], v[88:91]
	v_xor_b32_e32 v153, 64, v114
	s_add_i32 s4, s45, 61
	s_add_i32 s4, s4, s12
	s_lshl_b32 s4, s4, 14
	s_waitcnt lgkmcnt(3)
	v_mfma_f32_16x16x32_f16 v[60:63], v[40:43], v[68:71], v[60:63]
	ds_read_b128 v[120:123], v115 offset:2048
	v_lshl_add_u64 v[148:149], v[100:101], 0, s[4:5]
	s_and_b32 s42, s13, 0xc000
	s_add_i32 s42, s42, s27
	v_mfma_f32_16x16x32_f16 v[44:47], v[48:51], v[68:71], v[44:47]
	v_xor_b32_e32 v152, 64, v113
	s_mov_b32 m0, s42
	s_add_i32 s16, s13, 0xffff8000
	global_load_lds_dwordx4 v[148:149], off
	v_mfma_f32_16x16x32_f16 v[28:31], v[40:43], v[56:59], v[28:31]
	ds_read_b128 v[124:127], v153
	v_mfma_f32_16x16x32_f16 v[24:27], v[48:51], v[56:59], v[24:27]
	s_and_b32 s16, s16, 0xc000
	s_add_i32 s43, s42, 0x400
	v_lshl_add_u64 v[150:151], v[148:149], 0, s[8:9]
	v_mfma_f32_16x16x32_f16 v[12:15], v[40:43], v[52:55], v[12:15]
	ds_read_b128 v[128:131], v153 offset:2048
	v_mfma_f32_16x16x32_f16 v[8:11], v[48:51], v[52:55], v[8:11]
	v_add_u32_e32 v154, s16, v110
	s_add_i32 s44, s45, 103
	s_waitcnt lgkmcnt(5)
	v_mfma_f32_16x16x32_f16 v[84:87], v[76:79], v[64:67], v[84:87]
	ds_read_b128 v[132:135], v152
	s_waitcnt lgkmcnt(5)
	v_mfma_f32_16x16x32_f16 v[72:75], v[80:83], v[64:67], v[72:75]
	v_mfma_f32_16x16x32_f16 v[36:39], v[76:79], v[68:71], v[36:39]
	ds_read_b128 v[136:139], v152 offset:2048
	v_mfma_f32_16x16x32_f16 v[32:35], v[80:83], v[68:71], v[32:35]
	v_add_u32_e32 v155, s44, v98
	v_mfma_f32_16x16x32_f16 v[20:23], v[76:79], v[56:59], v[20:23]
	ds_read_b128 v[140:143], v115 offset:4096
	v_mfma_f32_16x16x32_f16 v[16:19], v[80:83], v[56:59], v[16:19]
	v_lshlrev_b32_e32 v156, 7, v155
	v_bitop3_b32 v155, v155, v99, 6 bitop3:0x6c
	v_mfma_f32_16x16x32_f16 v[4:7], v[76:79], v[52:55], v[4:7]
	ds_read_b128 v[144:147], v115 offset:6144
	v_mfma_f32_16x16x32_f16 v[0:3], v[80:83], v[52:55], v[0:3]
	v_lshl_or_b32 v114, v155, 4, v156
	v_add_u32_e32 v115, s16, v111
	s_waitcnt lgkmcnt(3)
	v_mfma_f32_16x16x32_f16 v[92:95], v[116:119], v[132:135], v[92:95]
	ds_read_b128 v[40:43], v154
	v_mfma_f32_16x16x32_f16 v[88:91], v[120:123], v[132:135], v[88:91]
	s_mov_b32 m0, s43
	s_addk_i32 s13, 0x4000
	global_load_lds_dwordx4 v[150:151], off
	s_waitcnt lgkmcnt(3)
	v_mfma_f32_16x16x32_f16 v[60:63], v[116:119], v[136:139], v[60:63]
	ds_read_b128 v[48:51], v154 offset:2048
	v_mfma_f32_16x16x32_f16 v[44:47], v[120:123], v[136:139], v[44:47]
	v_mfma_f32_16x16x32_f16 v[28:31], v[116:119], v[124:127], v[28:31]
	ds_read_b128 v[64:67], v114
	v_mfma_f32_16x16x32_f16 v[24:27], v[120:123], v[124:127], v[24:27]
	v_mfma_f32_16x16x32_f16 v[12:15], v[116:119], v[128:131], v[12:15]
	ds_read_b128 v[68:71], v114 offset:2048
	v_mfma_f32_16x16x32_f16 v[8:11], v[120:123], v[128:131], v[8:11]
	s_waitcnt lgkmcnt(5)
	v_mfma_f32_16x16x32_f16 v[84:87], v[140:143], v[132:135], v[84:87]
	s_waitcnt lgkmcnt(4)
	v_mfma_f32_16x16x32_f16 v[72:75], v[144:147], v[132:135], v[72:75]
	v_mfma_f32_16x16x32_f16 v[36:39], v[140:143], v[136:139], v[36:39]
	v_mfma_f32_16x16x32_f16 v[32:35], v[144:147], v[136:139], v[32:35]
	v_mfma_f32_16x16x32_f16 v[20:23], v[140:143], v[124:127], v[20:23]
	ds_read_b128 v[76:79], v154 offset:4096
	v_mfma_f32_16x16x32_f16 v[16:19], v[144:147], v[124:127], v[16:19]
	v_mfma_f32_16x16x32_f16 v[4:7], v[140:143], v[128:131], v[4:7]
	ds_read_b128 v[80:83], v154 offset:6144
	v_mfma_f32_16x16x32_f16 v[0:3], v[144:147], v[128:131], v[0:3]
	s_waitcnt vmcnt(2)
	s_barrier
	s_waitcnt lgkmcnt(5)
	v_mfma_f32_16x16x32_f16 v[92:95], v[40:43], v[56:59], v[92:95]
	ds_read_b128 v[116:119], v115
	s_waitcnt lgkmcnt(5)
	v_mfma_f32_16x16x32_f16 v[88:91], v[48:51], v[56:59], v[88:91]
	v_xor_b32_e32 v153, 64, v114
	s_add_i32 s4, s45, 81
	s_add_i32 s4, s4, s12
	s_lshl_b32 s4, s4, 14
	v_mfma_f32_16x16x32_f16 v[60:63], v[40:43], v[52:55], v[60:63]
	ds_read_b128 v[120:123], v115 offset:2048
	v_lshl_add_u64 v[148:149], v[100:101], 0, s[4:5]
	s_and_b32 s42, s13, 0xc000
	s_add_i32 s42, s42, s27
	v_mfma_f32_16x16x32_f16 v[44:47], v[48:51], v[52:55], v[44:47]
	s_mov_b32 m0, s42
	s_add_i32 s16, s13, 0xffff8000
	global_load_lds_dwordx4 v[148:149], off
	s_waitcnt lgkmcnt(5)
	v_mfma_f32_16x16x32_f16 v[28:31], v[40:43], v[64:67], v[28:31]
	ds_read_b128 v[132:135], v153
	v_mfma_f32_16x16x32_f16 v[24:27], v[48:51], v[64:67], v[24:27]
	s_and_b32 s16, s16, 0xc000
	s_add_i32 s43, s42, 0x400
	v_lshl_add_u64 v[150:151], v[148:149], 0, s[8:9]
	s_waitcnt lgkmcnt(5)
	v_mfma_f32_16x16x32_f16 v[12:15], v[40:43], v[68:71], v[12:15]
	ds_read_b128 v[136:139], v153 offset:2048
	v_mfma_f32_16x16x32_f16 v[8:11], v[48:51], v[68:71], v[8:11]
	v_add_u32_e32 v154, s16, v110
	s_add_i32 s44, s45, 154
	s_waitcnt lgkmcnt(5)
	v_mfma_f32_16x16x32_f16 v[84:87], v[76:79], v[56:59], v[84:87]
	s_waitcnt lgkmcnt(4)
	v_mfma_f32_16x16x32_f16 v[72:75], v[80:83], v[56:59], v[72:75]
	v_mfma_f32_16x16x32_f16 v[36:39], v[76:79], v[52:55], v[36:39]
	v_mfma_f32_16x16x32_f16 v[32:35], v[80:83], v[52:55], v[32:35]
	v_add_u32_e32 v155, s44, v98
	v_mfma_f32_16x16x32_f16 v[20:23], v[76:79], v[64:67], v[20:23]
	ds_read_b128 v[140:143], v115 offset:4096
	v_mfma_f32_16x16x32_f16 v[16:19], v[80:83], v[64:67], v[16:19]
	v_lshlrev_b32_e32 v156, 7, v155
	v_bitop3_b32 v155, v155, v99, 6 bitop3:0x6c
	v_mfma_f32_16x16x32_f16 v[4:7], v[76:79], v[68:71], v[4:7]
	ds_read_b128 v[144:147], v115 offset:6144
	v_mfma_f32_16x16x32_f16 v[0:3], v[80:83], v[68:71], v[0:3]
	v_lshl_or_b32 v114, v155, 4, v156
	v_add_u32_e32 v115, s16, v111
	s_waitcnt lgkmcnt(5)
	v_mfma_f32_16x16x32_f16 v[92:95], v[116:119], v[124:127], v[92:95]
	ds_read_b128 v[40:43], v154
	s_waitcnt lgkmcnt(5)
	v_mfma_f32_16x16x32_f16 v[88:91], v[120:123], v[124:127], v[88:91]
	s_mov_b32 m0, s43
	s_addk_i32 s13, 0x4000
	global_load_lds_dwordx4 v[150:151], off
	v_mfma_f32_16x16x32_f16 v[60:63], v[116:119], v[128:131], v[60:63]
	ds_read_b128 v[48:51], v154 offset:2048
	v_mfma_f32_16x16x32_f16 v[44:47], v[120:123], v[128:131], v[44:47]
	s_waitcnt lgkmcnt(5)
	v_mfma_f32_16x16x32_f16 v[28:31], v[116:119], v[132:135], v[28:31]
	ds_read_b128 v[56:59], v114
	v_mfma_f32_16x16x32_f16 v[24:27], v[120:123], v[132:135], v[24:27]
	s_waitcnt lgkmcnt(5)
	v_mfma_f32_16x16x32_f16 v[12:15], v[116:119], v[136:139], v[12:15]
	ds_read_b128 v[52:55], v114 offset:2048
	v_mfma_f32_16x16x32_f16 v[8:11], v[120:123], v[136:139], v[8:11]
	s_waitcnt lgkmcnt(5)
	v_mfma_f32_16x16x32_f16 v[84:87], v[140:143], v[124:127], v[84:87]
	s_waitcnt lgkmcnt(4)
	v_mfma_f32_16x16x32_f16 v[72:75], v[144:147], v[124:127], v[72:75]
	v_mfma_f32_16x16x32_f16 v[36:39], v[140:143], v[128:131], v[36:39]
	v_mfma_f32_16x16x32_f16 v[32:35], v[144:147], v[128:131], v[32:35]
	v_mfma_f32_16x16x32_f16 v[20:23], v[140:143], v[132:135], v[20:23]
	ds_read_b128 v[76:79], v154 offset:4096
	v_mfma_f32_16x16x32_f16 v[16:19], v[144:147], v[132:135], v[16:19]
	v_mfma_f32_16x16x32_f16 v[4:7], v[140:143], v[136:139], v[4:7]
	ds_read_b128 v[80:83], v154 offset:6144
	v_mfma_f32_16x16x32_f16 v[0:3], v[144:147], v[136:139], v[0:3]
	s_waitcnt vmcnt(2)
	s_barrier
	s_waitcnt lgkmcnt(5)
	v_mfma_f32_16x16x32_f16 v[92:95], v[40:43], v[64:67], v[92:95]
	ds_read_b128 v[116:119], v115
	s_waitcnt lgkmcnt(5)
	v_mfma_f32_16x16x32_f16 v[88:91], v[48:51], v[64:67], v[88:91]
	v_xor_b32_e32 v153, 64, v114
	s_add_i32 s4, s45, 2
	s_add_i32 s4, s4, s12
	s_lshl_b32 s4, s4, 14
	v_mfma_f32_16x16x32_f16 v[60:63], v[40:43], v[68:71], v[60:63]
	ds_read_b128 v[120:123], v115 offset:2048
	v_lshl_add_u64 v[148:149], v[100:101], 0, s[4:5]
	s_and_b32 s42, s13, 0xc000
	s_add_i32 s42, s42, s27
	v_mfma_f32_16x16x32_f16 v[44:47], v[48:51], v[68:71], v[44:47]
	s_mov_b32 m0, s42
	s_add_i32 s16, s13, 0xffff8000
	global_load_lds_dwordx4 v[148:149], off
	s_waitcnt lgkmcnt(5)
	v_mfma_f32_16x16x32_f16 v[28:31], v[40:43], v[56:59], v[28:31]
	ds_read_b128 v[124:127], v153
	v_mfma_f32_16x16x32_f16 v[24:27], v[48:51], v[56:59], v[24:27]
	s_and_b32 s16, s16, 0xc000
	s_add_i32 s43, s42, 0x400
	v_lshl_add_u64 v[150:151], v[148:149], 0, s[8:9]
	s_waitcnt lgkmcnt(5)
	v_mfma_f32_16x16x32_f16 v[12:15], v[40:43], v[52:55], v[12:15]
	ds_read_b128 v[128:131], v153 offset:2048
	v_mfma_f32_16x16x32_f16 v[8:11], v[48:51], v[52:55], v[8:11]
	v_add_u32_e32 v154, s16, v110
	s_add_i32 s44, s45, 205
	s_waitcnt lgkmcnt(5)
	v_mfma_f32_16x16x32_f16 v[84:87], v[76:79], v[64:67], v[84:87]
	s_waitcnt lgkmcnt(4)
	v_mfma_f32_16x16x32_f16 v[72:75], v[80:83], v[64:67], v[72:75]
	v_mfma_f32_16x16x32_f16 v[36:39], v[76:79], v[68:71], v[36:39]
	v_mfma_f32_16x16x32_f16 v[32:35], v[80:83], v[68:71], v[32:35]
	v_add_u32_e32 v155, s44, v98
	v_mfma_f32_16x16x32_f16 v[20:23], v[76:79], v[56:59], v[20:23]
	ds_read_b128 v[140:143], v115 offset:4096
	v_mfma_f32_16x16x32_f16 v[16:19], v[80:83], v[56:59], v[16:19]
	v_lshlrev_b32_e32 v156, 7, v155
	v_bitop3_b32 v155, v155, v99, 6 bitop3:0x6c
	v_mfma_f32_16x16x32_f16 v[4:7], v[76:79], v[52:55], v[4:7]
	ds_read_b128 v[144:147], v115 offset:6144
	v_mfma_f32_16x16x32_f16 v[0:3], v[80:83], v[52:55], v[0:3]
	v_lshl_or_b32 v114, v155, 4, v156
	v_add_u32_e32 v115, s16, v111
	s_waitcnt lgkmcnt(5)
	v_mfma_f32_16x16x32_f16 v[92:95], v[116:119], v[132:135], v[92:95]
	ds_read_b128 v[40:43], v154
	s_waitcnt lgkmcnt(5)
	v_mfma_f32_16x16x32_f16 v[88:91], v[120:123], v[132:135], v[88:91]
	s_mov_b32 m0, s43
	s_addk_i32 s13, 0x4000
	global_load_lds_dwordx4 v[150:151], off
	v_mfma_f32_16x16x32_f16 v[60:63], v[116:119], v[136:139], v[60:63]
	ds_read_b128 v[48:51], v154 offset:2048
	v_mfma_f32_16x16x32_f16 v[44:47], v[120:123], v[136:139], v[44:47]
	s_waitcnt lgkmcnt(5)
	v_mfma_f32_16x16x32_f16 v[28:31], v[116:119], v[124:127], v[28:31]
	ds_read_b128 v[64:67], v114
	v_mfma_f32_16x16x32_f16 v[24:27], v[120:123], v[124:127], v[24:27]
	s_waitcnt lgkmcnt(5)
	v_mfma_f32_16x16x32_f16 v[12:15], v[116:119], v[128:131], v[12:15]
	ds_read_b128 v[68:71], v114 offset:2048
	v_mfma_f32_16x16x32_f16 v[8:11], v[120:123], v[128:131], v[8:11]
	s_waitcnt lgkmcnt(5)
	v_mfma_f32_16x16x32_f16 v[84:87], v[140:143], v[132:135], v[84:87]
	s_waitcnt lgkmcnt(4)
	v_mfma_f32_16x16x32_f16 v[72:75], v[144:147], v[132:135], v[72:75]
	v_mfma_f32_16x16x32_f16 v[36:39], v[140:143], v[136:139], v[36:39]
	v_mfma_f32_16x16x32_f16 v[32:35], v[144:147], v[136:139], v[32:35]
	v_mfma_f32_16x16x32_f16 v[20:23], v[140:143], v[124:127], v[20:23]
	ds_read_b128 v[76:79], v154 offset:4096
	v_mfma_f32_16x16x32_f16 v[16:19], v[144:147], v[124:127], v[16:19]
	v_mfma_f32_16x16x32_f16 v[4:7], v[140:143], v[128:131], v[4:7]
	ds_read_b128 v[80:83], v154 offset:6144
	v_mfma_f32_16x16x32_f16 v[0:3], v[144:147], v[128:131], v[0:3]
	s_waitcnt vmcnt(2)
	s_barrier
	s_waitcnt lgkmcnt(5)
	v_mfma_f32_16x16x32_f16 v[92:95], v[40:43], v[56:59], v[92:95]
	ds_read_b128 v[116:119], v115
	s_waitcnt lgkmcnt(5)
	v_mfma_f32_16x16x32_f16 v[88:91], v[48:51], v[56:59], v[88:91]
	v_xor_b32_e32 v153, 64, v114
	s_add_i32 s4, s45, 22
	s_add_i32 s4, s4, s12
	s_lshl_b32 s4, s4, 14
	v_mfma_f32_16x16x32_f16 v[60:63], v[40:43], v[52:55], v[60:63]
	ds_read_b128 v[120:123], v115 offset:2048
	v_lshl_add_u64 v[148:149], v[100:101], 0, s[4:5]
	s_and_b32 s42, s13, 0xc000
	s_add_i32 s42, s42, s27
	v_mfma_f32_16x16x32_f16 v[44:47], v[48:51], v[52:55], v[44:47]
	s_mov_b32 m0, s42
	s_add_i32 s16, s13, 0xffff8000
	global_load_lds_dwordx4 v[148:149], off
	s_waitcnt lgkmcnt(5)
	v_mfma_f32_16x16x32_f16 v[28:31], v[40:43], v[64:67], v[28:31]
	ds_read_b128 v[132:135], v153
	v_mfma_f32_16x16x32_f16 v[24:27], v[48:51], v[64:67], v[24:27]
	s_and_b32 s16, s16, 0xc000
	s_add_i32 s43, s42, 0x400
	v_lshl_add_u64 v[150:151], v[148:149], 0, s[8:9]
	s_waitcnt lgkmcnt(5)
	v_mfma_f32_16x16x32_f16 v[12:15], v[40:43], v[68:71], v[12:15]
	ds_read_b128 v[136:139], v153 offset:2048
	v_mfma_f32_16x16x32_f16 v[8:11], v[48:51], v[68:71], v[8:11]
	v_add_u32_e32 v154, s16, v110
	s_add_i32 s44, s45, 256
	s_waitcnt lgkmcnt(5)
	v_mfma_f32_16x16x32_f16 v[84:87], v[76:79], v[56:59], v[84:87]
	s_waitcnt lgkmcnt(4)
	v_mfma_f32_16x16x32_f16 v[72:75], v[80:83], v[56:59], v[72:75]
	v_mfma_f32_16x16x32_f16 v[36:39], v[76:79], v[52:55], v[36:39]
	v_mfma_f32_16x16x32_f16 v[32:35], v[80:83], v[52:55], v[32:35]
	v_add_u32_e32 v155, s44, v98
	v_mfma_f32_16x16x32_f16 v[20:23], v[76:79], v[64:67], v[20:23]
	ds_read_b128 v[140:143], v115 offset:4096
	v_mfma_f32_16x16x32_f16 v[16:19], v[80:83], v[64:67], v[16:19]
	v_lshlrev_b32_e32 v156, 7, v155
	v_bitop3_b32 v155, v155, v99, 6 bitop3:0x6c
	v_mfma_f32_16x16x32_f16 v[4:7], v[76:79], v[68:71], v[4:7]
	ds_read_b128 v[144:147], v115 offset:6144
	v_mfma_f32_16x16x32_f16 v[0:3], v[80:83], v[68:71], v[0:3]
	v_lshl_or_b32 v114, v155, 4, v156
	v_add_u32_e32 v115, s16, v111
	s_waitcnt lgkmcnt(5)
	v_mfma_f32_16x16x32_f16 v[92:95], v[116:119], v[124:127], v[92:95]
	ds_read_b128 v[40:43], v154
	s_waitcnt lgkmcnt(5)
	v_mfma_f32_16x16x32_f16 v[88:91], v[120:123], v[124:127], v[88:91]
	s_mov_b32 m0, s43
	s_addk_i32 s13, 0x4000
	global_load_lds_dwordx4 v[150:151], off
	v_mfma_f32_16x16x32_f16 v[60:63], v[116:119], v[128:131], v[60:63]
	ds_read_b128 v[48:51], v154 offset:2048
	v_mfma_f32_16x16x32_f16 v[44:47], v[120:123], v[128:131], v[44:47]
	s_waitcnt lgkmcnt(5)
	v_mfma_f32_16x16x32_f16 v[28:31], v[116:119], v[132:135], v[28:31]
	ds_read_b128 v[56:59], v114
	v_mfma_f32_16x16x32_f16 v[24:27], v[120:123], v[132:135], v[24:27]
	s_waitcnt lgkmcnt(5)
	v_mfma_f32_16x16x32_f16 v[12:15], v[116:119], v[136:139], v[12:15]
	ds_read_b128 v[52:55], v114 offset:2048
	v_mfma_f32_16x16x32_f16 v[8:11], v[120:123], v[136:139], v[8:11]
	s_waitcnt lgkmcnt(5)
	v_mfma_f32_16x16x32_f16 v[84:87], v[140:143], v[124:127], v[84:87]
	s_waitcnt lgkmcnt(4)
	v_mfma_f32_16x16x32_f16 v[72:75], v[144:147], v[124:127], v[72:75]
	v_mfma_f32_16x16x32_f16 v[36:39], v[140:143], v[128:131], v[36:39]
	v_mfma_f32_16x16x32_f16 v[32:35], v[144:147], v[128:131], v[32:35]
	v_mfma_f32_16x16x32_f16 v[20:23], v[140:143], v[132:135], v[20:23]
	ds_read_b128 v[76:79], v154 offset:4096
	v_mfma_f32_16x16x32_f16 v[16:19], v[144:147], v[132:135], v[16:19]
	v_mfma_f32_16x16x32_f16 v[4:7], v[140:143], v[136:139], v[4:7]
	ds_read_b128 v[80:83], v154 offset:6144
	v_mfma_f32_16x16x32_f16 v[0:3], v[144:147], v[136:139], v[0:3]
	s_waitcnt vmcnt(2)
	s_barrier
	s_waitcnt lgkmcnt(5)
	v_mfma_f32_16x16x32_f16 v[92:95], v[40:43], v[64:67], v[92:95]
	ds_read_b128 v[116:119], v115
	s_waitcnt lgkmcnt(5)
	v_mfma_f32_16x16x32_f16 v[88:91], v[48:51], v[64:67], v[88:91]
	v_xor_b32_e32 v153, 64, v114
	s_add_i32 s4, s45, 42
	s_add_i32 s4, s4, s12
	s_lshl_b32 s4, s4, 14
	v_mfma_f32_16x16x32_f16 v[60:63], v[40:43], v[68:71], v[60:63]
	ds_read_b128 v[120:123], v115 offset:2048
	v_lshl_add_u64 v[148:149], v[100:101], 0, s[4:5]
	s_and_b32 s42, s13, 0xc000
	s_add_i32 s42, s42, s27
	v_mfma_f32_16x16x32_f16 v[44:47], v[48:51], v[68:71], v[44:47]
	s_mov_b32 m0, s42
	s_add_i32 s16, s13, 0xffff8000
	global_load_lds_dwordx4 v[148:149], off
	s_waitcnt lgkmcnt(5)
	v_mfma_f32_16x16x32_f16 v[28:31], v[40:43], v[56:59], v[28:31]
	ds_read_b128 v[124:127], v153
	v_mfma_f32_16x16x32_f16 v[24:27], v[48:51], v[56:59], v[24:27]
	s_and_b32 s16, s16, 0xc000
	s_add_i32 s43, s42, 0x400
	v_lshl_add_u64 v[150:151], v[148:149], 0, s[8:9]
	s_waitcnt lgkmcnt(5)
	v_mfma_f32_16x16x32_f16 v[12:15], v[40:43], v[52:55], v[12:15]
	ds_read_b128 v[128:131], v153 offset:2048
	v_mfma_f32_16x16x32_f16 v[8:11], v[48:51], v[52:55], v[8:11]
	v_add_u32_e32 v154, s16, v110
	s_add_i32 s44, s45, 53
	s_waitcnt lgkmcnt(5)
	v_mfma_f32_16x16x32_f16 v[84:87], v[76:79], v[64:67], v[84:87]
	s_waitcnt lgkmcnt(4)
	v_mfma_f32_16x16x32_f16 v[72:75], v[80:83], v[64:67], v[72:75]
	v_mfma_f32_16x16x32_f16 v[36:39], v[76:79], v[68:71], v[36:39]
	v_mfma_f32_16x16x32_f16 v[32:35], v[80:83], v[68:71], v[32:35]
	v_add_u32_e32 v155, s44, v98
	v_mfma_f32_16x16x32_f16 v[20:23], v[76:79], v[56:59], v[20:23]
	ds_read_b128 v[140:143], v115 offset:4096
	v_mfma_f32_16x16x32_f16 v[16:19], v[80:83], v[56:59], v[16:19]
	v_lshlrev_b32_e32 v156, 7, v155
	v_bitop3_b32 v155, v155, v99, 6 bitop3:0x6c
	v_mfma_f32_16x16x32_f16 v[4:7], v[76:79], v[52:55], v[4:7]
	ds_read_b128 v[144:147], v115 offset:6144
	v_mfma_f32_16x16x32_f16 v[0:3], v[80:83], v[52:55], v[0:3]
	v_lshl_or_b32 v114, v155, 4, v156
	v_add_u32_e32 v115, s16, v111
	s_waitcnt lgkmcnt(5)
	v_mfma_f32_16x16x32_f16 v[92:95], v[116:119], v[132:135], v[92:95]
	ds_read_b128 v[40:43], v154
	s_waitcnt lgkmcnt(5)
	v_mfma_f32_16x16x32_f16 v[88:91], v[120:123], v[132:135], v[88:91]
	s_mov_b32 m0, s43
	s_addk_i32 s13, 0x4000
	global_load_lds_dwordx4 v[150:151], off
	v_mfma_f32_16x16x32_f16 v[60:63], v[116:119], v[136:139], v[60:63]
	ds_read_b128 v[48:51], v154 offset:2048
	v_mfma_f32_16x16x32_f16 v[44:47], v[120:123], v[136:139], v[44:47]
	s_sub_i32 s44, s44, 51
	v_add_u32_e32 v155, s44, v98
	s_waitcnt lgkmcnt(5)
	v_mfma_f32_16x16x32_f16 v[28:31], v[116:119], v[124:127], v[28:31]
	ds_read_b128 v[64:67], v114
	v_mfma_f32_16x16x32_f16 v[24:27], v[120:123], v[124:127], v[24:27]
	v_lshlrev_b32_e32 v156, 7, v155
	v_bitop3_b32 v155, v155, v99, 6 bitop3:0x6c
	s_waitcnt lgkmcnt(5)
	v_mfma_f32_16x16x32_f16 v[12:15], v[116:119], v[128:131], v[12:15]
	ds_read_b128 v[68:71], v114 offset:2048
	v_mfma_f32_16x16x32_f16 v[8:11], v[120:123], v[128:131], v[8:11]
	v_lshl_or_b32 v113, v155, 4, v156
	s_waitcnt lgkmcnt(5)
	v_mfma_f32_16x16x32_f16 v[84:87], v[140:143], v[132:135], v[84:87]
	ds_read_b128 v[56:59], v113
	s_waitcnt lgkmcnt(5)
	v_mfma_f32_16x16x32_f16 v[72:75], v[144:147], v[132:135], v[72:75]
	v_mfma_f32_16x16x32_f16 v[36:39], v[140:143], v[136:139], v[36:39]
	ds_read_b128 v[52:55], v113 offset:2048
	v_mfma_f32_16x16x32_f16 v[32:35], v[144:147], v[136:139], v[32:35]
	v_mfma_f32_16x16x32_f16 v[20:23], v[140:143], v[124:127], v[20:23]
	ds_read_b128 v[76:79], v154 offset:4096
	v_mfma_f32_16x16x32_f16 v[16:19], v[144:147], v[124:127], v[16:19]
	s_add_i32 s45, s45, 2
	s_add_i32 s14, s14, 1
	v_mfma_f32_16x16x32_f16 v[4:7], v[140:143], v[128:131], v[4:7]
	ds_read_b128 v[80:83], v154 offset:6144
	s_cmp_eq_u32 s14, 10
	v_mfma_f32_16x16x32_f16 v[0:3], v[144:147], v[128:131], v[0:3]
	s_cbranch_scc0 .Lc1_loop
	s_waitcnt vmcnt(0) lgkmcnt(0)
	s_cmpk_gt_u32 s34, 0x1ff
	s_barrier
	s_cbranch_scc1 .LBB3_8
	s_mov_b32 s0, s88
	v_lshl_or_b32 v40, s10, 6, v96
	s_movk_i32 s4, 0x110
	v_lshlrev_b32_e32 v41, 3, v99
	s_lshl_b32 s1, s11, 1
	v_mul_lo_u32 v40, v40, s4
	v_add3_u32 v48, s1, v41, v40
	v_mov_b32_e32 v40, v93
	v_mov_b32_e32 v41, v94
	s_waitcnt lgkmcnt(0)
	v_pk_mul_f32 v[40:41], s[0:1], v[40:41] op_sel_hi:[0,1]
	v_fma_mixlo_f16 v42, s0, v92, 0
	v_cvt_pk_f16_f32 v41, v40, v41
	v_pack_b32_f16 v40, v42, v41
	v_fma_mixlo_f16 v42, s0, v95, 0
	v_alignbit_b32 v41, v42, v41, 16
	v_mov_b32_e32 v42, v89
	v_mov_b32_e32 v43, v90
	v_pk_mul_f32 v[42:43], s[0:1], v[42:43] op_sel_hi:[0,1]
	v_fma_mixlo_f16 v49, s0, v88, 0
	v_cvt_pk_f16_f32 v43, v42, v43
	v_pack_b32_f16 v42, v49, v43
	v_fma_mixlo_f16 v49, s0, v91, 0
	v_alignbit_b32 v43, v49, v43, 16
	ds_write2_b64 v48, v[40:41], v[42:43] offset1:4
	v_mov_b32_e32 v40, v85
	v_mov_b32_e32 v41, v86
	v_pk_mul_f32 v[40:41], s[0:1], v[40:41] op_sel_hi:[0,1]
	v_fma_mixlo_f16 v42, s0, v84, 0
	v_cvt_pk_f16_f32 v41, v40, v41
	v_pack_b32_f16 v40, v42, v41
	v_fma_mixlo_f16 v42, s0, v87, 0
	v_alignbit_b32 v41, v42, v41, 16
	v_mov_b32_e32 v42, v73
	v_mov_b32_e32 v43, v74
	v_pk_mul_f32 v[42:43], s[0:1], v[42:43] op_sel_hi:[0,1]
	v_fma_mixlo_f16 v49, s0, v72, 0
	v_cvt_pk_f16_f32 v43, v42, v43
	v_pack_b32_f16 v42, v49, v43
	v_fma_mixlo_f16 v49, s0, v75, 0
	v_alignbit_b32 v43, v49, v43, 16
	ds_write2_b64 v48, v[40:41], v[42:43] offset0:8 offset1:12
	v_mov_b32_e32 v40, v61
	v_mov_b32_e32 v41, v62
	v_pk_mul_f32 v[40:41], s[0:1], v[40:41] op_sel_hi:[0,1]
	v_fma_mixlo_f16 v42, s0, v60, 0
	v_cvt_pk_f16_f32 v41, v40, v41
	v_pack_b32_f16 v40, v42, v41
	v_fma_mixlo_f16 v42, s0, v63, 0
	v_alignbit_b32 v41, v42, v41, 16
	v_mov_b32_e32 v42, v45
	v_mov_b32_e32 v43, v46
	v_pk_mul_f32 v[42:43], s[0:1], v[42:43] op_sel_hi:[0,1]
	v_fma_mixlo_f16 v44, s0, v44, 0
	v_cvt_pk_f16_f32 v43, v42, v43
	v_pack_b32_f16 v42, v44, v43
	v_fma_mixlo_f16 v44, s0, v47, 0
	v_alignbit_b32 v43, v44, v43, 16
	v_add_u32_e32 v44, 0x1000, v48
	ds_write2_b64 v44, v[40:41], v[42:43] offset0:32 offset1:36
	v_fma_mixlo_f16 v40, s0, v36, 0
	v_mov_b32_e32 v36, v37
	v_mov_b32_e32 v37, v38
	v_pk_mul_f32 v[36:37], s[0:1], v[36:37] op_sel_hi:[0,1]
	v_cvt_pk_f16_f32 v37, v36, v37
	v_fma_mixlo_f16 v38, s0, v39, 0
	v_pack_b32_f16 v36, v40, v37
	v_alignbit_b32 v37, v38, v37, 16
	v_fma_mixlo_f16 v38, s0, v32, 0
	v_mov_b32_e32 v32, v33
	v_mov_b32_e32 v33, v34
	v_pk_mul_f32 v[32:33], s[0:1], v[32:33] op_sel_hi:[0,1]
	v_cvt_pk_f16_f32 v33, v32, v33
	v_fma_mixlo_f16 v34, s0, v35, 0
	v_pack_b32_f16 v32, v38, v33
	v_alignbit_b32 v33, v34, v33, 16
	ds_write2_b64 v44, v[36:37], v[32:33] offset0:40 offset1:44
	v_fma_mixlo_f16 v32, s0, v28, 0
	v_mov_b32_e32 v28, v29
	v_mov_b32_e32 v29, v30
	v_pk_mul_f32 v[28:29], s[0:1], v[28:29] op_sel_hi:[0,1]
	v_cvt_pk_f16_f32 v29, v28, v29
	v_fma_mixlo_f16 v30, s0, v31, 0
	v_pack_b32_f16 v28, v32, v29
	v_alignbit_b32 v29, v30, v29, 16
	v_fma_mixlo_f16 v30, s0, v24, 0
	v_mov_b32_e32 v24, v25
	v_mov_b32_e32 v25, v26
	v_pk_mul_f32 v[24:25], s[0:1], v[24:25] op_sel_hi:[0,1]
	v_cvt_pk_f16_f32 v25, v24, v25
	v_fma_mixlo_f16 v26, s0, v27, 0
	v_pack_b32_f16 v24, v30, v25
	v_alignbit_b32 v25, v26, v25, 16
	v_add_u32_e32 v26, 0x2000, v48
	ds_write2_b64 v26, v[28:29], v[24:25] offset0:64 offset1:68
	v_fma_mixlo_f16 v24, s0, v20, 0
	v_mov_b32_e32 v20, v21
	v_mov_b32_e32 v21, v22
	v_pk_mul_f32 v[20:21], s[0:1], v[20:21] op_sel_hi:[0,1]
	v_cvt_pk_f16_f32 v21, v20, v21
	v_fma_mixlo_f16 v22, s0, v23, 0
	v_pack_b32_f16 v20, v24, v21
	v_alignbit_b32 v21, v22, v21, 16
	v_fma_mixlo_f16 v22, s0, v16, 0
	v_mov_b32_e32 v16, v17
	v_mov_b32_e32 v17, v18
	v_pk_mul_f32 v[16:17], s[0:1], v[16:17] op_sel_hi:[0,1]
	v_cvt_pk_f16_f32 v17, v16, v17
	v_fma_mixlo_f16 v18, s0, v19, 0
	v_pack_b32_f16 v16, v22, v17
	v_alignbit_b32 v17, v18, v17, 16
	ds_write2_b64 v26, v[20:21], v[16:17] offset0:72 offset1:76
	v_fma_mixlo_f16 v16, s0, v12, 0
	v_mov_b32_e32 v12, v13
	v_mov_b32_e32 v13, v14
	v_pk_mul_f32 v[12:13], s[0:1], v[12:13] op_sel_hi:[0,1]
	v_cvt_pk_f16_f32 v13, v12, v13
	v_fma_mixlo_f16 v14, s0, v15, 0
	v_pack_b32_f16 v12, v16, v13
	v_alignbit_b32 v13, v14, v13, 16
	v_fma_mixlo_f16 v14, s0, v8, 0
	v_mov_b32_e32 v8, v9
	v_mov_b32_e32 v9, v10
	v_pk_mul_f32 v[8:9], s[0:1], v[8:9] op_sel_hi:[0,1]
	v_cvt_pk_f16_f32 v9, v8, v9
	v_fma_mixlo_f16 v10, s0, v11, 0
	v_pack_b32_f16 v8, v14, v9
	v_alignbit_b32 v9, v10, v9, 16
	v_add_u32_e32 v10, 0x3000, v48
	ds_write2_b64 v10, v[12:13], v[8:9] offset0:96 offset1:100
	v_fma_mixlo_f16 v8, s0, v4, 0
	v_mov_b32_e32 v4, v5
	v_mov_b32_e32 v5, v6
	v_pk_mul_f32 v[4:5], s[0:1], v[4:5] op_sel_hi:[0,1]
	v_cvt_pk_f16_f32 v5, v4, v5
	v_fma_mixlo_f16 v6, s0, v7, 0
	v_pack_b32_f16 v4, v8, v5
	v_alignbit_b32 v5, v6, v5, 16
	v_fma_mixlo_f16 v6, s0, v0, 0
	v_mov_b32_e32 v0, v1
	v_mov_b32_e32 v1, v2
	v_pk_mul_f32 v[0:1], s[0:1], v[0:1] op_sel_hi:[0,1]
	v_cvt_pk_f16_f32 v1, v0, v1
	v_fma_mixlo_f16 v2, s0, v3, 0
	v_pack_b32_f16 v0, v6, v1
	v_alignbit_b32 v1, v2, v1, 16
	ds_write2_b64 v10, v[4:5], v[0:1] offset0:104 offset1:108

_Z6conv_kILi128ELi256ELi3ELi64ELi1ELi1ELb0EEvPKDF16_S1_PKfS3_PDF16_S4_S1_fS3_S3_S3_S3_:
	s_lshl_b32 s3, s2, 3
	s_load_dwordx2 s[20:21], s[0:1], 0x0
	s_load_dword s88, s[0:1], 0x38
	s_load_dwordx2 s[84:85], s[0:1], 0x8
	s_load_dwordx4 s[4:7], s[0:1], 0x10
	s_load_dwordx2 s[18:19], s[0:1], 0x30
	s_and_b32 s3, s3, 56
	s_ashr_i32 s8, s2, 5
	s_add_i32 s3, s3, s8
	v_readfirstlane_b32 s27, v0
	s_lshl_b32 s8, s3, 2
	s_bfe_u32 s22, s2, 0x20003
	s_and_b32 s24, s8, 56
	s_lshr_b32 s33, s27, 6
	s_ashr_i32 s25, s3, 4
	s_and_b32 s15, s2, 32
	s_lshl_b32 s2, s22, 8
	v_bfe_u32 v24, v0, 3, 3
	v_and_b32_e32 v2, 7, v0
	s_waitcnt lgkmcnt(0)
	s_add_u32 s2, s4, s2
	v_bitop3_b32 v2, v24, v2, 6 bitop3:0x6c
	s_addc_u32 s3, s5, 0
	v_and_b32_e32 v18, 48, v0
	v_mov_b32_e32 v19, 0
	v_lshlrev_b32_e32 v20, 3, v2
	v_lshl_add_u64 v[2:3], s[2:3], 0, v[18:19]
	s_load_dword s14, s[6:7], 0x0
	global_load_dwordx4 v[14:17], v[2:3], off
	v_lshl_add_u64 v[4:5], v[2:3], 0, 64
	s_mov_b64 s[2:3], 0x80
	global_load_dwordx4 v[10:13], v[4:5], off
	v_lshl_add_u64 v[4:5], v[2:3], 0, s[2:3]
	s_mov_b64 s[2:3], 0xc0
	v_lshl_add_u64 v[2:3], v[2:3], 0, s[2:3]
	v_lshl_or_b32 v18, s33, 3, v24
	s_mov_b32 s2, 0x1e1e1e1f
	v_mul_hi_u32 v21, v18, s2
	v_lshrrev_b32_e32 v21, 2, v21
	s_movk_i32 s4, 0xffde
	s_add_i32 s12, s24, -1
	global_load_dwordx4 v[6:9], v[4:5], off
	v_mul_lo_u32 v22, v21, s4
	v_add_u32_e32 v46, s12, v21
	s_add_i32 s13, s15, -1
	s_movk_i32 s5, 0x154
	global_load_dwordx4 v[2:5], v[2:3], off
	v_add3_u32 v47, s13, v18, v22
	v_cmp_gt_u32_e32 vcc, s5, v18
	v_cmp_gt_u32_e64 s[2:3], 64, v46
	s_and_b64 s[2:3], vcc, s[2:3]
	v_cmp_gt_u32_e32 vcc, 64, v47
	v_and_b32_e32 v1, 63, v0
	s_and_b64 vcc, s[2:3], vcc
	v_mov_b64_e32 v[22:23], s[18:19]
	v_lshlrev_b32_e32 v18, 1, v20
	s_and_saveexec_b64 s[2:3], vcc
	s_lshl_b32 s6, s25, 13
	v_lshlrev_b32_e32 v21, 6, v46
	v_or3_b32 v22, v21, s6, v47
	v_ashrrev_i32_e32 v23, 31, v22
	v_lshlrev_b64 v[22:23], 7, v[22:23]
	v_lshl_add_u64 v[22:23], s[20:21], 0, v[22:23]
	v_lshl_add_u64 v[22:23], v[22:23], 0, v[18:19]
	s_or_b64 exec, exec, s[2:3]
	s_lshl_b32 s36, s33, 10
	v_lshlrev_b32_e32 v21, 4, v1
	v_or_b32_e32 v19, s36, v21
	s_add_i32 s7, s33, 8
	v_readfirstlane_b32 s2, v19
	s_mov_b32 m0, s2
	v_lshl_or_b32 v19, s7, 3, v24
	global_load_lds_dwordx4 v[22:23], off
	s_mov_b32 s6, 0x3c3c3c3d
	v_mul_hi_u32 v22, v19, s6
	v_lshrrev_b32_e32 v22, 3, v22
	v_mul_lo_u32 v23, v22, s4
	v_add_u32_e32 v48, s12, v22
	v_add3_u32 v49, s13, v19, v23
	v_cmp_gt_u32_e64 s[2:3], s5, v19
	v_cmp_gt_u32_e64 s[4:5], 64, v48
	s_and_b64 s[4:5], s[2:3], s[4:5]
	v_cmp_gt_u32_e64 s[2:3], 64, v49
	s_and_b64 s[2:3], s[4:5], s[2:3]
	v_mov_b64_e32 v[22:23], s[18:19]
	s_and_saveexec_b64 s[4:5], s[2:3]
	s_lshl_b32 s8, s25, 13
	v_lshlrev_b32_e32 v19, 6, v48
	v_or3_b32 v22, v19, s8, v49
	v_ashrrev_i32_e32 v23, 31, v22
	v_lshlrev_b64 v[22:23], 7, v[22:23]
	v_lshl_add_u64 v[22:23], s[20:21], 0, v[22:23]
	v_mov_b32_e32 v19, 0
	v_lshl_add_u64 v[22:23], v[22:23], 0, v[18:19]
	s_or_b64 exec, exec, s[4:5]
	s_lshl_b32 s37, s7, 10
	v_or_b32_e32 v19, s37, v21
	s_add_i32 s10, s33, 16
	v_readfirstlane_b32 s4, v19
	s_mov_b32 m0, s4
	v_lshl_or_b32 v19, s10, 3, v24
	global_load_lds_dwordx4 v[22:23], off
	v_mul_hi_u32 v22, v19, s6
	v_lshrrev_b32_e32 v22, 3, v22
	s_movk_i32 s8, 0xffde
	v_mul_lo_u32 v23, v22, s8
	v_add_u32_e32 v58, s12, v22
	s_movk_i32 s9, 0x154
	v_add3_u32 v59, s13, v19, v23
	v_cmp_gt_u32_e64 s[4:5], s9, v19
	v_cmp_gt_u32_e64 s[6:7], 64, v58
	s_and_b64 s[6:7], s[4:5], s[6:7]
	v_cmp_gt_u32_e64 s[4:5], 64, v59
	s_and_b64 s[4:5], s[6:7], s[4:5]
	v_mov_b64_e32 v[22:23], s[18:19]
	s_and_saveexec_b64 s[6:7], s[4:5]
	s_lshl_b32 s11, s25, 13
	v_lshlrev_b32_e32 v19, 6, v58
	v_or3_b32 v22, v19, s11, v59
	v_ashrrev_i32_e32 v23, 31, v22
	v_lshlrev_b64 v[22:23], 7, v[22:23]
	v_lshl_add_u64 v[22:23], s[20:21], 0, v[22:23]
	v_mov_b32_e32 v19, 0
	v_lshl_add_u64 v[22:23], v[22:23], 0, v[18:19]
	s_or_b64 exec, exec, s[6:7]
	s_lshl_b32 s38, s10, 10
	v_or_b32_e32 v19, s38, v21
	s_add_i32 s11, s33, 24
	v_readfirstlane_b32 s6, v19
	s_mov_b32 m0, s6
	v_lshl_or_b32 v19, s11, 3, v24
	global_load_lds_dwordx4 v[22:23], off
	s_mov_b32 s10, 0x3c3c3c3d
	v_mul_hi_u32 v22, v19, s10
	v_lshrrev_b32_e32 v22, 3, v22
	v_mul_lo_u32 v23, v22, s8
	v_add_u32_e32 v60, s12, v22
	v_add3_u32 v61, s13, v19, v23
	v_cmp_gt_u32_e64 s[6:7], s9, v19
	v_cmp_gt_u32_e64 s[8:9], 64, v60
	s_and_b64 s[8:9], s[6:7], s[8:9]
	v_cmp_gt_u32_e64 s[6:7], 64, v61
	s_and_b64 s[6:7], s[8:9], s[6:7]
	v_mov_b64_e32 v[22:23], s[18:19]
	s_and_saveexec_b64 s[8:9], s[6:7]
	s_lshl_b32 s16, s25, 13
	v_lshlrev_b32_e32 v19, 6, v60
	v_or3_b32 v22, v19, s16, v61
	v_ashrrev_i32_e32 v23, 31, v22
	v_lshlrev_b64 v[22:23], 7, v[22:23]
	v_lshl_add_u64 v[22:23], s[20:21], 0, v[22:23]
	v_mov_b32_e32 v19, 0
	v_lshl_add_u64 v[22:23], v[22:23], 0, v[18:19]
	s_or_b64 exec, exec, s[8:9]
	s_lshl_b32 s39, s11, 10
	v_or_b32_e32 v19, s39, v21
	s_add_i32 s16, s33, 32
	v_readfirstlane_b32 s8, v19
	s_mov_b32 m0, s8
	v_lshl_or_b32 v19, s16, 3, v24
	global_load_lds_dwordx4 v[22:23], off
	v_mul_hi_u32 v22, v19, s10
	v_lshrrev_b32_e32 v22, 3, v22
	s_movk_i32 s8, 0xffde
	v_mul_lo_u32 v23, v22, s8
	v_add_u32_e32 v62, s12, v22
	s_movk_i32 s8, 0x154
	v_add3_u32 v63, s13, v19, v23
	v_cmp_gt_u32_e64 s[8:9], s8, v19
	v_cmp_gt_u32_e64 s[10:11], 64, v62
	s_and_b64 s[10:11], s[8:9], s[10:11]
	v_cmp_gt_u32_e64 s[8:9], 64, v63
	s_and_b64 s[8:9], s[10:11], s[8:9]
	s_xor_b64 s[10:11], s[8:9], -1
	s_and_saveexec_b64 s[28:29], s[10:11]
	s_xor_b64 s[10:11], exec, s[28:29]
	s_lshl_b32 s17, s25, 13
	s_or_saveexec_b64 s[10:11], s[10:11]
	v_mov_b32_e32 v64, s17
	v_mov_b64_e32 v[22:23], s[18:19]
	s_xor_b64 exec, exec, s[10:11]
	s_lshl_b32 s17, s25, 13
	v_lshlrev_b32_e32 v19, 6, v62
	v_or3_b32 v22, v19, s17, v63
	v_ashrrev_i32_e32 v23, 31, v22
	v_lshlrev_b64 v[22:23], 7, v[22:23]
	v_lshl_add_u64 v[22:23], s[20:21], 0, v[22:23]
	v_mov_b32_e32 v19, 0
	v_lshl_add_u64 v[22:23], v[22:23], 0, v[18:19]
	v_mov_b32_e32 v64, s17
	s_or_b64 exec, exec, s[10:11]
	s_lshl_b32 s40, s16, 10
	v_or_b32_e32 v18, s40, v21
	s_add_i32 s23, s33, 40
	v_readfirstlane_b32 s10, v18
	s_mov_b32 m0, s10
	v_lshl_or_b32 v19, s23, 3, v24
	global_load_lds_dwordx4 v[22:23], off
	s_mov_b32 s10, 0x3c3c3c3d
	v_mul_hi_u32 v18, v19, s10
	v_lshrrev_b32_e32 v18, 3, v18
	s_movk_i32 s10, 0xffde
	s_mov_b64 s[16:17], s[84:85]
	v_mul_lo_u32 v22, v18, s10
	v_add_u32_e32 v18, s12, v18
	s_movk_i32 s10, 0x154
	v_add3_u32 v65, s13, v19, v22
	v_cmp_gt_u32_e64 s[10:11], s10, v19
	v_cmp_gt_u32_e64 s[12:13], 64, v18
	s_and_b64 s[12:13], s[10:11], s[12:13]
	v_cmp_gt_u32_e64 s[10:11], 64, v65
	s_and_b64 s[10:11], s[12:13], s[10:11]
	s_xor_b64 s[12:13], s[10:11], -1
	v_lshlrev_b32_e32 v66, 6, v18
	s_and_saveexec_b64 s[28:29], s[12:13]
	s_xor_b64 s[12:13], exec, s[28:29]
	v_lshlrev_b32_e32 v66, 6, v18
	s_or_saveexec_b64 s[12:13], s[12:13]
	v_mov_b64_e32 v[18:19], s[18:19]
	s_xor_b64 exec, exec, s[12:13]
	v_or3_b32 v18, v66, v64, v65
	v_ashrrev_i32_e32 v19, 31, v18
	v_lshlrev_b64 v[18:19], 7, v[18:19]
	v_lshl_add_u64 v[18:19], s[20:21], 0, v[18:19]
	v_lshlrev_b32_e32 v22, 1, v20
	v_mov_b32_e32 v23, 0
	v_lshl_add_u64 v[18:19], v[18:19], 0, v[22:23]
	s_or_b64 exec, exec, s[12:13]
	v_lshrrev_b32_e32 v129, 4, v1
	v_bitop3_b32 v23, v129, v0, 6 bitop3:0x78
	v_and_b32_e32 v128, 15, v0
	v_lshlrev_b32_e32 v23, 4, v23
	s_lshr_b32 s29, s27, 8
	v_lshl_or_b32 v23, v128, 7, v23
	v_lshl_or_b32 v23, s29, 13, v23
	s_lshl_b32 s41, s23, 10
	s_lshl_b32 s26, s22, 6
	s_and_b32 s28, s33, 3
	v_add_u32_e32 v132, 0x18000, v23
	v_or_b32_e32 v23, s41, v21
	s_lshl_b32 s22, s22, 13
	v_readfirstlane_b32 s23, v23
	s_waitcnt lgkmcnt(0)
	s_add_u32 s22, s16, s22
	s_mul_hi_u32 s44, s27, 0x38e38e39
	s_mov_b32 m0, s23
	s_addc_u32 s23, s17, 0
	s_lshr_b32 s16, s44, 10
	s_mul_i32 s16, s16, -9
	s_add_i32 s16, s16, s29
	s_lshl_b32 s34, s33, 11
	s_ashr_i32 s17, s16, 31
	s_add_i32 s33, s34, 0x18000
	s_lshl_b64 s[16:17], s[16:17], 15
	s_add_u32 s16, s22, s16
	s_addc_u32 s17, s23, s17
	s_add_i32 s42, s29, 2
	s_mul_hi_u32 s43, s42, 0xe38e38f
	v_lshl_or_b32 v22, v24, 6, s36
	s_movk_i32 s31, 0xdc0
	s_mul_i32 s43, s43, -9
	v_and_or_b32 v22, v22, s31, v20
	s_add_i32 s42, s43, s42
	global_load_lds_dwordx4 v[18:19], off
	v_lshlrev_b32_e32 v18, 1, v22
	v_mov_b32_e32 v19, 0
	s_mov_b32 m0, s33
	s_ashr_i32 s43, s42, 31
	v_lshl_add_u64 v[22:23], s[16:17], 0, v[18:19]
	global_load_lds_dwordx4 v18, s[16:17]
	s_mov_b64 s[16:17], 0x400
	s_add_i32 m0, s34, 0x18400
	s_lshl_b64 s[42:43], s[42:43], 15
	v_lshl_add_u64 v[22:23], v[22:23], 0, s[16:17]
	s_add_u32 s42, s22, s42
	global_load_lds_dwordx4 v[22:23], off
	s_addc_u32 s43, s23, s43
	s_add_i32 m0, s34, 0x1c000
	v_lshl_add_u64 v[22:23], s[42:43], 0, v[18:19]
	global_load_lds_dwordx4 v18, s[42:43]
	s_add_i32 s42, s29, 4
	s_mul_hi_u32 s43, s42, 0xe38e38f
	s_mul_i32 s43, s43, -9
	s_add_i32 s42, s43, s42
	s_ashr_i32 s43, s42, 31
	s_add_i32 m0, s34, 0x1c400
	s_lshl_b64 s[42:43], s[42:43], 15
	s_add_u32 s42, s22, s42
	v_lshl_add_u64 v[22:23], v[22:23], 0, s[16:17]
	s_addc_u32 s43, s23, s43
	global_load_lds_dwordx4 v[22:23], off
	s_add_i32 m0, s34, 0x20000
	v_lshl_add_u64 v[22:23], s[42:43], 0, v[18:19]
	global_load_lds_dwordx4 v18, s[42:43]
	v_lshl_add_u64 v[22:23], v[22:23], 0, s[16:17]
	s_add_i32 m0, s34, 0x20400
	s_lshr_b32 s34, s44, 9
	global_load_lds_dwordx4 v[22:23], off
	s_mul_i32 s34, s34, -9
	s_add_i32 s34, s34, s29
	s_mul_hi_i32 s42, s34, 0x55555556
	s_lshr_b32 s43, s42, 31
	s_mul_i32 s31, s28, 0x44
	s_add_i32 s42, s42, s43
	v_add_u32_e32 v130, s31, v128
	s_mul_i32 s42, s42, 31
	v_add_u32_e32 v131, 34, v130
	s_add_i32 s42, s42, s34
	s_bitcmp1_b32 s44, 9
	v_add_u32_e32 v30, s42, v130
	v_add_u32_e32 v38, s42, v131
	s_movk_i32 s42, 0x1000
	v_lshlrev_b32_e32 v68, 1, v20
	v_lshl_add_u32 v20, v48, 6, v64
	s_waitcnt vmcnt(4) lgkmcnt(0)
	s_barrier
	s_cselect_b32 s43, 0xc000, 0
	ds_read_b128 v[26:29], v132
	v_add3_u32 v48, v20, v49, s42
	v_lshl_add_u32 v20, v58, 6, v64
	ds_read_b128 v[22:25], v132 offset:2048
	v_bitop3_b32 v31, v30, v129, 6 bitop3:0x6c
	v_lshl_add_u32 v30, v30, 7, s43
	v_add3_u32 v58, v20, v59, s42
	v_lshl_add_u32 v20, v60, 6, v64
	v_lshl_or_b32 v134, v31, 4, v30
	ds_read_b128 v[34:37], v134
	v_lshl_add_u32 v46, v46, 6, v64
	v_add3_u32 v60, v20, v61, s42
	v_lshl_add_u32 v20, v62, 6, v64
	ds_read_b128 v[30:33], v134 offset:2048
	v_bitop3_b32 v39, v38, v129, 6 bitop3:0x6c
	v_lshl_add_u32 v38, v38, 7, s43
	v_add3_u32 v46, v46, v47, s42
	v_add3_u32 v62, v20, v63, s42
	v_add_u32_e32 v20, v66, v64
	v_lshl_add_u64 v[126:127], s[22:23], 0, v[18:19]
	v_add_u32_e32 v18, s36, v21
	v_lshl_or_b32 v135, v39, 4, v38
	ds_read_b128 v[42:45], v135
	v_ashrrev_i32_e32 v47, 31, v46
	v_add3_u32 v64, v20, v65, s42
	v_add_u32_e32 v136, 0xc000, v18
	v_add_u32_e32 v18, s37, v21
	s_load_dwordx2 s[12:13], s[0:1], 0x20
	ds_read_b128 v[38:41], v135 offset:2048
	v_lshlrev_b64 v[46:47], 7, v[46:47]
	v_ashrrev_i32_e32 v49, 31, v48
	v_ashrrev_i32_e32 v59, 31, v58
	v_ashrrev_i32_e32 v61, 31, v60
	v_ashrrev_i32_e32 v63, 31, v62
	v_ashrrev_i32_e32 v65, 31, v64
	v_add_u32_e32 v137, 0xc000, v18
	v_add_u32_e32 v18, s38, v21
	ds_read_b128 v[54:57], v132 offset:4096
	v_lshl_add_u64 v[46:47], s[20:21], 0, v[46:47]
	v_mov_b32_e32 v69, v19
	v_lshlrev_b64 v[48:49], 7, v[48:49]
	v_lshlrev_b64 v[58:59], 7, v[58:59]
	v_lshlrev_b64 v[60:61], 7, v[60:61]
	v_lshlrev_b64 v[62:63], 7, v[62:63]
	v_lshlrev_b64 v[64:65], 7, v[64:65]
	v_add_u32_e32 v138, 0xc000, v18
	v_add_u32_e32 v18, s39, v21
	ds_read_b128 v[50:53], v132 offset:6144
	v_lshl_add_u64 v[46:47], v[46:47], 0, v[68:69]
	v_lshl_add_u64 v[48:49], s[20:21], 0, v[48:49]
	v_lshl_add_u64 v[58:59], s[20:21], 0, v[58:59]
	v_lshl_add_u64 v[60:61], s[20:21], 0, v[60:61]
	v_lshl_add_u64 v[62:63], s[20:21], 0, v[62:63]
	v_lshl_add_u64 v[64:65], s[20:21], 0, v[64:65]
	v_mov_b32_e32 v20, s19
	v_add_u32_e32 v139, 0xc000, v18
	v_add_u32_e32 v18, s40, v21
	v_lshl_add_u64 v[48:49], v[48:49], 0, v[68:69]
	v_lshl_add_u64 v[58:59], v[58:59], 0, v[68:69]
	v_lshl_add_u64 v[60:61], v[60:61], 0, v[68:69]
	v_lshl_add_u64 v[62:63], v[62:63], 0, v[68:69]
	v_lshl_add_u64 v[64:65], v[64:65], 0, v[68:69]
	v_cndmask_b32_e32 v115, v20, v47, vcc
	v_mov_b32_e32 v47, s18
	v_add_u32_e32 v140, 0xc000, v18
	v_add_u32_e32 v18, s41, v21
	s_mov_b32 s30, 6
	v_xor_b32_e32 v133, 64, v132
	s_mov_b32 s31, 0
	s_mov_b32 s35, 1
	s_mov_b32 s34, 0xc000
	v_cndmask_b32_e32 v114, v47, v46, vcc
	v_cndmask_b32_e64 v117, v20, v49, s[2:3]
	v_cndmask_b32_e64 v116, v47, v48, s[2:3]
	v_cndmask_b32_e64 v119, v20, v59, s[4:5]
	v_cndmask_b32_e64 v118, v47, v58, s[4:5]
	v_cndmask_b32_e64 v121, v20, v61, s[6:7]
	v_cndmask_b32_e64 v120, v47, v60, s[6:7]
	v_cndmask_b32_e64 v123, v20, v63, s[8:9]
	v_cndmask_b32_e64 v122, v47, v62, s[8:9]
	v_cndmask_b32_e64 v125, v20, v65, s[10:11]
	v_cndmask_b32_e64 v124, v47, v64, s[10:11]
	s_mov_b64 s[2:3], 0
	v_add_u32_e32 v141, 0xc000, v18
	v_mov_b32_e32 v18, v19
	v_mov_b32_e32 v20, v19
	v_mov_b32_e32 v21, v19
	v_mov_b32_e32 v46, v19
	v_mov_b32_e32 v47, v19
	v_mov_b32_e32 v48, v19
	v_mov_b32_e32 v49, v19
	v_mov_b32_e32 v58, v19
	v_mov_b32_e32 v59, v19
	v_mov_b32_e32 v60, v19
	v_mov_b32_e32 v61, v19
	v_mov_b32_e32 v74, v19
	v_mov_b32_e32 v75, v19
	v_mov_b32_e32 v76, v19
	v_mov_b32_e32 v77, v19
	v_mov_b32_e32 v82, v19
	v_mov_b32_e32 v83, v19
	v_mov_b32_e32 v84, v19
	v_mov_b32_e32 v85, v19
	v_mov_b32_e32 v86, v19
	v_mov_b32_e32 v87, v19
	v_mov_b32_e32 v88, v19
	v_mov_b32_e32 v89, v19
	v_mov_b32_e32 v90, v19
	v_mov_b32_e32 v91, v19
	v_mov_b32_e32 v92, v19
	v_mov_b32_e32 v93, v19
	v_mov_b32_e32 v94, v19
	v_mov_b32_e32 v95, v19
	v_mov_b32_e32 v96, v19
	v_mov_b32_e32 v97, v19
	v_mov_b32_e32 v98, v19
	v_mov_b32_e32 v99, v19
	v_mov_b32_e32 v100, v19
	v_mov_b32_e32 v101, v19
	v_mov_b32_e32 v102, v19
	v_mov_b32_e32 v103, v19
	v_mov_b32_e32 v104, v19
	v_mov_b32_e32 v105, v19
	v_mov_b32_e32 v106, v19
	v_mov_b32_e32 v107, v19
	v_mov_b32_e32 v108, v19
	v_mov_b32_e32 v109, v19
	v_mov_b32_e32 v110, v19
	v_mov_b32_e32 v111, v19
	v_mov_b32_e32 v112, v19
	v_mov_b32_e32 v113, v19
	v_mov_b32_e32 v78, v19
	v_mov_b32_e32 v79, v19
	v_mov_b32_e32 v80, v19
	v_mov_b32_e32 v81, v19
	v_mov_b32_e32 v62, v19
	v_mov_b32_e32 v63, v19
	v_mov_b32_e32 v64, v19
	v_mov_b32_e32 v65, v19
	v_mov_b32_e32 v70, v19
	v_mov_b32_e32 v71, v19
	v_mov_b32_e32 v72, v19
	v_mov_b32_e32 v73, v19
	v_mov_b32_e32 v66, v19
	v_mov_b32_e32 v67, v19
	v_mov_b32_e32 v68, v19
	s_mov_b32 s60, 0
	s_add_i32 s63, s29, 2
	s_mul_i32 s73, s63, 11
	s_lshr_b32 s73, s73, 5
	s_mul_i32 s73, s73, 31
	s_add_i32 s62, s63, s73
	s_mov_b32 s64, 0
	s_mov_b32 s66, 1
	s_mov_b32 s67, 0
	s_add_i32 s75, s29, 6
	s_lshl_b32 s68, s75, 15
	s_mov_b32 s69, 0
	v_lshl_add_u64 v[178:179], v[126:127], 0, s[68:69]
	s_add_i32 s70, s33, 0xc000
	v_lshl_add_u64 v[180:181], v[178:179], 0, s[16:17]
	v_mov_b32_e32 v174, v133

.LBB5_28:
	s_cmpk_gt_u32 s27, 0xff
	s_waitcnt vmcnt(0) lgkmcnt(0)
	s_barrier
	s_cbranch_scc1 .LBB5_30
	ds_read_b128 v[22:25], v1
	ds_read_b128 v[26:29], v1 offset:1024
	ds_read_b128 v[30:33], v1 offset:2048
	ds_read_b128 v[40:43], v1 offset:14336
	s_mov_b32 s0, s88
	s_waitcnt lgkmcnt(0)
	v_pk_add_f32 v[50:51], v[24:25], v[112:113]
	v_pk_add_f32 v[52:53], v[22:23], v[110:111]
	ds_read_b128 v[22:25], v1 offset:3072
	v_pk_add_f32 v[54:55], v[28:29], v[108:109]
	v_pk_add_f32 v[56:57], v[26:27], v[106:107]
	v_pk_add_f32 v[104:105], v[32:33], v[104:105]
	ds_read_b128 v[26:29], v1 offset:4096
	v_pk_add_f32 v[102:103], v[30:31], v[102:103]
	ds_read_b128 v[30:33], v1 offset:5120
	s_waitcnt lgkmcnt(2)
	v_pk_add_f32 v[100:101], v[24:25], v[100:101]
	v_pk_add_f32 v[98:99], v[22:23], v[98:99]
	ds_read_b128 v[22:25], v1 offset:6144
	s_waitcnt lgkmcnt(2)
	v_pk_add_f32 v[96:97], v[28:29], v[96:97]
	v_pk_add_f32 v[94:95], v[26:27], v[94:95]
	s_waitcnt lgkmcnt(1)
	v_pk_add_f32 v[92:93], v[32:33], v[92:93]
	ds_read_b128 v[26:29], v1 offset:7168
	v_pk_add_f32 v[90:91], v[30:31], v[90:91]
	ds_read_b128 v[30:33], v1 offset:8192
	s_waitcnt lgkmcnt(2)
	v_pk_add_f32 v[88:89], v[24:25], v[88:89]
	v_pk_add_f32 v[86:87], v[22:23], v[86:87]
	ds_read_b128 v[22:25], v1 offset:9216
	s_waitcnt lgkmcnt(2)
	v_pk_add_f32 v[84:85], v[28:29], v[84:85]
	v_pk_add_f32 v[82:83], v[26:27], v[82:83]
	s_waitcnt lgkmcnt(1)
	v_pk_add_f32 v[76:77], v[32:33], v[76:77]
	ds_read_b128 v[26:29], v1 offset:10240
	v_pk_add_f32 v[74:75], v[30:31], v[74:75]
	ds_read_b128 v[30:33], v1 offset:11264
	s_waitcnt lgkmcnt(2)
	v_pk_add_f32 v[60:61], v[24:25], v[60:61]
	v_pk_add_f32 v[58:59], v[22:23], v[58:59]
	ds_read_b128 v[22:25], v1 offset:12288
	s_and_b32 s1, s27, 0xc0
	s_waitcnt lgkmcnt(2)
	v_pk_add_f32 v[38:39], v[28:29], v[48:49]
	v_pk_add_f32 v[48:49], v[26:27], v[46:47]
	s_waitcnt lgkmcnt(1)
	v_pk_add_f32 v[32:33], v[32:33], v[20:21]
	v_pk_add_f32 v[36:37], v[30:31], v[18:19]
	ds_read_b128 v[18:21], v1 offset:13312
	ds_read_b128 v[44:47], v1 offset:15360
	v_or_b32_e32 v1, s1, v128
	s_waitcnt lgkmcnt(2)
	v_pk_add_f32 v[28:29], v[24:25], v[80:81]
	v_pk_add_f32 v[24:25], v[40:41], v[70:71]
	v_lshlrev_b32_e32 v40, 3, v129
	v_mul_u32_u24_e32 v1, 0x90, v1
	s_mov_b32 s1, 0x10000
	v_add3_u32 v1, v1, v40, s1
	v_pk_fma_f32 v[40:41], s[0:1], v[52:53], v[14:15] op_sel_hi:[0,1,1]
	v_pk_add_f32 v[34:35], v[22:23], v[78:79]
	v_pk_add_f32 v[22:23], v[42:43], v[72:73]
	v_pk_mul_f32 v[42:43], s[14:15], v[40:41] op_sel_hi:[0,1]
	v_cmp_le_f32_e32 vcc, 0, v41
	s_waitcnt lgkmcnt(1)
	v_pk_add_f32 v[26:27], v[20:21], v[64:65]
	s_waitcnt lgkmcnt(0)
	v_pk_add_f32 v[20:21], v[44:45], v[66:67]
	v_cndmask_b32_e32 v41, v43, v41, vcc
	v_cmp_le_f32_e32 vcc, 0, v40
	v_pk_add_f32 v[30:31], v[18:19], v[62:63]
	v_pk_add_f32 v[18:19], v[46:47], v[68:69]
	v_cndmask_b32_e32 v40, v42, v40, vcc
	v_pk_fma_f32 v[42:43], s[0:1], v[50:51], v[16:17] op_sel_hi:[0,1,1]
	v_pk_mul_f32 v[44:45], s[14:15], v[42:43] op_sel_hi:[0,1]
	v_cmp_le_f32_e32 vcc, 0, v43
	v_cvt_pk_f16_f32 v40, v40, v41
	v_add_u32_e32 v50, 0x800, v1
	v_cndmask_b32_e32 v41, v45, v43, vcc
	v_cmp_le_f32_e32 vcc, 0, v42
	v_pk_fma_f32 v[38:39], s[0:1], v[38:39], v[8:9] op_sel_hi:[0,1,1]
	v_pk_fma_f32 v[36:37], s[0:1], v[36:37], v[2:3] op_sel_hi:[0,1,1]
	v_cndmask_b32_e32 v42, v44, v42, vcc
	v_cvt_pk_f16_f32 v41, v42, v41
	v_pk_fma_f32 v[42:43], s[0:1], v[56:57], v[10:11] op_sel_hi:[0,1,1]
	v_pk_mul_f32 v[44:45], s[14:15], v[42:43] op_sel_hi:[0,1]
	v_cmp_le_f32_e32 vcc, 0, v43
	v_pk_fma_f32 v[32:33], s[0:1], v[32:33], v[4:5] op_sel_hi:[0,1,1]
	s_nop 0
	v_cndmask_b32_e32 v43, v45, v43, vcc
	v_cmp_le_f32_e32 vcc, 0, v42
	s_nop 1
	v_cndmask_b32_e32 v42, v44, v42, vcc
	v_pk_fma_f32 v[44:45], s[0:1], v[54:55], v[12:13] op_sel_hi:[0,1,1]
	v_pk_mul_f32 v[46:47], s[14:15], v[44:45] op_sel_hi:[0,1]
	v_cmp_le_f32_e32 vcc, 0, v45
	v_cvt_pk_f16_f32 v42, v42, v43
	s_nop 0
	v_cndmask_b32_e32 v43, v47, v45, vcc
	v_cmp_le_f32_e32 vcc, 0, v44
	s_nop 1
	v_cndmask_b32_e32 v44, v46, v44, vcc
	v_cvt_pk_f16_f32 v43, v44, v43
	ds_write2_b64 v1, v[40:41], v[42:43] offset1:4
	v_pk_fma_f32 v[40:41], s[0:1], v[102:103], v[6:7] op_sel_hi:[0,1,1]
	v_pk_mul_f32 v[42:43], s[14:15], v[40:41] op_sel_hi:[0,1]
	v_cmp_le_f32_e32 vcc, 0, v41
	s_nop 1
	v_cndmask_b32_e32 v41, v43, v41, vcc
	v_cmp_le_f32_e32 vcc, 0, v40
	s_nop 1
	v_cndmask_b32_e32 v40, v42, v40, vcc
	v_pk_fma_f32 v[42:43], s[0:1], v[104:105], v[8:9] op_sel_hi:[0,1,1]
	v_pk_mul_f32 v[44:45], s[14:15], v[42:43] op_sel_hi:[0,1]
	v_cmp_le_f32_e32 vcc, 0, v43
	v_cvt_pk_f16_f32 v40, v40, v41
	s_nop 0
	v_cndmask_b32_e32 v41, v45, v43, vcc
	v_cmp_le_f32_e32 vcc, 0, v42
	s_nop 1
	v_cndmask_b32_e32 v42, v44, v42, vcc
	v_cvt_pk_f16_f32 v41, v42, v41
	v_pk_fma_f32 v[42:43], s[0:1], v[98:99], v[2:3] op_sel_hi:[0,1,1]
	v_pk_mul_f32 v[44:45], s[14:15], v[42:43] op_sel_hi:[0,1]
	v_cmp_le_f32_e32 vcc, 0, v43
	s_nop 1
	v_cndmask_b32_e32 v43, v45, v43, vcc
	v_cmp_le_f32_e32 vcc, 0, v42
	s_nop 1
	v_cndmask_b32_e32 v42, v44, v42, vcc
	v_pk_fma_f32 v[44:45], s[0:1], v[100:101], v[4:5] op_sel_hi:[0,1,1]
	v_pk_mul_f32 v[46:47], s[14:15], v[44:45] op_sel_hi:[0,1]
	v_cmp_le_f32_e32 vcc, 0, v45
	v_cvt_pk_f16_f32 v42, v42, v43
	s_nop 0
	v_cndmask_b32_e32 v43, v47, v45, vcc
	v_cmp_le_f32_e32 vcc, 0, v44
	s_nop 1
	v_cndmask_b32_e32 v44, v46, v44, vcc
	v_cvt_pk_f16_f32 v43, v44, v43
	ds_write2_b64 v1, v[40:41], v[42:43] offset0:8 offset1:12
	v_pk_fma_f32 v[40:41], s[0:1], v[94:95], v[14:15] op_sel_hi:[0,1,1]
	v_pk_mul_f32 v[42:43], s[14:15], v[40:41] op_sel_hi:[0,1]
	v_cmp_le_f32_e32 vcc, 0, v41
	s_nop 1
	v_cndmask_b32_e32 v41, v43, v41, vcc
	v_cmp_le_f32_e32 vcc, 0, v40
	s_nop 1
	v_cndmask_b32_e32 v40, v42, v40, vcc
	v_pk_fma_f32 v[42:43], s[0:1], v[96:97], v[16:17] op_sel_hi:[0,1,1]
	v_pk_mul_f32 v[44:45], s[14:15], v[42:43] op_sel_hi:[0,1]
	v_cmp_le_f32_e32 vcc, 0, v43
	v_cvt_pk_f16_f32 v40, v40, v41
	s_nop 0
	v_cndmask_b32_e32 v41, v45, v43, vcc
	v_cmp_le_f32_e32 vcc, 0, v42
	s_nop 1
	v_cndmask_b32_e32 v42, v44, v42, vcc
	v_cvt_pk_f16_f32 v41, v42, v41
	v_pk_fma_f32 v[42:43], s[0:1], v[90:91], v[10:11] op_sel_hi:[0,1,1]
	v_pk_mul_f32 v[44:45], s[14:15], v[42:43] op_sel_hi:[0,1]
	v_cmp_le_f32_e32 vcc, 0, v43
	s_nop 1
	v_cndmask_b32_e32 v43, v45, v43, vcc
	v_cmp_le_f32_e32 vcc, 0, v42
	s_nop 1
	v_cndmask_b32_e32 v42, v44, v42, vcc
	v_pk_fma_f32 v[44:45], s[0:1], v[92:93], v[12:13] op_sel_hi:[0,1,1]
	v_pk_mul_f32 v[46:47], s[14:15], v[44:45] op_sel_hi:[0,1]
	v_cmp_le_f32_e32 vcc, 0, v45
	v_cvt_pk_f16_f32 v42, v42, v43
	s_nop 0
	v_cndmask_b32_e32 v43, v47, v45, vcc
	v_cmp_le_f32_e32 vcc, 0, v44
	s_nop 1
	v_cndmask_b32_e32 v44, v46, v44, vcc
	v_cvt_pk_f16_f32 v43, v44, v43
	ds_write2_b64 v50, v[40:41], v[42:43] offset0:32 offset1:36
	v_pk_fma_f32 v[40:41], s[0:1], v[86:87], v[6:7] op_sel_hi:[0,1,1]
	v_pk_mul_f32 v[42:43], s[14:15], v[40:41] op_sel_hi:[0,1]
	v_cmp_le_f32_e32 vcc, 0, v41
	s_nop 1
	v_cndmask_b32_e32 v41, v43, v41, vcc
	v_cmp_le_f32_e32 vcc, 0, v40
	s_nop 1
	v_cndmask_b32_e32 v40, v42, v40, vcc
	v_pk_fma_f32 v[42:43], s[0:1], v[88:89], v[8:9] op_sel_hi:[0,1,1]
	v_pk_mul_f32 v[44:45], s[14:15], v[42:43] op_sel_hi:[0,1]
	v_cmp_le_f32_e32 vcc, 0, v43
	v_cvt_pk_f16_f32 v40, v40, v41
	v_pk_fma_f32 v[8:9], s[0:1], v[22:23], v[8:9] op_sel_hi:[0,1,1]
	v_cndmask_b32_e32 v41, v45, v43, vcc
	v_cmp_le_f32_e32 vcc, 0, v42
	s_nop 1
	v_cndmask_b32_e32 v42, v44, v42, vcc
	v_cvt_pk_f16_f32 v41, v42, v41
	v_pk_fma_f32 v[42:43], s[0:1], v[82:83], v[2:3] op_sel_hi:[0,1,1]
	v_pk_mul_f32 v[44:45], s[14:15], v[42:43] op_sel_hi:[0,1]
	v_cmp_le_f32_e32 vcc, 0, v43
	v_pk_fma_f32 v[2:3], s[0:1], v[20:21], v[2:3] op_sel_hi:[0,1,1]
	s_nop 0
	v_cndmask_b32_e32 v43, v45, v43, vcc
	v_cmp_le_f32_e32 vcc, 0, v42
	s_nop 1
	v_cndmask_b32_e32 v42, v44, v42, vcc
	v_pk_fma_f32 v[44:45], s[0:1], v[84:85], v[4:5] op_sel_hi:[0,1,1]
	v_pk_mul_f32 v[46:47], s[14:15], v[44:45] op_sel_hi:[0,1]
	v_cmp_le_f32_e32 vcc, 0, v45
	v_cvt_pk_f16_f32 v42, v42, v43
	v_pk_fma_f32 v[4:5], s[0:1], v[18:19], v[4:5] op_sel_hi:[0,1,1]
	v_cndmask_b32_e32 v43, v47, v45, vcc
	v_cmp_le_f32_e32 vcc, 0, v44
	s_nop 1
	v_cndmask_b32_e32 v44, v46, v44, vcc
	v_cvt_pk_f16_f32 v43, v44, v43
	ds_write2_b64 v50, v[40:41], v[42:43] offset0:40 offset1:44
	v_pk_fma_f32 v[40:41], s[0:1], v[74:75], v[14:15] op_sel_hi:[0,1,1]
	v_pk_mul_f32 v[42:43], s[14:15], v[40:41] op_sel_hi:[0,1]
	v_cmp_le_f32_e32 vcc, 0, v41
	v_pk_fma_f32 v[14:15], s[0:1], v[34:35], v[14:15] op_sel_hi:[0,1,1]
	s_nop 0
	v_cndmask_b32_e32 v41, v43, v41, vcc
	v_cmp_le_f32_e32 vcc, 0, v40
	s_nop 1
	v_cndmask_b32_e32 v40, v42, v40, vcc
	v_pk_fma_f32 v[42:43], s[0:1], v[76:77], v[16:17] op_sel_hi:[0,1,1]
	v_pk_mul_f32 v[44:45], s[14:15], v[42:43] op_sel_hi:[0,1]
	v_cmp_le_f32_e32 vcc, 0, v43
	v_cvt_pk_f16_f32 v40, v40, v41
	v_pk_fma_f32 v[16:17], s[0:1], v[28:29], v[16:17] op_sel_hi:[0,1,1]
	v_cndmask_b32_e32 v41, v45, v43, vcc
	v_cmp_le_f32_e32 vcc, 0, v42
	v_pk_mul_f32 v[28:29], s[14:15], v[16:17] op_sel_hi:[0,1]
	s_nop 0
	v_cndmask_b32_e32 v42, v44, v42, vcc
	v_cvt_pk_f16_f32 v41, v42, v41
	v_pk_fma_f32 v[42:43], s[0:1], v[58:59], v[10:11] op_sel_hi:[0,1,1]
	v_pk_mul_f32 v[44:45], s[14:15], v[42:43] op_sel_hi:[0,1]
	v_cmp_le_f32_e32 vcc, 0, v43
	v_pk_fma_f32 v[10:11], s[0:1], v[30:31], v[10:11] op_sel_hi:[0,1,1]
	s_nop 0
	v_cndmask_b32_e32 v43, v45, v43, vcc
	v_cmp_le_f32_e32 vcc, 0, v42
	s_nop 1
	v_cndmask_b32_e32 v42, v44, v42, vcc
	v_pk_fma_f32 v[44:45], s[0:1], v[60:61], v[12:13] op_sel_hi:[0,1,1]
	v_pk_mul_f32 v[46:47], s[14:15], v[44:45] op_sel_hi:[0,1]
	v_cmp_le_f32_e32 vcc, 0, v45
	v_cvt_pk_f16_f32 v42, v42, v43
	v_pk_fma_f32 v[12:13], s[0:1], v[26:27], v[12:13] op_sel_hi:[0,1,1]
	v_cndmask_b32_e32 v43, v47, v45, vcc
	v_cmp_le_f32_e32 vcc, 0, v44
	s_nop 1
	v_cndmask_b32_e32 v44, v46, v44, vcc
	v_cvt_pk_f16_f32 v43, v44, v43
	v_add_u32_e32 v44, 0x1000, v1
	ds_write2_b64 v44, v[40:41], v[42:43] offset0:64 offset1:68
	v_pk_fma_f32 v[40:41], s[0:1], v[48:49], v[6:7] op_sel_hi:[0,1,1]
	v_pk_mul_f32 v[42:43], s[14:15], v[40:41] op_sel_hi:[0,1]
	v_cmp_le_f32_e32 vcc, 0, v41
	v_add_u32_e32 v1, 0x1800, v1
	v_pk_fma_f32 v[6:7], s[0:1], v[24:25], v[6:7] op_sel_hi:[0,1,1]
	v_cndmask_b32_e32 v41, v43, v41, vcc
	v_cmp_le_f32_e32 vcc, 0, v40
	s_nop 1
	v_cndmask_b32_e32 v40, v42, v40, vcc
	v_pk_mul_f32 v[42:43], s[14:15], v[38:39] op_sel_hi:[0,1]
	v_cmp_le_f32_e32 vcc, 0, v39
	v_cvt_pk_f16_f32 v40, v40, v41
	s_nop 0
	v_cndmask_b32_e32 v39, v43, v39, vcc
	v_cmp_le_f32_e32 vcc, 0, v38
	s_nop 1
	v_cndmask_b32_e32 v38, v42, v38, vcc
	v_cvt_pk_f16_f32 v41, v38, v39
	v_pk_mul_f32 v[38:39], s[14:15], v[36:37] op_sel_hi:[0,1]
	v_cmp_le_f32_e32 vcc, 0, v37
	s_nop 1
	v_cndmask_b32_e32 v37, v39, v37, vcc
	v_cmp_le_f32_e32 vcc, 0, v36
	s_nop 1
	v_cndmask_b32_e32 v36, v38, v36, vcc
	v_pk_mul_f32 v[38:39], s[14:15], v[32:33] op_sel_hi:[0,1]
	v_cmp_le_f32_e32 vcc, 0, v33
	v_cvt_pk_f16_f32 v36, v36, v37
	s_nop 0
	v_cndmask_b32_e32 v33, v39, v33, vcc
	v_cmp_le_f32_e32 vcc, 0, v32
	s_nop 1
	v_cndmask_b32_e32 v32, v38, v32, vcc
	v_cvt_pk_f16_f32 v37, v32, v33
	v_pk_mul_f32 v[32:33], s[14:15], v[14:15] op_sel_hi:[0,1]
	v_cmp_le_f32_e32 vcc, 0, v15
	ds_write2_b64 v44, v[40:41], v[36:37] offset0:72 offset1:76
	s_nop 0
	v_cndmask_b32_e32 v15, v33, v15, vcc
	v_cmp_le_f32_e32 vcc, 0, v14
	s_nop 1
	v_cndmask_b32_e32 v14, v32, v14, vcc
	v_cmp_le_f32_e32 vcc, 0, v17
	v_cvt_pk_f16_f32 v14, v14, v15
	s_nop 0
	v_cndmask_b32_e32 v15, v29, v17, vcc
	v_cmp_le_f32_e32 vcc, 0, v16
	s_nop 1
	v_cndmask_b32_e32 v16, v28, v16, vcc
	v_cvt_pk_f16_f32 v15, v16, v15
	v_pk_mul_f32 v[16:17], s[14:15], v[10:11] op_sel_hi:[0,1]
	v_cmp_le_f32_e32 vcc, 0, v11
	s_nop 1
	v_cndmask_b32_e32 v11, v17, v11, vcc
	v_cmp_le_f32_e32 vcc, 0, v10
	s_nop 1
	v_cndmask_b32_e32 v10, v16, v10, vcc
	v_pk_mul_f32 v[16:17], s[14:15], v[12:13] op_sel_hi:[0,1]
	v_cmp_le_f32_e32 vcc, 0, v13
	v_cvt_pk_f16_f32 v10, v10, v11
	s_nop 0
	v_cndmask_b32_e32 v11, v17, v13, vcc
	v_cmp_le_f32_e32 vcc, 0, v12
	s_nop 1
	v_cndmask_b32_e32 v12, v16, v12, vcc
	v_cvt_pk_f16_f32 v11, v12, v11
	ds_write2_b64 v1, v[14:15], v[10:11] offset0:96 offset1:100
	v_pk_mul_f32 v[10:11], s[14:15], v[6:7] op_sel_hi:[0,1]
	v_cmp_le_f32_e32 vcc, 0, v7
	s_nop 1
	v_cndmask_b32_e32 v7, v11, v7, vcc
	v_cmp_le_f32_e32 vcc, 0, v6
	s_nop 1
	v_cndmask_b32_e32 v6, v10, v6, vcc
	v_pk_mul_f32 v[10:11], s[14:15], v[8:9] op_sel_hi:[0,1]
	v_cmp_le_f32_e32 vcc, 0, v9
	v_cvt_pk_f16_f32 v6, v6, v7
	s_nop 0
	v_cndmask_b32_e32 v7, v11, v9, vcc
	v_cmp_le_f32_e32 vcc, 0, v8
	s_nop 1
	v_cndmask_b32_e32 v8, v10, v8, vcc
	v_cvt_pk_f16_f32 v7, v8, v7
	v_pk_mul_f32 v[8:9], s[14:15], v[2:3] op_sel_hi:[0,1]
	v_cmp_le_f32_e32 vcc, 0, v3
	s_nop 1
	v_cndmask_b32_e32 v3, v9, v3, vcc
	v_cmp_le_f32_e32 vcc, 0, v2
	s_nop 1
	v_cndmask_b32_e32 v2, v8, v2, vcc
	v_pk_mul_f32 v[8:9], s[14:15], v[4:5] op_sel_hi:[0,1]
	v_cmp_le_f32_e32 vcc, 0, v5
	v_cvt_pk_f16_f32 v2, v2, v3
	s_nop 0
	v_cndmask_b32_e32 v3, v9, v5, vcc
	v_cmp_le_f32_e32 vcc, 0, v4
	s_nop 1
	v_cndmask_b32_e32 v4, v8, v4, vcc
	v_cvt_pk_f16_f32 v3, v4, v3
	ds_write2_b64 v1, v[6:7], v[2:3] offset0:104 offset1:108

_Z6conv_kILi256ELi512ELi3ELi128ELi1ELi1ELb0EEvPKDF16_S1_PKfS3_PDF16_S4_S1_fS3_S3_S3_S3_:
	s_lshl_b32 s3, s2, 3
	s_load_dwordx2 s[36:37], s[0:1], 0x0
	s_load_dword s88, s[0:1], 0x38
	s_load_dwordx2 s[84:85], s[0:1], 0x8
	s_load_dwordx4 s[4:7], s[0:1], 0x10
	s_load_dwordx2 s[30:31], s[0:1], 0x30
	s_and_b32 s3, s3, 56
	s_ashr_i32 s8, s2, 5
	s_add_i32 s3, s3, s8
	v_readfirstlane_b32 s40, v0
	s_lshl_b32 s8, s3, 2
	s_bfe_u32 s49, s2, 0x20003
	s_and_b32 s33, s8, 56
	s_lshr_b32 s50, s40, 6
	s_bfe_u32 s41, s40, 0x10006
	s_ashr_i32 s38, s3, 4
	s_and_b32 s27, s2, 32
	s_lshl_b32 s2, s49, 9
	s_waitcnt lgkmcnt(0)
	s_add_u32 s2, s4, s2
	s_addc_u32 s3, s5, 0
	s_lshl_b32 s4, s41, 8
	s_add_u32 s2, s2, s4
	s_addc_u32 s3, s3, 0
	v_and_b32_e32 v18, 48, v0
	v_mov_b32_e32 v19, 0
	v_lshl_add_u64 v[2:3], s[2:3], 0, v[18:19]
	s_load_dword s26, s[6:7], 0x0
	global_load_dwordx4 v[14:17], v[2:3], off
	v_lshl_add_u64 v[4:5], v[2:3], 0, 64
	s_mov_b64 s[2:3], 0x80
	v_bfe_u32 v28, v0, 3, 3
	v_and_b32_e32 v1, 7, v0
	global_load_dwordx4 v[10:13], v[4:5], off
	v_lshl_add_u64 v[4:5], v[2:3], 0, s[2:3]
	s_mov_b64 s[2:3], 0xc0
	v_bitop3_b32 v1, v28, v1, 6 bitop3:0x6c
	v_lshl_add_u64 v[2:3], v[2:3], 0, s[2:3]
	v_lshl_or_b32 v18, s50, 3, v28
	s_mov_b32 s2, 0x1e1e1e1f
	v_lshlrev_b32_e32 v20, 3, v1
	v_mul_hi_u32 v1, v18, s2
	v_lshrrev_b32_e32 v21, 2, v1
	s_movk_i32 s8, 0xffde
	s_add_i32 s24, s33, -1
	global_load_dwordx4 v[6:9], v[4:5], off
	v_mul_lo_u32 v22, v21, s8
	v_add_u32_e32 v1, s24, v21
	s_add_i32 s25, s27, -1
	s_movk_i32 s9, 0x154
	global_load_dwordx4 v[2:5], v[2:3], off
	v_add3_u32 v24, s25, v18, v22
	v_cmp_gt_u32_e64 s[2:3], s9, v18
	v_cmp_gt_u32_e32 vcc, 64, v1
	s_and_b64 s[6:7], s[2:3], vcc
	v_cmp_gt_u32_e64 s[4:5], 64, v24
	v_and_b32_e32 v25, 63, v0
	s_and_b64 s[10:11], s[6:7], s[4:5]
	v_mov_b64_e32 v[22:23], s[30:31]
	v_lshlrev_b32_e32 v18, 1, v20
	s_and_saveexec_b64 s[6:7], s[10:11]
	s_lshl_b32 s10, s38, 14
	v_lshlrev_b32_e32 v1, 6, v1
	v_or3_b32 v22, v1, s10, v24
	v_ashrrev_i32_e32 v23, 31, v22
	v_lshlrev_b64 v[22:23], 7, v[22:23]
	v_lshl_add_u64 v[22:23], s[36:37], 0, v[22:23]
	v_lshl_add_u64 v[22:23], v[22:23], 0, v[18:19]
	s_or_b64 exec, exec, s[6:7]
	s_lshl_b32 s42, s50, 10
	v_lshlrev_b32_e32 v1, 4, v25
	v_or_b32_e32 v19, s42, v1
	s_add_i32 s13, s50, 8
	v_readfirstlane_b32 s6, v19
	s_mov_b32 m0, s6
	s_mov_b32 s12, 0x3c3c3c3d
	global_load_lds_dwordx4 v[22:23], off
	v_lshl_or_b32 v22, s13, 3, v28
	v_mul_hi_u32 v19, v22, s12
	v_lshrrev_b32_e32 v26, 3, v19
	v_mul_lo_u32 v23, v26, s8
	v_add_u32_e32 v19, s24, v26
	v_add3_u32 v27, s25, v22, v23
	v_cmp_gt_u32_e64 s[6:7], s9, v22
	v_cmp_gt_u32_e32 vcc, 64, v19
	s_and_b64 s[10:11], s[6:7], vcc
	v_cmp_gt_u32_e64 s[8:9], 64, v27
	s_and_b64 s[14:15], s[10:11], s[8:9]
	v_mov_b64_e32 v[22:23], s[30:31]
	s_and_saveexec_b64 s[10:11], s[14:15]
	s_lshl_b32 s14, s38, 14
	v_lshlrev_b32_e32 v19, 6, v19
	v_or3_b32 v22, v19, s14, v27
	v_ashrrev_i32_e32 v23, 31, v22
	v_lshlrev_b64 v[22:23], 7, v[22:23]
	v_lshl_add_u64 v[22:23], s[36:37], 0, v[22:23]
	v_mov_b32_e32 v19, 0
	v_lshl_add_u64 v[22:23], v[22:23], 0, v[18:19]
	s_or_b64 exec, exec, s[10:11]
	s_lshl_b32 s43, s13, 10
	v_or_b32_e32 v19, s43, v1
	s_add_i32 s18, s50, 16
	v_readfirstlane_b32 s10, v19
	s_mov_b32 m0, s10
	s_movk_i32 s16, 0xffde
	global_load_lds_dwordx4 v[22:23], off
	v_lshl_or_b32 v22, s18, 3, v28
	v_mul_hi_u32 v19, v22, s12
	v_lshrrev_b32_e32 v29, 3, v19
	v_mul_lo_u32 v23, v29, s16
	v_add_u32_e32 v19, s24, v29
	s_movk_i32 s17, 0x154
	v_add3_u32 v30, s25, v22, v23
	v_cmp_gt_u32_e64 s[10:11], s17, v22
	v_cmp_gt_u32_e32 vcc, 64, v19
	s_and_b64 s[14:15], s[10:11], vcc
	v_cmp_gt_u32_e64 s[12:13], 64, v30
	s_and_b64 s[20:21], s[14:15], s[12:13]
	v_mov_b64_e32 v[22:23], s[30:31]
	s_and_saveexec_b64 s[14:15], s[20:21]
	s_lshl_b32 s19, s38, 14
	v_lshlrev_b32_e32 v19, 6, v19
	v_or3_b32 v22, v19, s19, v30
	v_ashrrev_i32_e32 v23, 31, v22
	v_lshlrev_b64 v[22:23], 7, v[22:23]
	v_lshl_add_u64 v[22:23], s[36:37], 0, v[22:23]
	v_mov_b32_e32 v19, 0
	v_lshl_add_u64 v[22:23], v[22:23], 0, v[18:19]
	s_or_b64 exec, exec, s[14:15]
	s_lshl_b32 s44, s18, 10
	v_or_b32_e32 v19, s44, v1
	s_add_i32 s21, s50, 24
	v_readfirstlane_b32 s14, v19
	s_mov_b32 m0, s14
	s_mov_b32 s20, 0x3c3c3c3d
	global_load_lds_dwordx4 v[22:23], off
	v_lshl_or_b32 v22, s21, 3, v28
	v_mul_hi_u32 v19, v22, s20
	v_lshrrev_b32_e32 v31, 3, v19
	v_mul_lo_u32 v23, v31, s16
	v_add_u32_e32 v19, s24, v31
	v_add3_u32 v32, s25, v22, v23
	v_cmp_gt_u32_e64 s[14:15], s17, v22
	v_cmp_gt_u32_e32 vcc, 64, v19
	s_and_b64 s[18:19], s[14:15], vcc
	v_cmp_gt_u32_e64 s[16:17], 64, v32
	s_and_b64 s[22:23], s[18:19], s[16:17]
	v_mov_b64_e32 v[22:23], s[30:31]
	s_and_saveexec_b64 s[18:19], s[22:23]
	s_lshl_b32 s22, s38, 14
	v_lshlrev_b32_e32 v19, 6, v19
	v_or3_b32 v22, v19, s22, v32
	v_ashrrev_i32_e32 v23, 31, v22
	v_lshlrev_b64 v[22:23], 7, v[22:23]
	v_lshl_add_u64 v[22:23], s[36:37], 0, v[22:23]
	v_mov_b32_e32 v19, 0
	v_lshl_add_u64 v[22:23], v[22:23], 0, v[18:19]
	s_or_b64 exec, exec, s[18:19]
	s_lshl_b32 s45, s21, 10
	v_or_b32_e32 v19, s45, v1
	s_add_i32 s28, s50, 32
	v_readfirstlane_b32 s18, v19
	s_mov_b32 m0, s18
	s_movk_i32 s18, 0xffde
	global_load_lds_dwordx4 v[22:23], off
	v_lshl_or_b32 v22, s28, 3, v28
	v_mul_hi_u32 v19, v22, s20
	v_lshrrev_b32_e32 v33, 3, v19
	v_mul_lo_u32 v23, v33, s18
	v_add_u32_e32 v19, s24, v33
	s_movk_i32 s18, 0x154
	v_add3_u32 v34, s25, v22, v23
	v_cmp_gt_u32_e64 s[18:19], s18, v22
	v_cmp_gt_u32_e32 vcc, 64, v19
	s_and_b64 s[22:23], s[18:19], vcc
	v_cmp_gt_u32_e64 s[20:21], 64, v34
	s_and_b64 s[22:23], s[22:23], s[20:21]
	s_xor_b64 s[22:23], s[22:23], -1
	s_and_saveexec_b64 s[34:35], s[22:23]
	s_xor_b64 s[22:23], exec, s[34:35]
	s_lshl_b32 s29, s38, 14
	s_or_saveexec_b64 s[22:23], s[22:23]
	v_mov_b32_e32 v35, s29
	v_mov_b64_e32 v[22:23], s[30:31]
	s_xor_b64 exec, exec, s[22:23]
	s_lshl_b32 s29, s38, 14
	v_lshlrev_b32_e32 v19, 6, v19
	v_or3_b32 v22, v19, s29, v34
	v_ashrrev_i32_e32 v23, 31, v22
	v_lshlrev_b64 v[22:23], 7, v[22:23]
	v_lshl_add_u64 v[22:23], s[36:37], 0, v[22:23]
	v_mov_b32_e32 v19, 0
	v_lshl_add_u64 v[22:23], v[22:23], 0, v[18:19]
	v_mov_b32_e32 v35, s29
	s_or_b64 exec, exec, s[22:23]
	s_lshl_b32 s46, s28, 10
	v_or_b32_e32 v18, s46, v1
	s_add_i32 s48, s50, 40
	v_readfirstlane_b32 s22, v18
	s_mov_b32 m0, s22
	v_lshl_or_b32 v19, s48, 3, v28
	global_load_lds_dwordx4 v[22:23], off
	s_mov_b32 s22, 0x3c3c3c3d
	v_mul_hi_u32 v18, v19, s22
	v_lshrrev_b32_e32 v36, 3, v18
	s_movk_i32 s22, 0xffde
	s_mov_b64 s[34:35], s[84:85]
	v_mul_lo_u32 v22, v36, s22
	v_add_u32_e32 v18, s24, v36
	s_movk_i32 s22, 0x154
	v_add3_u32 v37, s25, v19, v22
	v_cmp_gt_u32_e64 s[22:23], s22, v19
	v_cmp_gt_u32_e32 vcc, 64, v18
	s_and_b64 s[28:29], s[22:23], vcc
	v_cmp_gt_u32_e64 s[24:25], 64, v37
	s_and_b64 s[28:29], s[28:29], s[24:25]
	s_xor_b64 s[28:29], s[28:29], -1
	s_and_saveexec_b64 s[52:53], s[28:29]
	s_xor_b64 s[28:29], exec, s[52:53]
	s_or_saveexec_b64 s[28:29], s[28:29]
	s_lshl_b32 s51, s41, 6
	v_mov_b64_e32 v[22:23], s[30:31]
	s_xor_b64 exec, exec, s[28:29]
	v_lshlrev_b32_e32 v18, 6, v18
	v_or3_b32 v18, v18, v35, v37
	v_ashrrev_i32_e32 v19, 31, v18
	v_lshlrev_b64 v[18:19], 7, v[18:19]
	v_lshl_add_u64 v[18:19], s[36:37], 0, v[18:19]
	v_lshlrev_b32_e32 v22, 1, v20
	v_mov_b32_e32 v23, 0
	v_lshl_add_u64 v[22:23], v[18:19], 0, v[22:23]
	s_or_b64 exec, exec, s[28:29]
	v_and_b32_e32 v114, 15, v0
	s_and_b32 s52, s50, 6
	v_mad_u64_u32 v[116:117], s[52:53], s52, 34, v[114:115]
	v_lshrrev_b32_e32 v115, 4, v25
	v_or_b32_e32 v19, s51, v114
	v_bitop3_b32 v25, v115, v0, 6 bitop3:0x78
	v_lshlrev_b32_e32 v19, 7, v19
	v_lshlrev_b32_e32 v25, 4, v25
	s_mov_b32 s51, 0x18040
	s_lshl_b32 s48, s48, 10
	v_lshlrev_b32_e32 v18, 6, v28
	v_or_b32_e32 v28, v19, v25
	v_bitop3_b32 v125, v19, s51, v25 bitop3:0x36
	v_or_b32_e32 v19, s48, v1
	s_lshl_b32 s39, s49, 7
	v_readfirstlane_b32 s51, v19
	s_lshr_b32 s47, s40, 7
	s_mov_b32 m0, s51
	s_lshl_b32 s51, s49, 14
	s_waitcnt lgkmcnt(0)
	s_add_u32 s52, s34, s51
	v_or3_b32 v18, s42, v18, v20
	s_addc_u32 s53, s35, 0
	s_lshl_b32 s56, s50, 11
	v_mov_b32_e32 v19, 0
	global_load_lds_dwordx4 v[22:23], off
	s_add_i32 s50, s56, 0x18000
	v_lshlrev_b64 v[22:23], 1, v[18:19]
	v_lshl_add_u64 v[118:119], s[52:53], 0, v[22:23]
	s_mov_b32 m0, s50
	s_mov_b64 s[34:35], 0x400
	global_load_lds_dwordx4 v[118:119], off
	s_add_i32 m0, s56, 0x18400
	s_add_u32 s54, s52, 0x30000
	v_lshl_add_u64 v[40:41], v[118:119], 0, s[34:35]
	s_addc_u32 s55, s53, 0
	global_load_lds_dwordx4 v[40:41], off
	s_add_i32 m0, s56, 0x1c000
	v_lshl_add_u64 v[40:41], s[54:55], 0, v[22:23]
	v_or_b32_e32 v38, 0x200, v18
	v_mov_b32_e32 v39, v19
	global_load_lds_dwordx4 v[40:41], off
	s_add_i32 m0, s56, 0x1c400
	v_lshlrev_b64 v[38:39], 1, v[38:39]
	s_add_u32 s52, s52, 0x60000
	v_lshl_add_u64 v[40:41], s[54:55], 0, v[38:39]
	s_addc_u32 s53, s53, 0
	global_load_lds_dwordx4 v[40:41], off
	s_add_i32 m0, s56, 0x20000
	v_lshl_add_u64 v[22:23], s[52:53], 0, v[22:23]
	global_load_lds_dwordx4 v[22:23], off
	v_lshl_add_u64 v[22:23], s[52:53], 0, v[38:39]
	s_add_i32 m0, s56, 0x20400
	v_or_b32_e32 v124, 0x18000, v28
	global_load_lds_dwordx4 v[22:23], off
	s_waitcnt vmcnt(4) lgkmcnt(0)
	s_barrier
	ds_read_b128 v[66:69], v124
	ds_read_b128 v[70:73], v124 offset:2048
	v_lshlrev_b32_e32 v18, 7, v116
	v_bitop3_b32 v22, v116, v115, 6 bitop3:0x6c
	v_add_u32_e32 v117, 34, v116
	v_lshl_or_b32 v138, v22, 4, v18
	ds_read_b128 v[78:81], v138
	ds_read_b128 v[74:77], v138 offset:2048
	v_lshlrev_b32_e32 v18, 7, v117
	v_bitop3_b32 v22, v117, v115, 6 bitop3:0x6c
	v_lshl_or_b32 v139, v22, 4, v18
	ds_read_b128 v[82:85], v139
	s_load_dwordx2 s[28:29], s[0:1], 0x20
	ds_read_b128 v[86:89], v139 offset:2048
	ds_read_b128 v[94:97], v124 offset:4096
	ds_read_b128 v[98:101], v124 offset:6144
	v_lshlrev_b32_e32 v18, 1, v20
	s_mov_b32 s49, 0
	s_mov_b32 s51, 1
	v_add_u32_e32 v126, s33, v21
	v_add_u32_e32 v127, v35, v24
	v_lshl_add_u64 v[120:121], s[36:37], 0, v[18:19]
	v_add_u32_e32 v128, s33, v26
	v_add_u32_e32 v129, v35, v27
	v_add_u32_e32 v130, s33, v29
	v_add_u32_e32 v131, v35, v30
	v_add_u32_e32 v132, s33, v31
	v_add_u32_e32 v133, v35, v32
	v_add_u32_e32 v134, s33, v33
	v_add_u32_e32 v135, v35, v34
	v_add_u32_e32 v136, s33, v36
	v_add_u32_e32 v137, v35, v37
	s_mov_b64 s[36:37], 0
	s_mov_b32 s52, 0
	v_mov_b32_e32 v18, v19
	v_mov_b32_e32 v20, v19
	v_mov_b32_e32 v21, v19
	v_mov_b32_e32 v38, v19
	v_mov_b32_e32 v39, v19
	v_mov_b32_e32 v40, v19
	v_mov_b32_e32 v41, v19
	v_mov_b32_e32 v42, v19
	v_mov_b32_e32 v43, v19
	v_mov_b32_e32 v44, v19
	v_mov_b32_e32 v45, v19
	v_mov_b32_e32 v46, v19
	v_mov_b32_e32 v47, v19
	v_mov_b32_e32 v48, v19
	v_mov_b32_e32 v49, v19
	v_mov_b32_e32 v50, v19
	v_mov_b32_e32 v51, v19
	v_mov_b32_e32 v52, v19
	v_mov_b32_e32 v53, v19
	v_mov_b32_e32 v54, v19
	v_mov_b32_e32 v55, v19
	v_mov_b32_e32 v56, v19
	v_mov_b32_e32 v57, v19
	v_mov_b32_e32 v58, v19
	v_mov_b32_e32 v59, v19
	v_mov_b32_e32 v60, v19
	v_mov_b32_e32 v61, v19
	v_mov_b32_e32 v62, v19
	v_mov_b32_e32 v63, v19
	v_mov_b32_e32 v64, v19
	v_mov_b32_e32 v65, v19
	v_mov_b32_e32 v90, v19
	v_mov_b32_e32 v91, v19
	v_mov_b32_e32 v92, v19
	v_mov_b32_e32 v93, v19
	v_mov_b32_e32 v102, v19
	v_mov_b32_e32 v103, v19
	v_mov_b32_e32 v104, v19
	v_mov_b32_e32 v105, v19
	v_mov_b32_e32 v106, v19
	v_mov_b32_e32 v107, v19
	v_mov_b32_e32 v108, v19
	v_mov_b32_e32 v109, v19
	v_mov_b32_e32 v110, v19
	v_mov_b32_e32 v111, v19
	v_mov_b32_e32 v112, v19
	v_mov_b32_e32 v113, v19
	v_mov_b32_e32 v34, v19
	v_mov_b32_e32 v35, v19
	v_mov_b32_e32 v36, v19
	v_mov_b32_e32 v37, v19
	v_mov_b32_e32 v30, v19
	v_mov_b32_e32 v31, v19
	v_mov_b32_e32 v32, v19
	v_mov_b32_e32 v33, v19
	v_mov_b32_e32 v26, v19
	v_mov_b32_e32 v27, v19
	v_mov_b32_e32 v28, v19
	v_mov_b32_e32 v29, v19
	v_mov_b32_e32 v22, v19
	v_mov_b32_e32 v23, v19
	v_mov_b32_e32 v24, v19
	v_mov_b32_e32 v25, v19
	s_mov_b32 s60, 0
	s_mov_b32 s61, 0
	s_mov_b32 s62, 0
	s_mov_b32 s64, 0
	s_mov_b32 s66, 1
	s_mov_b32 s67, 0
	s_mov_b32 s69, 0
	v_mov_b32_e32 v172, v125
	s_waitcnt lgkmcnt(0)

.LBB6_37:
	s_waitcnt vmcnt(0) lgkmcnt(0)
	s_cmpk_gt_u32 s40, 0x1ff
	s_barrier
	s_cbranch_scc1 .LBB6_39
	s_mov_b32 s0, s88
	s_movk_i32 s1, 0x110
	v_lshlrev_b32_e32 v66, 3, v115
	v_lshl_or_b32 v1, s47, 6, v114
	v_lshl_or_b32 v66, s41, 7, v66
	s_waitcnt lgkmcnt(0)
	v_pk_fma_f32 v[68:69], s[0:1], v[110:111], v[14:15] op_sel_hi:[0,1,1]
	v_pk_mul_f32 v[70:71], s[26:27], v[68:69] op_sel_hi:[0,1]
	v_cmp_le_f32_e32 vcc, 0, v69
	v_mad_u64_u32 v[66:67], s[2:3], v1, s1, v[66:67]
	s_nop 0
	v_cndmask_b32_e32 v1, v71, v69, vcc
	v_cmp_le_f32_e32 vcc, 0, v68
	v_pk_fma_f32 v[62:63], s[0:1], v[62:63], v[14:15] op_sel_hi:[0,1,1]
	v_pk_fma_f32 v[64:65], s[0:1], v[64:65], v[16:17] op_sel_hi:[0,1,1]
	v_cndmask_b32_e32 v67, v70, v68, vcc
	v_pk_fma_f32 v[70:71], s[0:1], v[112:113], v[16:17] op_sel_hi:[0,1,1]
	v_pk_mul_f32 v[72:73], s[26:27], v[70:71] op_sel_hi:[0,1]
	v_cmp_le_f32_e32 vcc, 0, v71
	v_cvt_pk_f16_f32 v68, v67, v1
	v_pk_fma_f32 v[58:59], s[0:1], v[58:59], v[10:11] op_sel_hi:[0,1,1]
	v_cndmask_b32_e32 v1, v73, v71, vcc
	v_cmp_le_f32_e32 vcc, 0, v70
	v_pk_fma_f32 v[60:61], s[0:1], v[60:61], v[12:13] op_sel_hi:[0,1,1]
	v_pk_fma_f32 v[54:55], s[0:1], v[54:55], v[6:7] op_sel_hi:[0,1,1]
	v_cndmask_b32_e32 v67, v72, v70, vcc
	v_pk_fma_f32 v[70:71], s[0:1], v[106:107], v[10:11] op_sel_hi:[0,1,1]
	v_pk_mul_f32 v[72:73], s[26:27], v[70:71] op_sel_hi:[0,1]
	v_cmp_le_f32_e32 vcc, 0, v71
	v_cvt_pk_f16_f32 v69, v67, v1
	v_pk_fma_f32 v[56:57], s[0:1], v[56:57], v[8:9] op_sel_hi:[0,1,1]
	v_cndmask_b32_e32 v1, v73, v71, vcc
	v_cmp_le_f32_e32 vcc, 0, v70
	v_pk_fma_f32 v[50:51], s[0:1], v[50:51], v[2:3] op_sel_hi:[0,1,1]
	v_pk_fma_f32 v[52:53], s[0:1], v[52:53], v[4:5] op_sel_hi:[0,1,1]
	v_cndmask_b32_e32 v67, v72, v70, vcc
	v_pk_fma_f32 v[72:73], s[0:1], v[108:109], v[12:13] op_sel_hi:[0,1,1]
	v_pk_mul_f32 v[74:75], s[26:27], v[72:73] op_sel_hi:[0,1]
	v_cmp_le_f32_e32 vcc, 0, v73
	v_cvt_pk_f16_f32 v70, v67, v1
	v_pk_fma_f32 v[46:47], s[0:1], v[46:47], v[14:15] op_sel_hi:[0,1,1]
	v_cndmask_b32_e32 v1, v75, v73, vcc
	v_cmp_le_f32_e32 vcc, 0, v72
	v_pk_fma_f32 v[48:49], s[0:1], v[48:49], v[16:17] op_sel_hi:[0,1,1]
	v_pk_fma_f32 v[42:43], s[0:1], v[42:43], v[10:11] op_sel_hi:[0,1,1]
	v_cndmask_b32_e32 v67, v74, v72, vcc
	v_cvt_pk_f16_f32 v71, v67, v1
	ds_write2_b64 v66, v[68:69], v[70:71] offset1:4
	v_pk_fma_f32 v[68:69], s[0:1], v[102:103], v[6:7] op_sel_hi:[0,1,1]
	v_pk_mul_f32 v[70:71], s[26:27], v[68:69] op_sel_hi:[0,1]
	v_cmp_le_f32_e32 vcc, 0, v69
	v_pk_fma_f32 v[44:45], s[0:1], v[44:45], v[12:13] op_sel_hi:[0,1,1]
	v_pk_fma_f32 v[38:39], s[0:1], v[38:39], v[6:7] op_sel_hi:[0,1,1]
	v_cndmask_b32_e32 v1, v71, v69, vcc
	v_cmp_le_f32_e32 vcc, 0, v68
	v_pk_fma_f32 v[40:41], s[0:1], v[40:41], v[8:9] op_sel_hi:[0,1,1]
	v_pk_fma_f32 v[18:19], s[0:1], v[18:19], v[2:3] op_sel_hi:[0,1,1]
	v_cndmask_b32_e32 v67, v70, v68, vcc
	v_pk_fma_f32 v[70:71], s[0:1], v[104:105], v[8:9] op_sel_hi:[0,1,1]
	v_pk_mul_f32 v[72:73], s[26:27], v[70:71] op_sel_hi:[0,1]
	v_cmp_le_f32_e32 vcc, 0, v71
	v_cvt_pk_f16_f32 v68, v67, v1
	v_pk_fma_f32 v[20:21], s[0:1], v[20:21], v[4:5] op_sel_hi:[0,1,1]
	v_cndmask_b32_e32 v1, v73, v71, vcc
	v_cmp_le_f32_e32 vcc, 0, v70
	v_pk_fma_f32 v[14:15], s[0:1], v[34:35], v[14:15] op_sel_hi:[0,1,1]
	v_pk_fma_f32 v[16:17], s[0:1], v[36:37], v[16:17] op_sel_hi:[0,1,1]
	v_cndmask_b32_e32 v67, v72, v70, vcc
	v_pk_fma_f32 v[70:71], s[0:1], v[90:91], v[2:3] op_sel_hi:[0,1,1]
	v_pk_mul_f32 v[72:73], s[26:27], v[70:71] op_sel_hi:[0,1]
	v_cmp_le_f32_e32 vcc, 0, v71
	v_cvt_pk_f16_f32 v69, v67, v1
	v_pk_fma_f32 v[10:11], s[0:1], v[30:31], v[10:11] op_sel_hi:[0,1,1]
	v_cndmask_b32_e32 v1, v73, v71, vcc
	v_cmp_le_f32_e32 vcc, 0, v70
	v_pk_fma_f32 v[12:13], s[0:1], v[32:33], v[12:13] op_sel_hi:[0,1,1]
	v_pk_fma_f32 v[6:7], s[0:1], v[26:27], v[6:7] op_sel_hi:[0,1,1]
	v_cndmask_b32_e32 v67, v72, v70, vcc
	v_pk_fma_f32 v[72:73], s[0:1], v[92:93], v[4:5] op_sel_hi:[0,1,1]
	v_pk_mul_f32 v[74:75], s[26:27], v[72:73] op_sel_hi:[0,1]
	v_cmp_le_f32_e32 vcc, 0, v73
	v_cvt_pk_f16_f32 v70, v67, v1
	v_pk_fma_f32 v[8:9], s[0:1], v[28:29], v[8:9] op_sel_hi:[0,1,1]
	v_cndmask_b32_e32 v1, v75, v73, vcc
	v_cmp_le_f32_e32 vcc, 0, v72
	v_pk_fma_f32 v[2:3], s[0:1], v[22:23], v[2:3] op_sel_hi:[0,1,1]
	v_pk_fma_f32 v[4:5], s[0:1], v[24:25], v[4:5] op_sel_hi:[0,1,1]
	v_cndmask_b32_e32 v67, v74, v72, vcc
	v_cvt_pk_f16_f32 v71, v67, v1
	ds_write2_b64 v66, v[68:69], v[70:71] offset0:8 offset1:12
	v_pk_mul_f32 v[68:69], s[26:27], v[62:63] op_sel_hi:[0,1]
	v_cmp_le_f32_e32 vcc, 0, v63
	s_nop 1
	v_cndmask_b32_e32 v1, v69, v63, vcc
	v_cmp_le_f32_e32 vcc, 0, v62
	s_nop 1
	v_cndmask_b32_e32 v62, v68, v62, vcc
	v_pk_mul_f32 v[68:69], s[26:27], v[64:65] op_sel_hi:[0,1]
	v_cmp_le_f32_e32 vcc, 0, v65
	v_cvt_pk_f16_f32 v62, v62, v1
	s_nop 0
	v_cndmask_b32_e32 v1, v69, v65, vcc
	v_cmp_le_f32_e32 vcc, 0, v64
	s_nop 1
	v_cndmask_b32_e32 v63, v68, v64, vcc
	v_pk_mul_f32 v[64:65], s[26:27], v[58:59] op_sel_hi:[0,1]
	v_cmp_le_f32_e32 vcc, 0, v59
	v_cvt_pk_f16_f32 v63, v63, v1
	s_nop 0
	v_cndmask_b32_e32 v1, v65, v59, vcc
	v_cmp_le_f32_e32 vcc, 0, v58
	s_nop 1
	v_cndmask_b32_e32 v58, v64, v58, vcc
	v_pk_mul_f32 v[64:65], s[26:27], v[60:61] op_sel_hi:[0,1]
	v_cmp_le_f32_e32 vcc, 0, v61
	v_cvt_pk_f16_f32 v58, v58, v1
	s_nop 0
	v_cndmask_b32_e32 v1, v65, v61, vcc
	v_cmp_le_f32_e32 vcc, 0, v60
	s_nop 1
	v_cndmask_b32_e32 v59, v64, v60, vcc
	v_cvt_pk_f16_f32 v59, v59, v1
	v_add_u32_e32 v1, 0x1000, v66
	ds_write2_b64 v1, v[62:63], v[58:59] offset0:32 offset1:36
	v_pk_mul_f32 v[58:59], s[26:27], v[54:55] op_sel_hi:[0,1]
	v_cmp_le_f32_e32 vcc, 0, v55
	s_nop 1
	v_cndmask_b32_e32 v55, v59, v55, vcc
	v_cmp_le_f32_e32 vcc, 0, v54
	s_nop 1
	v_cndmask_b32_e32 v54, v58, v54, vcc
	v_pk_mul_f32 v[58:59], s[26:27], v[56:57] op_sel_hi:[0,1]
	v_cmp_le_f32_e32 vcc, 0, v57
	v_cvt_pk_f16_f32 v54, v54, v55
	s_nop 0
	v_cndmask_b32_e32 v55, v59, v57, vcc
	v_cmp_le_f32_e32 vcc, 0, v56
	s_nop 1
	v_cndmask_b32_e32 v56, v58, v56, vcc
	v_cvt_pk_f16_f32 v55, v56, v55
	v_pk_mul_f32 v[56:57], s[26:27], v[50:51] op_sel_hi:[0,1]
	v_cmp_le_f32_e32 vcc, 0, v51
	s_nop 1
	v_cndmask_b32_e32 v51, v57, v51, vcc
	v_cmp_le_f32_e32 vcc, 0, v50
	s_nop 1
	v_cndmask_b32_e32 v50, v56, v50, vcc
	v_pk_mul_f32 v[56:57], s[26:27], v[52:53] op_sel_hi:[0,1]
	v_cmp_le_f32_e32 vcc, 0, v53
	v_cvt_pk_f16_f32 v50, v50, v51
	s_nop 0
	v_cndmask_b32_e32 v51, v57, v53, vcc
	v_cmp_le_f32_e32 vcc, 0, v52
	s_nop 1
	v_cndmask_b32_e32 v52, v56, v52, vcc
	v_cvt_pk_f16_f32 v51, v52, v51
	ds_write2_b64 v1, v[54:55], v[50:51] offset0:40 offset1:44
	v_pk_mul_f32 v[50:51], s[26:27], v[46:47] op_sel_hi:[0,1]
	v_cmp_le_f32_e32 vcc, 0, v47
	s_nop 1
	v_cndmask_b32_e32 v1, v51, v47, vcc
	v_cmp_le_f32_e32 vcc, 0, v46
	s_nop 1
	v_cndmask_b32_e32 v46, v50, v46, vcc
	v_pk_mul_f32 v[50:51], s[26:27], v[48:49] op_sel_hi:[0,1]
	v_cmp_le_f32_e32 vcc, 0, v49
	v_cvt_pk_f16_f32 v46, v46, v1
	s_nop 0
	v_cndmask_b32_e32 v1, v51, v49, vcc
	v_cmp_le_f32_e32 vcc, 0, v48
	s_nop 1
	v_cndmask_b32_e32 v47, v50, v48, vcc
	v_pk_mul_f32 v[48:49], s[26:27], v[42:43] op_sel_hi:[0,1]
	v_cmp_le_f32_e32 vcc, 0, v43
	v_cvt_pk_f16_f32 v47, v47, v1
	s_nop 0
	v_cndmask_b32_e32 v1, v49, v43, vcc
	v_cmp_le_f32_e32 vcc, 0, v42
	s_nop 1
	v_cndmask_b32_e32 v42, v48, v42, vcc
	v_pk_mul_f32 v[48:49], s[26:27], v[44:45] op_sel_hi:[0,1]
	v_cmp_le_f32_e32 vcc, 0, v45
	v_cvt_pk_f16_f32 v42, v42, v1
	s_nop 0
	v_cndmask_b32_e32 v1, v49, v45, vcc
	v_cmp_le_f32_e32 vcc, 0, v44
	s_nop 1
	v_cndmask_b32_e32 v43, v48, v44, vcc
	v_cvt_pk_f16_f32 v43, v43, v1
	v_add_u32_e32 v1, 0x2000, v66
	ds_write2_b64 v1, v[46:47], v[42:43] offset0:64 offset1:68
	v_pk_mul_f32 v[42:43], s[26:27], v[38:39] op_sel_hi:[0,1]
	v_cmp_le_f32_e32 vcc, 0, v39
	s_nop 1
	v_cndmask_b32_e32 v39, v43, v39, vcc
	v_cmp_le_f32_e32 vcc, 0, v38
	s_nop 1
	v_cndmask_b32_e32 v38, v42, v38, vcc
	v_pk_mul_f32 v[42:43], s[26:27], v[40:41] op_sel_hi:[0,1]
	v_cmp_le_f32_e32 vcc, 0, v41
	v_cvt_pk_f16_f32 v38, v38, v39
	s_nop 0
	v_cndmask_b32_e32 v39, v43, v41, vcc
	v_cmp_le_f32_e32 vcc, 0, v40
	s_nop 1
	v_cndmask_b32_e32 v40, v42, v40, vcc
	v_cvt_pk_f16_f32 v39, v40, v39
	v_pk_mul_f32 v[40:41], s[26:27], v[18:19] op_sel_hi:[0,1]
	v_cmp_le_f32_e32 vcc, 0, v19
	s_nop 1
	v_cndmask_b32_e32 v19, v41, v19, vcc
	v_cmp_le_f32_e32 vcc, 0, v18
	s_nop 1
	v_cndmask_b32_e32 v18, v40, v18, vcc
	v_pk_mul_f32 v[40:41], s[26:27], v[20:21] op_sel_hi:[0,1]
	v_cmp_le_f32_e32 vcc, 0, v21
	v_cvt_pk_f16_f32 v18, v18, v19
	s_nop 0
	v_cndmask_b32_e32 v19, v41, v21, vcc
	v_cmp_le_f32_e32 vcc, 0, v20
	s_nop 1
	v_cndmask_b32_e32 v20, v40, v20, vcc
	v_cvt_pk_f16_f32 v19, v20, v19
	ds_write2_b64 v1, v[38:39], v[18:19] offset0:72 offset1:76
	v_pk_mul_f32 v[18:19], s[26:27], v[14:15] op_sel_hi:[0,1]
	v_cmp_le_f32_e32 vcc, 0, v15
	s_nop 1
	v_cndmask_b32_e32 v1, v19, v15, vcc
	v_cmp_le_f32_e32 vcc, 0, v14
	s_nop 1
	v_cndmask_b32_e32 v14, v18, v14, vcc
	v_pk_mul_f32 v[18:19], s[26:27], v[16:17] op_sel_hi:[0,1]
	v_cmp_le_f32_e32 vcc, 0, v17
	v_cvt_pk_f16_f32 v14, v14, v1
	s_nop 0
	v_cndmask_b32_e32 v1, v19, v17, vcc
	v_cmp_le_f32_e32 vcc, 0, v16
	s_nop 1
	v_cndmask_b32_e32 v15, v18, v16, vcc
	v_pk_mul_f32 v[16:17], s[26:27], v[10:11] op_sel_hi:[0,1]
	v_cmp_le_f32_e32 vcc, 0, v11
	v_cvt_pk_f16_f32 v15, v15, v1
	s_nop 0
	v_cndmask_b32_e32 v1, v17, v11, vcc
	v_cmp_le_f32_e32 vcc, 0, v10
	s_nop 1
	v_cndmask_b32_e32 v10, v16, v10, vcc
	v_pk_mul_f32 v[16:17], s[26:27], v[12:13] op_sel_hi:[0,1]
	v_cmp_le_f32_e32 vcc, 0, v13
	v_cvt_pk_f16_f32 v10, v10, v1
	s_nop 0
	v_cndmask_b32_e32 v1, v17, v13, vcc
	v_cmp_le_f32_e32 vcc, 0, v12
	s_nop 1
	v_cndmask_b32_e32 v11, v16, v12, vcc
	v_cvt_pk_f16_f32 v11, v11, v1
	v_add_u32_e32 v1, 0x3000, v66
	ds_write2_b64 v1, v[14:15], v[10:11] offset0:96 offset1:100
	v_pk_mul_f32 v[10:11], s[26:27], v[6:7] op_sel_hi:[0,1]
	v_cmp_le_f32_e32 vcc, 0, v7
	s_nop 1
	v_cndmask_b32_e32 v7, v11, v7, vcc
	v_cmp_le_f32_e32 vcc, 0, v6
	s_nop 1
	v_cndmask_b32_e32 v6, v10, v6, vcc
	v_pk_mul_f32 v[10:11], s[26:27], v[8:9] op_sel_hi:[0,1]
	v_cmp_le_f32_e32 vcc, 0, v9
	v_cvt_pk_f16_f32 v6, v6, v7
	s_nop 0
	v_cndmask_b32_e32 v7, v11, v9, vcc
	v_cmp_le_f32_e32 vcc, 0, v8
	s_nop 1
	v_cndmask_b32_e32 v8, v10, v8, vcc
	v_cvt_pk_f16_f32 v7, v8, v7
	v_pk_mul_f32 v[8:9], s[26:27], v[2:3] op_sel_hi:[0,1]
	v_cmp_le_f32_e32 vcc, 0, v3
	s_nop 1
	v_cndmask_b32_e32 v3, v9, v3, vcc
	v_cmp_le_f32_e32 vcc, 0, v2
	s_nop 1
	v_cndmask_b32_e32 v2, v8, v2, vcc
	v_pk_mul_f32 v[8:9], s[26:27], v[4:5] op_sel_hi:[0,1]
	v_cmp_le_f32_e32 vcc, 0, v5
	v_cvt_pk_f16_f32 v2, v2, v3
	s_nop 0
	v_cndmask_b32_e32 v3, v9, v5, vcc
	v_cmp_le_f32_e32 vcc, 0, v4
	s_nop 1
	v_cndmask_b32_e32 v4, v8, v4, vcc
	v_cvt_pk_f16_f32 v3, v4, v3
	ds_write2_b64 v1, v[6:7], v[2:3] offset0:104 offset1:108

_Z6conv_kILi512ELi256ELi3ELi64ELi1ELi1ELb0EEvPKDF16_S1_PKfS3_PDF16_S4_S1_fS3_S3_S3_S3_:
	s_lshl_b32 s3, s2, 3
	s_load_dwordx2 s[36:37], s[0:1], 0x0
	s_load_dword s88, s[0:1], 0x38
	s_load_dwordx2 s[84:85], s[0:1], 0x8
	s_load_dwordx4 s[4:7], s[0:1], 0x10
	s_load_dwordx2 s[30:31], s[0:1], 0x30
	s_and_b32 s3, s3, 56
	s_ashr_i32 s8, s2, 5
	s_add_i32 s3, s3, s8
	v_readfirstlane_b32 s42, v0
	s_lshl_b32 s8, s3, 2
	s_bfe_u32 s38, s2, 0x20003
	s_and_b32 s33, s8, 56
	s_lshr_b32 s52, s42, 6
	s_ashr_i32 s40, s3, 4
	s_and_b32 s27, s2, 32
	s_lshl_b32 s2, s38, 8
	v_bfe_u32 v29, v0, 3, 3
	v_and_b32_e32 v2, 7, v0
	s_waitcnt lgkmcnt(0)
	s_add_u32 s2, s4, s2
	v_bitop3_b32 v2, v29, v2, 6 bitop3:0x6c
	s_addc_u32 s3, s5, 0
	v_and_b32_e32 v18, 48, v0
	v_mov_b32_e32 v19, 0
	v_lshlrev_b32_e32 v20, 3, v2
	v_lshl_add_u64 v[2:3], s[2:3], 0, v[18:19]
	s_load_dword s26, s[6:7], 0x0
	global_load_dwordx4 v[14:17], v[2:3], off
	v_lshl_add_u64 v[4:5], v[2:3], 0, 64
	s_mov_b64 s[2:3], 0x80
	global_load_dwordx4 v[10:13], v[4:5], off
	v_lshl_add_u64 v[4:5], v[2:3], 0, s[2:3]
	s_mov_b64 s[2:3], 0xc0
	v_lshl_add_u64 v[2:3], v[2:3], 0, s[2:3]
	v_lshl_or_b32 v18, s52, 3, v29
	s_mov_b32 s2, 0x1e1e1e1f
	v_mul_hi_u32 v21, v18, s2
	v_lshrrev_b32_e32 v21, 2, v21
	s_movk_i32 s8, 0xffde
	s_add_i32 s24, s33, -1
	global_load_dwordx4 v[6:9], v[4:5], off
	v_mul_lo_u32 v22, v21, s8
	v_add_u32_e32 v25, s24, v21
	s_add_i32 s25, s27, -1
	s_movk_i32 s9, 0x154
	global_load_dwordx4 v[2:5], v[2:3], off
	v_add3_u32 v24, s25, v18, v22
	v_cmp_gt_u32_e64 s[2:3], s9, v18
	v_cmp_gt_u32_e32 vcc, 64, v25
	s_and_b64 s[6:7], s[2:3], vcc
	v_cmp_gt_u32_e64 s[4:5], 64, v24
	v_and_b32_e32 v1, 63, v0
	s_and_b64 s[10:11], s[6:7], s[4:5]
	v_mov_b64_e32 v[22:23], s[30:31]
	v_lshlrev_b32_e32 v18, 1, v20
	s_and_saveexec_b64 s[6:7], s[10:11]
	s_lshl_b32 s10, s40, 15
	v_lshlrev_b32_e32 v22, 6, v25
	v_or3_b32 v22, v22, s10, v24
	v_ashrrev_i32_e32 v23, 31, v22
	v_lshlrev_b64 v[22:23], 7, v[22:23]
	v_lshl_add_u64 v[22:23], s[36:37], 0, v[22:23]
	v_lshl_add_u64 v[22:23], v[22:23], 0, v[18:19]
	s_or_b64 exec, exec, s[6:7]
	s_lshl_b32 s43, s52, 10
	v_lshlrev_b32_e32 v120, 4, v1
	v_or_b32_e32 v19, s43, v120
	s_add_i32 s13, s52, 8
	v_readfirstlane_b32 s6, v19
	s_mov_b32 m0, s6
	s_mov_b32 s12, 0x3c3c3c3d
	v_mov_b64_e32 v[184:185], v[22:23]
	global_load_lds_dwordx4 v[22:23], off
	v_lshl_or_b32 v22, s13, 3, v29
	v_mul_hi_u32 v19, v22, s12
	v_lshrrev_b32_e32 v25, 3, v19
	v_mul_lo_u32 v23, v25, s8
	v_add_u32_e32 v19, s24, v25
	v_add3_u32 v26, s25, v22, v23
	v_cmp_gt_u32_e64 s[6:7], s9, v22
	v_cmp_gt_u32_e32 vcc, 64, v19
	s_and_b64 s[10:11], s[6:7], vcc
	v_cmp_gt_u32_e64 s[8:9], 64, v26
	s_and_b64 s[14:15], s[10:11], s[8:9]
	v_mov_b64_e32 v[22:23], s[30:31]
	s_and_saveexec_b64 s[10:11], s[14:15]
	s_lshl_b32 s14, s40, 15
	v_lshlrev_b32_e32 v19, 6, v19
	v_or3_b32 v22, v19, s14, v26
	v_ashrrev_i32_e32 v23, 31, v22
	v_lshlrev_b64 v[22:23], 7, v[22:23]
	v_lshl_add_u64 v[22:23], s[36:37], 0, v[22:23]
	v_mov_b32_e32 v19, 0
	v_lshl_add_u64 v[22:23], v[22:23], 0, v[18:19]
	s_or_b64 exec, exec, s[10:11]
	s_lshl_b32 s44, s13, 10
	v_or_b32_e32 v19, s44, v120
	s_add_i32 s18, s52, 16
	v_readfirstlane_b32 s10, v19
	s_mov_b32 m0, s10
	s_movk_i32 s16, 0xffde
	v_mov_b64_e32 v[186:187], v[22:23]
	global_load_lds_dwordx4 v[22:23], off
	v_lshl_or_b32 v22, s18, 3, v29
	v_mul_hi_u32 v19, v22, s12
	v_lshrrev_b32_e32 v27, 3, v19
	v_mul_lo_u32 v23, v27, s16
	v_add_u32_e32 v19, s24, v27
	s_movk_i32 s17, 0x154
	v_add3_u32 v28, s25, v22, v23
	v_cmp_gt_u32_e64 s[10:11], s17, v22
	v_cmp_gt_u32_e32 vcc, 64, v19
	s_and_b64 s[14:15], s[10:11], vcc
	v_cmp_gt_u32_e64 s[12:13], 64, v28
	s_and_b64 s[20:21], s[14:15], s[12:13]
	v_mov_b64_e32 v[22:23], s[30:31]
	s_and_saveexec_b64 s[14:15], s[20:21]
	s_lshl_b32 s19, s40, 15
	v_lshlrev_b32_e32 v19, 6, v19
	v_or3_b32 v22, v19, s19, v28
	v_ashrrev_i32_e32 v23, 31, v22
	v_lshlrev_b64 v[22:23], 7, v[22:23]
	v_lshl_add_u64 v[22:23], s[36:37], 0, v[22:23]
	v_mov_b32_e32 v19, 0
	v_lshl_add_u64 v[22:23], v[22:23], 0, v[18:19]
	s_or_b64 exec, exec, s[14:15]
	s_lshl_b32 s45, s18, 10
	v_or_b32_e32 v19, s45, v120
	s_add_i32 s21, s52, 24
	v_readfirstlane_b32 s14, v19
	s_mov_b32 m0, s14
	s_mov_b32 s20, 0x3c3c3c3d
	v_mov_b64_e32 v[188:189], v[22:23]
	global_load_lds_dwordx4 v[22:23], off
	v_lshl_or_b32 v22, s21, 3, v29
	v_mul_hi_u32 v19, v22, s20
	v_lshrrev_b32_e32 v30, 3, v19
	v_mul_lo_u32 v23, v30, s16
	v_add_u32_e32 v19, s24, v30
	v_add3_u32 v31, s25, v22, v23
	v_cmp_gt_u32_e64 s[14:15], s17, v22
	v_cmp_gt_u32_e32 vcc, 64, v19
	s_and_b64 s[18:19], s[14:15], vcc
	v_cmp_gt_u32_e64 s[16:17], 64, v31
	s_and_b64 s[22:23], s[18:19], s[16:17]
	v_mov_b64_e32 v[22:23], s[30:31]
	s_and_saveexec_b64 s[18:19], s[22:23]
	s_lshl_b32 s22, s40, 15
	v_lshlrev_b32_e32 v19, 6, v19
	v_or3_b32 v22, v19, s22, v31
	v_ashrrev_i32_e32 v23, 31, v22
	v_lshlrev_b64 v[22:23], 7, v[22:23]
	v_lshl_add_u64 v[22:23], s[36:37], 0, v[22:23]
	v_mov_b32_e32 v19, 0
	v_lshl_add_u64 v[22:23], v[22:23], 0, v[18:19]
	s_or_b64 exec, exec, s[18:19]
	s_lshl_b32 s46, s21, 10
	v_or_b32_e32 v19, s46, v120
	s_add_i32 s28, s52, 32
	v_readfirstlane_b32 s18, v19
	s_mov_b32 m0, s18
	s_movk_i32 s18, 0xffde
	v_mov_b64_e32 v[190:191], v[22:23]
	global_load_lds_dwordx4 v[22:23], off
	v_lshl_or_b32 v22, s28, 3, v29
	v_mul_hi_u32 v19, v22, s20
	v_lshrrev_b32_e32 v32, 3, v19
	v_mul_lo_u32 v23, v32, s18
	v_add_u32_e32 v19, s24, v32
	s_movk_i32 s18, 0x154
	v_add3_u32 v33, s25, v22, v23
	v_cmp_gt_u32_e64 s[18:19], s18, v22
	v_cmp_gt_u32_e32 vcc, 64, v19
	s_and_b64 s[22:23], s[18:19], vcc
	v_cmp_gt_u32_e64 s[20:21], 64, v33
	s_and_b64 s[22:23], s[22:23], s[20:21]
	s_xor_b64 s[22:23], s[22:23], -1
	s_and_saveexec_b64 s[34:35], s[22:23]
	s_xor_b64 s[22:23], exec, s[34:35]
	s_lshl_b32 s29, s40, 15
	s_or_saveexec_b64 s[22:23], s[22:23]
	v_mov_b32_e32 v34, s29
	v_mov_b64_e32 v[22:23], s[30:31]
	s_xor_b64 exec, exec, s[22:23]
	s_lshl_b32 s29, s40, 15
	v_lshlrev_b32_e32 v19, 6, v19
	v_or3_b32 v22, v19, s29, v33
	v_ashrrev_i32_e32 v23, 31, v22
	v_lshlrev_b64 v[22:23], 7, v[22:23]
	v_lshl_add_u64 v[22:23], s[36:37], 0, v[22:23]
	v_mov_b32_e32 v19, 0
	v_lshl_add_u64 v[22:23], v[22:23], 0, v[18:19]
	v_mov_b32_e32 v34, s29
	s_or_b64 exec, exec, s[22:23]
	s_lshl_b32 s47, s28, 10
	v_or_b32_e32 v18, s47, v120
	s_add_i32 s39, s52, 40
	v_readfirstlane_b32 s22, v18
	s_mov_b32 m0, s22
	v_lshl_or_b32 v18, s39, 3, v29
	v_mov_b64_e32 v[192:193], v[22:23]
	global_load_lds_dwordx4 v[22:23], off
	s_mov_b32 s22, 0x3c3c3c3d
	v_mul_hi_u32 v19, v18, s22
	v_lshrrev_b32_e32 v22, 3, v19
	s_movk_i32 s22, 0xffde
	s_mov_b64 s[34:35], s[84:85]
	v_mul_lo_u32 v19, v22, s22
	v_add_u32_e32 v35, s24, v22
	s_movk_i32 s22, 0x154
	v_add3_u32 v23, s25, v18, v19
	v_cmp_gt_u32_e64 s[22:23], s22, v18
	v_cmp_gt_u32_e32 vcc, 64, v35
	s_and_b64 s[28:29], s[22:23], vcc
	v_cmp_gt_u32_e64 s[24:25], 64, v23
	s_and_b64 s[28:29], s[28:29], s[24:25]
	s_xor_b64 s[28:29], s[28:29], -1
	s_and_saveexec_b64 s[48:49], s[28:29]
	s_xor_b64 s[28:29], exec, s[48:49]
	s_or_saveexec_b64 s[28:29], s[28:29]
	v_mov_b64_e32 v[18:19], s[30:31]
	s_xor_b64 exec, exec, s[28:29]
	v_lshlrev_b32_e32 v18, 6, v35
	v_or3_b32 v18, v18, v34, v23
	v_ashrrev_i32_e32 v19, 31, v18
	v_lshlrev_b64 v[18:19], 7, v[18:19]
	v_lshl_add_u64 v[18:19], s[36:37], 0, v[18:19]
	v_lshlrev_b32_e32 v36, 1, v20
	v_mov_b32_e32 v37, 0
	v_lshl_add_u64 v[18:19], v[18:19], 0, v[36:37]
	s_or_b64 exec, exec, s[28:29]
	v_lshrrev_b32_e32 v122, 4, v1
	v_bitop3_b32 v35, v122, v0, 6 bitop3:0x78
	s_and_b32 s48, s52, 3
	v_lshl_or_b32 v29, v29, 6, s43
	s_movk_i32 s50, 0xdc0
	v_and_b32_e32 v121, 15, v0
	v_lshlrev_b32_e32 v35, 4, v35
	s_lshr_b32 s49, s42, 8
	v_and_or_b32 v29, v29, s50, v20
	s_mul_i32 s50, s48, 0x44
	v_lshl_or_b32 v35, v121, 7, v35
	v_add_u32_e32 v123, s50, v121
	v_lshl_or_b32 v35, s49, 13, v35
	s_lshl_b32 s50, s39, 10
	s_lshl_b32 s41, s38, 6
	v_add_u32_e32 v125, 0x18000, v35
	v_or_b32_e32 v35, s50, v120
	s_lshl_b32 s38, s38, 13
	v_readfirstlane_b32 s39, v35
	s_waitcnt lgkmcnt(0)
	s_add_u32 s38, s34, s38
	s_mul_hi_u32 s57, s42, 0x38e38e39
	s_mov_b32 m0, s39
	s_addc_u32 s39, s35, 0
	s_lshr_b32 s34, s57, 12
	s_mulk_i32 s34, 0xffc1
	s_add_i32 s34, s34, s49
	s_mul_i32 s34, s49, 3
	s_lshl_b32 s56, s52, 11
	s_ashr_i32 s35, s34, 31
	s_add_i32 s52, s56, 0x18000
	s_lshl_b64 s[34:35], s[34:35], 15
	s_add_u32 s34, s38, s34
	s_addc_u32 s35, s39, s35
	s_mul_i32 s54, s49, -5
	s_add_i32 s54, s54, 6
	s_mul_hi_u32 s55, s54, 0x38e38e4
	s_mulk_i32 s55, 0xffc1
	s_add_i32 s54, s55, s54
	v_mov_b64_e32 v[194:195], v[18:19]
	global_load_lds_dwordx4 v[18:19], off
	v_lshlrev_b32_e32 v18, 1, v29
	v_mov_b32_e32 v19, 0
	s_mov_b32 m0, s52
	s_ashr_i32 s55, s54, 31
	v_lshl_add_u64 v[36:37], s[34:35], 0, v[18:19]
	global_load_lds_dwordx4 v18, s[34:35]
	s_mov_b64 s[34:35], 0x400
	s_add_i32 m0, s56, 0x18400
	s_lshl_b64 s[54:55], s[54:55], 15
	v_lshl_add_u64 v[36:37], v[36:37], 0, s[34:35]
	s_add_u32 s54, s38, s54
	global_load_lds_dwordx4 v[36:37], off
	s_addc_u32 s55, s39, s55
	s_add_i32 m0, s56, 0x1c000
	v_lshl_add_u64 v[36:37], s[54:55], 0, v[18:19]
	global_load_lds_dwordx4 v18, s[54:55]
	s_mul_i32 s54, s49, 3
	s_add_i32 s54, s54, 4
	s_mul_hi_u32 s55, s54, 0x38e38e4
	s_mulk_i32 s55, 0xffc1
	s_add_i32 s54, s55, s54
	s_ashr_i32 s55, s54, 31
	s_add_i32 m0, s56, 0x1c400
	s_lshl_b64 s[54:55], s[54:55], 15
	s_add_u32 s54, s38, s54
	v_lshl_add_u64 v[36:37], v[36:37], 0, s[34:35]
	s_addc_u32 s55, s39, s55
	global_load_lds_dwordx4 v[36:37], off
	s_add_i32 m0, s56, 0x20000
	v_lshl_add_u64 v[36:37], s[54:55], 0, v[18:19]
	global_load_lds_dwordx4 v18, s[54:55]
	v_lshl_add_u64 v[36:37], v[36:37], 0, s[34:35]
	s_add_i32 m0, s56, 0x20400
	s_lshr_b32 s54, s57, 9
	global_load_lds_dwordx4 v[36:37], off
	s_mul_i32 s54, s54, -9
	s_add_i32 s54, s54, s49
	s_mul_hi_i32 s55, s54, 0x55555556
	s_lshr_b32 s56, s55, 31
	s_add_i32 s55, s55, s56
	s_mul_i32 s55, s55, 31
	s_add_i32 s55, s55, s54
	s_bitcmp1_b32 s57, 9
	s_waitcnt vmcnt(4) lgkmcnt(0)
	s_barrier
	s_cselect_b32 s54, 0xc000, 0
	ds_read_b128 v[62:65], v125
	v_add_u32_e32 v29, s55, v123
	v_add_u32_e32 v124, 34, v123
	ds_read_b128 v[58:61], v125 offset:2048
	v_bitop3_b32 v35, v29, v122, 6 bitop3:0x6c
	v_lshl_add_u32 v29, v29, 7, s54
	v_lshl_or_b32 v139, v35, 4, v29
	ds_read_b128 v[70:73], v139
	v_add_u32_e32 v29, s55, v124
	ds_read_b128 v[66:69], v139 offset:2048
	v_bitop3_b32 v35, v29, v122, 6 bitop3:0x6c
	v_lshl_add_u32 v29, v29, 7, s54
	v_lshl_or_b32 v140, v35, 4, v29
	ds_read_b128 v[82:85], v140
	s_load_dwordx2 s[28:29], s[0:1], 0x20
	ds_read_b128 v[78:81], v140 offset:2048
	ds_read_b128 v[90:93], v125 offset:4096
	ds_read_b128 v[86:89], v125 offset:6144
	v_add_u32_e32 v127, s33, v21
	v_lshlrev_b32_e32 v20, 1, v20
	v_mov_b32_e32 v21, v19
	v_xor_b32_e32 v126, 64, v125
	s_mov_b32 s51, 0
	s_mov_b32 s53, 1
	v_add_u32_e32 v128, v34, v24
	v_lshl_add_u64 v[114:115], s[36:37], 0, v[20:21]
	v_add_u32_e32 v129, s33, v25
	v_add_u32_e32 v130, v34, v26
	v_add_u32_e32 v131, s33, v27
	v_add_u32_e32 v132, v34, v28
	v_add_u32_e32 v133, s33, v30
	v_add_u32_e32 v134, v34, v31
	v_add_u32_e32 v135, s33, v32
	v_add_u32_e32 v136, v34, v33
	v_add_u32_e32 v137, s33, v22
	v_add_u32_e32 v138, v34, v23
	v_lshl_add_u64 v[116:117], s[38:39], 0, v[18:19]
	s_mov_b64 s[36:37], 0
	s_mov_b32 s38, 0
	s_mov_b32 s39, 0
	v_mov_b32_e32 v18, v19
	v_mov_b32_e32 v20, v19
	v_mov_b32_e32 v22, v19
	v_mov_b32_e32 v23, v19
	v_mov_b32_e32 v24, v19
	v_mov_b32_e32 v25, v19
	v_mov_b32_e32 v26, v19
	v_mov_b32_e32 v27, v19
	v_mov_b32_e32 v28, v19
	v_mov_b32_e32 v29, v19
	v_mov_b32_e32 v42, v19
	v_mov_b32_e32 v43, v19
	v_mov_b32_e32 v44, v19
	v_mov_b32_e32 v45, v19
	v_mov_b32_e32 v50, v19
	v_mov_b32_e32 v51, v19
	v_mov_b32_e32 v52, v19
	v_mov_b32_e32 v53, v19
	v_mov_b32_e32 v54, v19
	v_mov_b32_e32 v55, v19
	v_mov_b32_e32 v56, v19
	v_mov_b32_e32 v57, v19
	v_mov_b32_e32 v74, v19
	v_mov_b32_e32 v75, v19
	v_mov_b32_e32 v76, v19
	v_mov_b32_e32 v77, v19
	v_mov_b32_e32 v94, v19
	v_mov_b32_e32 v95, v19
	v_mov_b32_e32 v96, v19
	v_mov_b32_e32 v97, v19
	v_mov_b32_e32 v98, v19
	v_mov_b32_e32 v99, v19
	v_mov_b32_e32 v100, v19
	v_mov_b32_e32 v101, v19
	v_mov_b32_e32 v102, v19
	v_mov_b32_e32 v103, v19
	v_mov_b32_e32 v104, v19
	v_mov_b32_e32 v105, v19
	v_mov_b32_e32 v106, v19
	v_mov_b32_e32 v107, v19
	v_mov_b32_e32 v108, v19
	v_mov_b32_e32 v109, v19
	v_mov_b32_e32 v110, v19
	v_mov_b32_e32 v111, v19
	v_mov_b32_e32 v112, v19
	v_mov_b32_e32 v113, v19
	v_mov_b32_e32 v46, v19
	v_mov_b32_e32 v47, v19
	v_mov_b32_e32 v48, v19
	v_mov_b32_e32 v49, v19
	v_mov_b32_e32 v30, v19
	v_mov_b32_e32 v31, v19
	v_mov_b32_e32 v32, v19
	v_mov_b32_e32 v33, v19
	v_mov_b32_e32 v38, v19
	v_mov_b32_e32 v39, v19
	v_mov_b32_e32 v40, v19
	v_mov_b32_e32 v41, v19
	v_mov_b32_e32 v34, v19
	v_mov_b32_e32 v35, v19
	v_mov_b32_e32 v36, v19
	v_mov_b32_e32 v37, v19
	v_mov_b32_e32 v202, 0x80000
	v_cmp_ne_u64_e64 s[76:77], v[184:185], s[30:31]
	s_nop 1
	v_cndmask_b32_e64 v196, 0, v202, s[76:77]
	v_cmp_ne_u64_e64 s[76:77], v[186:187], s[30:31]
	s_nop 1
	v_cndmask_b32_e64 v197, 0, v202, s[76:77]
	v_cmp_ne_u64_e64 s[76:77], v[188:189], s[30:31]
	s_nop 1
	v_cndmask_b32_e64 v198, 0, v202, s[76:77]
	v_cmp_ne_u64_e64 s[76:77], v[190:191], s[30:31]
	s_nop 1
	v_cndmask_b32_e64 v199, 0, v202, s[76:77]
	v_cmp_ne_u64_e64 s[76:77], v[192:193], s[30:31]
	s_nop 1
	v_cndmask_b32_e64 v200, 0, v202, s[76:77]
	v_cmp_ne_u64_e64 s[76:77], v[194:195], s[30:31]
	s_nop 1
	v_cndmask_b32_e64 v201, 0, v202, s[76:77]
	s_mov_b32 s61, 0
	s_mov_b32 s78, 0
	s_mov_b32 s67, 0
	s_mov_b32 s69, 0
	s_mov_b32 s80, 0xc000
	s_lshl_b32 s81, s49, 6
	s_lshl_b32 s79, s49, 13
	v_subrev_u32_e32 v204, s79, v125
	v_xor_b32_e32 v204, s81, v204
	v_add_u32_e32 v205, 0x2000, v204
	v_mov_b32_e32 v174, v205
	v_mov_b32_e32 v182, v123
	v_bitop3_b32 v183, v182, v122, 6 bitop3:0x6c
	v_lshl_add_u32 v182, v182, 7, 0
	v_lshl_or_b32 v176, v183, 4, v182
	v_xor_b32_e32 v176, s81, v176
	v_add_u32_e32 v182, 34, v123
	v_bitop3_b32 v183, v182, v122, 6 bitop3:0x6c
	v_lshl_add_u32 v182, v182, 7, 0
	v_lshl_or_b32 v177, v183, 4, v182
	v_xor_b32_e32 v177, s81, v177
	ds_read_b128 v[62:65], v204
	ds_read_b128 v[58:61], v204 offset:2048
	ds_read_b128 v[90:93], v204 offset:4096
	ds_read_b128 v[86:89], v204 offset:6144
	ds_read_b128 v[70:73], v176
	ds_read_b128 v[66:69], v176 offset:2048
	ds_read_b128 v[82:85], v177
	ds_read_b128 v[78:81], v177 offset:2048
	s_waitcnt lgkmcnt(0)

.LBB7_39:
	s_cmpk_gt_u32 s42, 0xff
	s_waitcnt vmcnt(0) lgkmcnt(0)
	s_barrier
	s_cbranch_scc1 .LBB7_41
	ds_read_b128 v[58:61], v1
	ds_read_b128 v[62:65], v1 offset:1024
	ds_read_b128 v[66:69], v1 offset:2048
	s_mov_b32 s0, s88
	s_and_b32 s1, s42, 0xc0
	s_waitcnt lgkmcnt(0)
	v_pk_add_f32 v[70:71], v[60:61], v[112:113]
	v_pk_add_f32 v[72:73], v[58:59], v[110:111]
	v_pk_add_f32 v[78:79], v[64:65], v[108:109]
	ds_read_b128 v[58:61], v1 offset:3072
	v_pk_add_f32 v[80:81], v[62:63], v[106:107]
	ds_read_b128 v[62:65], v1 offset:4096
	v_pk_add_f32 v[82:83], v[68:69], v[104:105]
	v_pk_add_f32 v[84:85], v[66:67], v[102:103]
	s_waitcnt lgkmcnt(1)
	v_pk_add_f32 v[86:87], v[60:61], v[100:101]
	ds_read_b128 v[66:69], v1 offset:5120
	v_pk_add_f32 v[88:89], v[58:59], v[98:99]
	s_waitcnt lgkmcnt(1)
	v_pk_add_f32 v[90:91], v[64:65], v[96:97]
	ds_read_b128 v[58:61], v1 offset:6144
	v_pk_add_f32 v[92:93], v[62:63], v[94:95]
	ds_read_b128 v[62:65], v1 offset:7168
	s_waitcnt lgkmcnt(2)
	v_pk_add_f32 v[76:77], v[68:69], v[76:77]
	v_pk_add_f32 v[74:75], v[66:67], v[74:75]
	s_waitcnt lgkmcnt(1)
	v_pk_add_f32 v[94:95], v[60:61], v[56:57]
	ds_read_b128 v[66:69], v1 offset:8192
	v_pk_add_f32 v[96:97], v[58:59], v[54:55]
	s_waitcnt lgkmcnt(1)
	v_pk_add_f32 v[64:65], v[64:65], v[52:53]
	ds_read_b128 v[52:55], v1 offset:9216
	ds_read_b128 v[56:59], v1 offset:10240
	v_pk_add_f32 v[98:99], v[62:63], v[50:51]
	ds_read_b128 v[60:63], v1 offset:11264
	s_waitcnt lgkmcnt(3)
	v_pk_add_f32 v[66:67], v[66:67], v[42:43]
	s_waitcnt lgkmcnt(2)
	v_pk_add_f32 v[102:103], v[52:53], v[26:27]
	s_waitcnt lgkmcnt(1)
	v_pk_add_f32 v[52:53], v[58:59], v[24:25]
	ds_read_b128 v[24:27], v1 offset:12288
	s_waitcnt lgkmcnt(1)
	v_pk_add_f32 v[42:43], v[62:63], v[20:21]
	v_pk_add_f32 v[50:51], v[60:61], v[18:19]
	ds_read_b128 v[18:21], v1 offset:13312
	v_pk_add_f32 v[68:69], v[68:69], v[44:45]
	v_pk_add_f32 v[100:101], v[54:55], v[28:29]
	v_pk_add_f32 v[58:59], v[56:57], v[22:23]
	s_waitcnt lgkmcnt(1)
	v_pk_add_f32 v[28:29], v[26:27], v[48:49]
	ds_read_b128 v[54:57], v1 offset:14336
	v_pk_add_f32 v[44:45], v[24:25], v[46:47]
	ds_read_b128 v[46:49], v1 offset:15360
	v_or_b32_e32 v1, s1, v121
	s_waitcnt lgkmcnt(2)
	v_pk_add_f32 v[26:27], v[20:21], v[32:33]
	v_lshlrev_b32_e32 v32, 3, v122
	v_mul_u32_u24_e32 v1, 0x90, v1
	s_mov_b32 s1, 0x10000
	v_add3_u32 v1, v1, v32, s1
	v_pk_fma_f32 v[32:33], s[0:1], v[72:73], v[14:15] op_sel_hi:[0,1,1]
	s_waitcnt lgkmcnt(0)
	v_pk_add_f32 v[20:21], v[46:47], v[34:35]
	v_pk_mul_f32 v[34:35], s[26:27], v[32:33] op_sel_hi:[0,1]
	v_cmp_le_f32_e32 vcc, 0, v33
	v_pk_add_f32 v[30:31], v[18:19], v[30:31]
	v_pk_add_f32 v[18:19], v[48:49], v[36:37]
	v_cndmask_b32_e32 v33, v35, v33, vcc
	v_cmp_le_f32_e32 vcc, 0, v32
	v_pk_add_f32 v[24:25], v[54:55], v[38:39]
	v_pk_add_f32 v[22:23], v[56:57], v[40:41]
	v_cndmask_b32_e32 v32, v34, v32, vcc
	v_pk_fma_f32 v[34:35], s[0:1], v[70:71], v[16:17] op_sel_hi:[0,1,1]
	v_pk_mul_f32 v[36:37], s[26:27], v[34:35] op_sel_hi:[0,1]
	v_cmp_le_f32_e32 vcc, 0, v35
	v_cvt_pk_f16_f32 v32, v32, v33
	v_add_u32_e32 v40, 0x800, v1
	v_cndmask_b32_e32 v33, v37, v35, vcc
	v_cmp_le_f32_e32 vcc, 0, v34
	s_nop 1
	v_cndmask_b32_e32 v34, v36, v34, vcc
	v_cvt_pk_f16_f32 v33, v34, v33
	v_pk_fma_f32 v[34:35], s[0:1], v[80:81], v[10:11] op_sel_hi:[0,1,1]
	v_pk_mul_f32 v[36:37], s[26:27], v[34:35] op_sel_hi:[0,1]
	v_cmp_le_f32_e32 vcc, 0, v35
	s_nop 1
	v_cndmask_b32_e32 v35, v37, v35, vcc
	v_cmp_le_f32_e32 vcc, 0, v34
	s_nop 1
	v_cndmask_b32_e32 v34, v36, v34, vcc
	v_pk_fma_f32 v[36:37], s[0:1], v[78:79], v[12:13] op_sel_hi:[0,1,1]
	v_pk_mul_f32 v[38:39], s[26:27], v[36:37] op_sel_hi:[0,1]
	v_cmp_le_f32_e32 vcc, 0, v37
	v_cvt_pk_f16_f32 v34, v34, v35
	s_nop 0
	v_cndmask_b32_e32 v35, v39, v37, vcc
	v_cmp_le_f32_e32 vcc, 0, v36
	s_nop 1
	v_cndmask_b32_e32 v36, v38, v36, vcc
	v_cvt_pk_f16_f32 v35, v36, v35
	ds_write2_b64 v1, v[32:33], v[34:35] offset1:4
	v_pk_fma_f32 v[32:33], s[0:1], v[84:85], v[6:7] op_sel_hi:[0,1,1]
	v_pk_mul_f32 v[34:35], s[26:27], v[32:33] op_sel_hi:[0,1]
	v_cmp_le_f32_e32 vcc, 0, v33
	s_nop 1
	v_cndmask_b32_e32 v33, v35, v33, vcc
	v_cmp_le_f32_e32 vcc, 0, v32
	s_nop 1
	v_cndmask_b32_e32 v32, v34, v32, vcc
	v_pk_fma_f32 v[34:35], s[0:1], v[82:83], v[8:9] op_sel_hi:[0,1,1]
	v_pk_mul_f32 v[36:37], s[26:27], v[34:35] op_sel_hi:[0,1]
	v_cmp_le_f32_e32 vcc, 0, v35
	v_cvt_pk_f16_f32 v32, v32, v33
	s_nop 0
	v_cndmask_b32_e32 v33, v37, v35, vcc
	v_cmp_le_f32_e32 vcc, 0, v34
	s_nop 1
	v_cndmask_b32_e32 v34, v36, v34, vcc
	v_cvt_pk_f16_f32 v33, v34, v33
	v_pk_fma_f32 v[34:35], s[0:1], v[88:89], v[2:3] op_sel_hi:[0,1,1]
	v_pk_mul_f32 v[36:37], s[26:27], v[34:35] op_sel_hi:[0,1]
	v_cmp_le_f32_e32 vcc, 0, v35
	s_nop 1
	v_cndmask_b32_e32 v35, v37, v35, vcc
	v_cmp_le_f32_e32 vcc, 0, v34
	s_nop 1
	v_cndmask_b32_e32 v34, v36, v34, vcc
	v_pk_fma_f32 v[36:37], s[0:1], v[86:87], v[4:5] op_sel_hi:[0,1,1]
	v_pk_mul_f32 v[38:39], s[26:27], v[36:37] op_sel_hi:[0,1]
	v_cmp_le_f32_e32 vcc, 0, v37
	v_cvt_pk_f16_f32 v34, v34, v35
	s_nop 0
	v_cndmask_b32_e32 v35, v39, v37, vcc
	v_cmp_le_f32_e32 vcc, 0, v36
	s_nop 1
	v_cndmask_b32_e32 v36, v38, v36, vcc
	v_cvt_pk_f16_f32 v35, v36, v35
	ds_write2_b64 v1, v[32:33], v[34:35] offset0:8 offset1:12
	v_pk_fma_f32 v[32:33], s[0:1], v[92:93], v[14:15] op_sel_hi:[0,1,1]
	v_pk_mul_f32 v[34:35], s[26:27], v[32:33] op_sel_hi:[0,1]
	v_cmp_le_f32_e32 vcc, 0, v33
	s_nop 1
	v_cndmask_b32_e32 v33, v35, v33, vcc
	v_cmp_le_f32_e32 vcc, 0, v32
	s_nop 1
	v_cndmask_b32_e32 v32, v34, v32, vcc
	v_pk_fma_f32 v[34:35], s[0:1], v[90:91], v[16:17] op_sel_hi:[0,1,1]
	v_pk_mul_f32 v[36:37], s[26:27], v[34:35] op_sel_hi:[0,1]
	v_cmp_le_f32_e32 vcc, 0, v35
	v_cvt_pk_f16_f32 v32, v32, v33
	s_nop 0
	v_cndmask_b32_e32 v33, v37, v35, vcc
	v_cmp_le_f32_e32 vcc, 0, v34
	s_nop 1
	v_cndmask_b32_e32 v34, v36, v34, vcc
	v_cvt_pk_f16_f32 v33, v34, v33
	v_pk_fma_f32 v[34:35], s[0:1], v[74:75], v[10:11] op_sel_hi:[0,1,1]
	v_pk_mul_f32 v[36:37], s[26:27], v[34:35] op_sel_hi:[0,1]
	v_cmp_le_f32_e32 vcc, 0, v35
	s_nop 1
	v_cndmask_b32_e32 v35, v37, v35, vcc
	v_cmp_le_f32_e32 vcc, 0, v34
	s_nop 1
	v_cndmask_b32_e32 v34, v36, v34, vcc
	v_pk_fma_f32 v[36:37], s[0:1], v[76:77], v[12:13] op_sel_hi:[0,1,1]
	v_pk_mul_f32 v[38:39], s[26:27], v[36:37] op_sel_hi:[0,1]
	v_cmp_le_f32_e32 vcc, 0, v37
	v_cvt_pk_f16_f32 v34, v34, v35
	s_nop 0
	v_cndmask_b32_e32 v35, v39, v37, vcc
	v_cmp_le_f32_e32 vcc, 0, v36
	s_nop 1
	v_cndmask_b32_e32 v36, v38, v36, vcc
	v_cvt_pk_f16_f32 v35, v36, v35
	ds_write2_b64 v40, v[32:33], v[34:35] offset0:32 offset1:36
	v_pk_fma_f32 v[32:33], s[0:1], v[96:97], v[6:7] op_sel_hi:[0,1,1]
	v_pk_mul_f32 v[34:35], s[26:27], v[32:33] op_sel_hi:[0,1]
	v_cmp_le_f32_e32 vcc, 0, v33
	s_nop 1
	v_cndmask_b32_e32 v33, v35, v33, vcc
	v_cmp_le_f32_e32 vcc, 0, v32
	s_nop 1
	v_cndmask_b32_e32 v32, v34, v32, vcc
	v_pk_fma_f32 v[34:35], s[0:1], v[94:95], v[8:9] op_sel_hi:[0,1,1]
	v_pk_mul_f32 v[36:37], s[26:27], v[34:35] op_sel_hi:[0,1]
	v_cmp_le_f32_e32 vcc, 0, v35
	v_cvt_pk_f16_f32 v32, v32, v33
	s_nop 0
	v_cndmask_b32_e32 v33, v37, v35, vcc
	v_cmp_le_f32_e32 vcc, 0, v34
	s_nop 1
	v_cndmask_b32_e32 v34, v36, v34, vcc
	v_cvt_pk_f16_f32 v33, v34, v33
	v_pk_fma_f32 v[34:35], s[0:1], v[98:99], v[2:3] op_sel_hi:[0,1,1]
	v_pk_mul_f32 v[36:37], s[26:27], v[34:35] op_sel_hi:[0,1]
	v_cmp_le_f32_e32 vcc, 0, v35
	s_nop 1
	v_cndmask_b32_e32 v35, v37, v35, vcc
	v_cmp_le_f32_e32 vcc, 0, v34
	s_nop 1
	v_cndmask_b32_e32 v34, v36, v34, vcc
	v_pk_fma_f32 v[36:37], s[0:1], v[64:65], v[4:5] op_sel_hi:[0,1,1]
	v_pk_mul_f32 v[38:39], s[26:27], v[36:37] op_sel_hi:[0,1]
	v_cmp_le_f32_e32 vcc, 0, v37
	v_cvt_pk_f16_f32 v34, v34, v35
	s_nop 0
	v_cndmask_b32_e32 v35, v39, v37, vcc
	v_cmp_le_f32_e32 vcc, 0, v36
	s_nop 1
	v_cndmask_b32_e32 v36, v38, v36, vcc
	v_cvt_pk_f16_f32 v35, v36, v35
	ds_write2_b64 v40, v[32:33], v[34:35] offset0:40 offset1:44
	v_pk_fma_f32 v[32:33], s[0:1], v[66:67], v[14:15] op_sel_hi:[0,1,1]
	v_pk_mul_f32 v[34:35], s[26:27], v[32:33] op_sel_hi:[0,1]
	v_cmp_le_f32_e32 vcc, 0, v33
	v_add_u32_e32 v40, 0x1000, v1
	v_pk_fma_f32 v[14:15], s[0:1], v[44:45], v[14:15] op_sel_hi:[0,1,1]
	v_cndmask_b32_e32 v33, v35, v33, vcc
	v_cmp_le_f32_e32 vcc, 0, v32
	v_add_u32_e32 v1, 0x1800, v1
	s_nop 0
	v_cndmask_b32_e32 v32, v34, v32, vcc
	v_pk_fma_f32 v[34:35], s[0:1], v[68:69], v[16:17] op_sel_hi:[0,1,1]
	v_pk_mul_f32 v[36:37], s[26:27], v[34:35] op_sel_hi:[0,1]
	v_cmp_le_f32_e32 vcc, 0, v35
	v_cvt_pk_f16_f32 v32, v32, v33
	v_pk_fma_f32 v[16:17], s[0:1], v[28:29], v[16:17] op_sel_hi:[0,1,1]
	v_cndmask_b32_e32 v33, v37, v35, vcc
	v_cmp_le_f32_e32 vcc, 0, v34
	v_pk_mul_f32 v[28:29], s[26:27], v[16:17] op_sel_hi:[0,1]
	s_nop 0
	v_cndmask_b32_e32 v34, v36, v34, vcc
	v_cvt_pk_f16_f32 v33, v34, v33
	v_pk_fma_f32 v[34:35], s[0:1], v[102:103], v[10:11] op_sel_hi:[0,1,1]
	v_pk_mul_f32 v[36:37], s[26:27], v[34:35] op_sel_hi:[0,1]
	v_cmp_le_f32_e32 vcc, 0, v35
	v_pk_fma_f32 v[10:11], s[0:1], v[30:31], v[10:11] op_sel_hi:[0,1,1]
	s_nop 0
	v_cndmask_b32_e32 v35, v37, v35, vcc
	v_cmp_le_f32_e32 vcc, 0, v34
	s_nop 1
	v_cndmask_b32_e32 v34, v36, v34, vcc
	v_pk_fma_f32 v[36:37], s[0:1], v[100:101], v[12:13] op_sel_hi:[0,1,1]
	v_pk_mul_f32 v[38:39], s[26:27], v[36:37] op_sel_hi:[0,1]
	v_cmp_le_f32_e32 vcc, 0, v37
	v_cvt_pk_f16_f32 v34, v34, v35
	v_pk_fma_f32 v[12:13], s[0:1], v[26:27], v[12:13] op_sel_hi:[0,1,1]
	v_cndmask_b32_e32 v35, v39, v37, vcc
	v_cmp_le_f32_e32 vcc, 0, v36
	s_nop 1
	v_cndmask_b32_e32 v36, v38, v36, vcc
	v_cvt_pk_f16_f32 v35, v36, v35
	ds_write2_b64 v40, v[32:33], v[34:35] offset0:64 offset1:68
	v_pk_fma_f32 v[32:33], s[0:1], v[58:59], v[6:7] op_sel_hi:[0,1,1]
	v_pk_mul_f32 v[34:35], s[26:27], v[32:33] op_sel_hi:[0,1]
	v_cmp_le_f32_e32 vcc, 0, v33
	v_pk_fma_f32 v[6:7], s[0:1], v[24:25], v[6:7] op_sel_hi:[0,1,1]
	s_nop 0
	v_cndmask_b32_e32 v33, v35, v33, vcc
	v_cmp_le_f32_e32 vcc, 0, v32
	s_nop 1
	v_cndmask_b32_e32 v32, v34, v32, vcc
	v_pk_fma_f32 v[34:35], s[0:1], v[52:53], v[8:9] op_sel_hi:[0,1,1]
	v_pk_mul_f32 v[36:37], s[26:27], v[34:35] op_sel_hi:[0,1]
	v_cmp_le_f32_e32 vcc, 0, v35
	v_cvt_pk_f16_f32 v32, v32, v33
	v_pk_fma_f32 v[8:9], s[0:1], v[22:23], v[8:9] op_sel_hi:[0,1,1]
	v_cndmask_b32_e32 v33, v37, v35, vcc
	v_cmp_le_f32_e32 vcc, 0, v34
	s_nop 1
	v_cndmask_b32_e32 v34, v36, v34, vcc
	v_cvt_pk_f16_f32 v33, v34, v33
	v_pk_fma_f32 v[34:35], s[0:1], v[50:51], v[2:3] op_sel_hi:[0,1,1]
	v_pk_mul_f32 v[36:37], s[26:27], v[34:35] op_sel_hi:[0,1]
	v_cmp_le_f32_e32 vcc, 0, v35
	v_pk_fma_f32 v[2:3], s[0:1], v[20:21], v[2:3] op_sel_hi:[0,1,1]
	s_nop 0
	v_cndmask_b32_e32 v35, v37, v35, vcc
	v_cmp_le_f32_e32 vcc, 0, v34
	s_nop 1
	v_cndmask_b32_e32 v34, v36, v34, vcc
	v_pk_fma_f32 v[36:37], s[0:1], v[42:43], v[4:5] op_sel_hi:[0,1,1]
	v_pk_mul_f32 v[38:39], s[26:27], v[36:37] op_sel_hi:[0,1]
	v_cmp_le_f32_e32 vcc, 0, v37
	v_cvt_pk_f16_f32 v34, v34, v35
	v_pk_fma_f32 v[4:5], s[0:1], v[18:19], v[4:5] op_sel_hi:[0,1,1]
	v_cndmask_b32_e32 v35, v39, v37, vcc
	v_cmp_le_f32_e32 vcc, 0, v36
	s_nop 1
	v_cndmask_b32_e32 v36, v38, v36, vcc
	v_cvt_pk_f16_f32 v35, v36, v35
	ds_write2_b64 v40, v[32:33], v[34:35] offset0:72 offset1:76
	v_pk_mul_f32 v[32:33], s[26:27], v[14:15] op_sel_hi:[0,1]
	v_cmp_le_f32_e32 vcc, 0, v15
	s_nop 1
	v_cndmask_b32_e32 v15, v33, v15, vcc
	v_cmp_le_f32_e32 vcc, 0, v14
	s_nop 1
	v_cndmask_b32_e32 v14, v32, v14, vcc
	v_cmp_le_f32_e32 vcc, 0, v17
	v_cvt_pk_f16_f32 v14, v14, v15
	s_nop 0
	v_cndmask_b32_e32 v15, v29, v17, vcc
	v_cmp_le_f32_e32 vcc, 0, v16
	s_nop 1
	v_cndmask_b32_e32 v16, v28, v16, vcc
	v_cvt_pk_f16_f32 v15, v16, v15
	v_pk_mul_f32 v[16:17], s[26:27], v[10:11] op_sel_hi:[0,1]
	v_cmp_le_f32_e32 vcc, 0, v11
	s_nop 1
	v_cndmask_b32_e32 v11, v17, v11, vcc
	v_cmp_le_f32_e32 vcc, 0, v10
	s_nop 1
	v_cndmask_b32_e32 v10, v16, v10, vcc
	v_pk_mul_f32 v[16:17], s[26:27], v[12:13] op_sel_hi:[0,1]
	v_cmp_le_f32_e32 vcc, 0, v13
	v_cvt_pk_f16_f32 v10, v10, v11
	s_nop 0
	v_cndmask_b32_e32 v11, v17, v13, vcc
	v_cmp_le_f32_e32 vcc, 0, v12
	s_nop 1
	v_cndmask_b32_e32 v12, v16, v12, vcc
	v_cvt_pk_f16_f32 v11, v12, v11
	ds_write2_b64 v1, v[14:15], v[10:11] offset0:96 offset1:100
	v_pk_mul_f32 v[10:11], s[26:27], v[6:7] op_sel_hi:[0,1]
	v_cmp_le_f32_e32 vcc, 0, v7
	s_nop 1
	v_cndmask_b32_e32 v7, v11, v7, vcc
	v_cmp_le_f32_e32 vcc, 0, v6
	s_nop 1
	v_cndmask_b32_e32 v6, v10, v6, vcc
	v_pk_mul_f32 v[10:11], s[26:27], v[8:9] op_sel_hi:[0,1]
	v_cmp_le_f32_e32 vcc, 0, v9
	v_cvt_pk_f16_f32 v6, v6, v7
	s_nop 0
	v_cndmask_b32_e32 v7, v11, v9, vcc
	v_cmp_le_f32_e32 vcc, 0, v8
	s_nop 1
	v_cndmask_b32_e32 v8, v10, v8, vcc
	v_cvt_pk_f16_f32 v7, v8, v7
	v_pk_mul_f32 v[8:9], s[26:27], v[2:3] op_sel_hi:[0,1]
	v_cmp_le_f32_e32 vcc, 0, v3
	s_nop 1
	v_cndmask_b32_e32 v3, v9, v3, vcc
	v_cmp_le_f32_e32 vcc, 0, v2
	s_nop 1
	v_cndmask_b32_e32 v2, v8, v2, vcc
	v_pk_mul_f32 v[8:9], s[26:27], v[4:5] op_sel_hi:[0,1]
	v_cmp_le_f32_e32 vcc, 0, v5
	v_cvt_pk_f16_f32 v2, v2, v3
	s_nop 0
	v_cndmask_b32_e32 v3, v9, v5, vcc
	v_cmp_le_f32_e32 vcc, 0, v4
	s_nop 1
	v_cndmask_b32_e32 v4, v8, v4, vcc
	v_cvt_pk_f16_f32 v3, v4, v3
	ds_write2_b64 v1, v[6:7], v[2:3] offset0:104 offset1:108

_Z6conv_kILi256ELi128ELi3ELi64ELi1ELi2ELb0EEvPKDF16_S1_PKfS3_PDF16_S4_S1_fS3_S3_S3_S3_:
	s_lshl_b32 s3, s2, 3
	s_and_b32 s3, s3, 56
	s_ashr_i32 s4, s2, 5
	s_add_i32 s4, s3, s4
	v_readfirstlane_b32 s28, v0
	v_bfe_u32 v8, v0, 3, 3
	s_lshl_b32 s3, s4, 2
	v_and_b32_e32 v1, 7, v0
	s_and_b32 s24, s3, 56
	s_lshr_b32 s3, s28, 6
	v_bitop3_b32 v2, v8, v1, 6 bitop3:0x6c
	s_ashr_i32 s26, s4, 4
	v_lshlrev_b32_e32 v4, 3, v2
	v_lshl_or_b32 v2, s3, 3, v8
	s_mov_b32 s4, 0x1e1e1e1f
	s_load_dwordx2 s[18:19], s[0:1], 0x0
	s_load_dword s88, s[0:1], 0x38
	s_load_dwordx2 s[84:85], s[0:1], 0x8
	s_load_dwordx2 s[86:87], s[0:1], 0x28
	s_load_dwordx2 s[16:17], s[0:1], 0x30
	v_mul_hi_u32 v3, v2, s4
	s_and_b32 s25, s2, 32
	v_lshrrev_b32_e32 v3, 2, v3
	s_movk_i32 s6, 0xffde
	s_add_i32 s14, s24, -1
	v_mul_lo_u32 v5, v3, s6
	v_add_u32_e32 v30, s14, v3
	s_add_i32 s15, s25, -1
	s_movk_i32 s7, 0x154
	v_add3_u32 v31, s15, v2, v5
	v_cmp_gt_u32_e32 vcc, s7, v2
	v_cmp_gt_u32_e64 s[4:5], 64, v30
	s_bfe_u32 s27, s2, 0x10004
	s_and_b64 s[4:5], vcc, s[4:5]
	v_cmp_gt_u32_e32 vcc, 64, v31
	v_and_b32_e32 v112, 63, v0
	s_lshl_b32 s39, s27, 7
	s_and_b64 vcc, s[4:5], vcc
	s_waitcnt lgkmcnt(0)
	v_mov_b64_e32 v[6:7], s[16:17]
	v_lshlrev_b32_e32 v2, 1, v4
	s_and_saveexec_b64 s[4:5], vcc
	v_or_b32_e32 v3, s39, v30
	s_lshl_b32 s8, s26, 14
	v_lshlrev_b32_e32 v3, 6, v3
	v_or3_b32 v6, v3, s8, v31
	v_ashrrev_i32_e32 v7, 31, v6
	v_lshlrev_b64 v[6:7], 7, v[6:7]
	v_lshl_add_u64 v[6:7], s[18:19], 0, v[6:7]
	v_mov_b32_e32 v3, 0
	v_lshl_add_u64 v[6:7], v[6:7], 0, v[2:3]
	s_or_b64 exec, exec, s[4:5]
	s_lshl_b32 s37, s3, 10
	v_lshlrev_b32_e32 v5, 4, v112
	v_or_b32_e32 v3, s37, v5
	s_add_i32 s9, s3, 8
	v_readfirstlane_b32 s4, v3
	s_mov_b32 m0, s4
	v_lshl_or_b32 v3, s9, 3, v8
	global_load_lds_dwordx4 v[6:7], off
	s_mov_b32 s8, 0x3c3c3c3d
	v_mul_hi_u32 v6, v3, s8
	v_lshrrev_b32_e32 v6, 3, v6
	v_mul_lo_u32 v7, v6, s6
	v_add_u32_e32 v32, s14, v6
	v_add3_u32 v33, s15, v3, v7
	v_cmp_gt_u32_e64 s[4:5], s7, v3
	v_cmp_gt_u32_e64 s[6:7], 64, v32
	s_and_b64 s[6:7], s[4:5], s[6:7]
	v_cmp_gt_u32_e64 s[4:5], 64, v33
	s_and_b64 s[12:13], s[6:7], s[4:5]
	v_mov_b64_e32 v[6:7], s[16:17]
	s_and_saveexec_b64 s[4:5], s[12:13]
	v_or_b32_e32 v3, s39, v32
	s_lshl_b32 s6, s26, 14
	v_lshlrev_b32_e32 v3, 6, v3
	v_or3_b32 v6, v3, s6, v33
	v_ashrrev_i32_e32 v7, 31, v6
	v_lshlrev_b64 v[6:7], 7, v[6:7]
	v_lshl_add_u64 v[6:7], s[18:19], 0, v[6:7]
	v_mov_b32_e32 v3, 0
	v_lshl_add_u64 v[6:7], v[6:7], 0, v[2:3]
	s_or_b64 exec, exec, s[4:5]
	s_lshl_b32 s38, s9, 10
	v_or_b32_e32 v3, s38, v5
	s_add_i32 s10, s3, 16
	v_readfirstlane_b32 s4, v3
	s_mov_b32 m0, s4
	v_lshl_or_b32 v3, s10, 3, v8
	global_load_lds_dwordx4 v[6:7], off
	v_mul_hi_u32 v6, v3, s8
	v_lshrrev_b32_e32 v6, 3, v6
	s_movk_i32 s8, 0xffde
	v_mul_lo_u32 v7, v6, s8
	v_add_u32_e32 v42, s14, v6
	s_movk_i32 s9, 0x154
	v_add3_u32 v43, s15, v3, v7
	v_cmp_gt_u32_e64 s[4:5], s9, v3
	v_cmp_gt_u32_e64 s[6:7], 64, v42
	s_and_b64 s[6:7], s[4:5], s[6:7]
	v_cmp_gt_u32_e64 s[4:5], 64, v43
	s_and_b64 s[4:5], s[6:7], s[4:5]
	v_mov_b64_e32 v[6:7], s[16:17]
	s_and_saveexec_b64 s[6:7], s[4:5]
	v_or_b32_e32 v3, s39, v42
	s_lshl_b32 s11, s26, 14
	v_lshlrev_b32_e32 v3, 6, v3
	v_or3_b32 v6, v3, s11, v43
	v_ashrrev_i32_e32 v7, 31, v6
	v_lshlrev_b64 v[6:7], 7, v[6:7]
	v_lshl_add_u64 v[6:7], s[18:19], 0, v[6:7]
	v_mov_b32_e32 v3, 0
	v_lshl_add_u64 v[6:7], v[6:7], 0, v[2:3]
	s_or_b64 exec, exec, s[6:7]
	s_lshl_b32 s40, s10, 10
	v_or_b32_e32 v3, s40, v5
	s_add_i32 s11, s3, 24
	v_readfirstlane_b32 s6, v3
	s_mov_b32 m0, s6
	v_lshl_or_b32 v3, s11, 3, v8
	global_load_lds_dwordx4 v[6:7], off
	s_mov_b32 s10, 0x3c3c3c3d
	v_mul_hi_u32 v6, v3, s10
	v_lshrrev_b32_e32 v6, 3, v6
	v_mul_lo_u32 v7, v6, s8
	v_add_u32_e32 v44, s14, v6
	v_add3_u32 v45, s15, v3, v7
	v_cmp_gt_u32_e64 s[6:7], s9, v3
	v_cmp_gt_u32_e64 s[8:9], 64, v44
	s_and_b64 s[8:9], s[6:7], s[8:9]
	v_cmp_gt_u32_e64 s[6:7], 64, v45
	s_and_b64 s[6:7], s[8:9], s[6:7]
	v_mov_b64_e32 v[6:7], s[16:17]
	s_and_saveexec_b64 s[8:9], s[6:7]
	v_or_b32_e32 v3, s39, v44
	s_lshl_b32 s20, s26, 14
	v_lshlrev_b32_e32 v3, 6, v3
	v_or3_b32 v6, v3, s20, v45
	v_ashrrev_i32_e32 v7, 31, v6
	v_lshlrev_b64 v[6:7], 7, v[6:7]
	v_lshl_add_u64 v[6:7], s[18:19], 0, v[6:7]
	v_mov_b32_e32 v3, 0
	v_lshl_add_u64 v[6:7], v[6:7], 0, v[2:3]
	s_or_b64 exec, exec, s[8:9]
	s_lshl_b32 s41, s11, 10
	v_or_b32_e32 v3, s41, v5
	s_add_i32 s20, s3, 32
	v_readfirstlane_b32 s8, v3
	s_mov_b32 m0, s8
	v_lshl_or_b32 v3, s20, 3, v8
	global_load_lds_dwordx4 v[6:7], off
	v_mul_hi_u32 v6, v3, s10
	v_lshrrev_b32_e32 v6, 3, v6
	s_movk_i32 s22, 0xffde
	v_mul_lo_u32 v7, v6, s22
	v_add_u32_e32 v46, s14, v6
	s_movk_i32 s23, 0x154
	v_add3_u32 v47, s15, v3, v7
	v_cmp_gt_u32_e64 s[8:9], s23, v3
	v_cmp_gt_u32_e64 s[10:11], 64, v46
	s_and_b64 s[10:11], s[8:9], s[10:11]
	v_cmp_gt_u32_e64 s[8:9], 64, v47
	s_and_b64 s[8:9], s[10:11], s[8:9]
	v_mov_b64_e32 v[6:7], s[16:17]
	s_and_saveexec_b64 s[10:11], s[8:9]
	v_or_b32_e32 v3, s39, v46
	s_lshl_b32 s21, s26, 14
	v_lshlrev_b32_e32 v3, 6, v3
	v_or3_b32 v6, v3, s21, v47
	v_ashrrev_i32_e32 v7, 31, v6
	v_lshlrev_b64 v[6:7], 7, v[6:7]
	v_lshl_add_u64 v[6:7], s[18:19], 0, v[6:7]
	v_mov_b32_e32 v3, 0
	v_lshl_add_u64 v[6:7], v[6:7], 0, v[2:3]
	s_or_b64 exec, exec, s[10:11]
	s_lshl_b32 s42, s20, 10
	v_or_b32_e32 v2, s42, v5
	s_add_i32 s33, s3, 40
	v_readfirstlane_b32 s10, v2
	s_mov_b32 m0, s10
	v_lshl_or_b32 v2, s33, 3, v8
	global_load_lds_dwordx4 v[6:7], off
	s_mov_b32 s10, 0x3c3c3c3d
	v_mul_hi_u32 v3, v2, s10
	v_lshrrev_b32_e32 v3, 3, v3
	s_mov_b64 s[20:21], s[84:85]
	v_mul_lo_u32 v6, v3, s22
	v_add_u32_e32 v48, s14, v3
	v_add3_u32 v49, s15, v2, v6
	v_cmp_gt_u32_e64 s[10:11], s23, v2
	v_cmp_gt_u32_e64 s[14:15], 64, v48
	s_and_b64 s[14:15], s[10:11], s[14:15]
	v_cmp_gt_u32_e64 s[10:11], 64, v49
	s_and_b64 s[10:11], s[14:15], s[10:11]
	s_xor_b64 s[14:15], s[10:11], -1
	s_and_saveexec_b64 s[22:23], s[14:15]
	s_xor_b64 s[14:15], exec, s[22:23]
	s_lshl_b32 s29, s26, 14
	s_or_saveexec_b64 s[22:23], s[14:15]
	s_mov_b64 s[14:15], s[86:87]
	v_mov_b32_e32 v50, s29
	v_mov_b64_e32 v[2:3], s[16:17]
	s_xor_b64 exec, exec, s[22:23]
	s_cbranch_execz .LBB8_14
	v_or_b32_e32 v2, s39, v48
	s_lshl_b32 s29, s26, 14
	v_lshlrev_b32_e32 v2, 6, v2
	v_or3_b32 v2, v2, s29, v49
	v_ashrrev_i32_e32 v3, 31, v2
	v_lshlrev_b64 v[2:3], 7, v[2:3]
	v_lshl_add_u64 v[2:3], s[18:19], 0, v[2:3]
	v_lshlrev_b32_e32 v6, 1, v4
	v_mov_b32_e32 v7, 0
	v_lshl_add_u64 v[2:3], v[2:3], 0, v[6:7]
	v_mov_b32_e32 v50, s29

.LBB8_26:
	s_cmpk_gt_u32 s28, 0xff
	s_waitcnt vmcnt(0) lgkmcnt(0)
	s_barrier
	s_cbranch_scc1 .LBB8_28
	ds_read_b128 v[8:11], v6
	ds_read_b128 v[12:15], v6 offset:1024
	ds_read_b128 v[16:19], v6 offset:2048
	s_mov_b32 s0, s88
	s_and_b32 s1, s28, 0xc0
	s_waitcnt lgkmcnt(0)
	v_pk_add_f32 v[20:21], v[10:11], v[96:97]
	v_pk_add_f32 v[22:23], v[8:9], v[94:95]
	v_pk_add_f32 v[24:25], v[14:15], v[92:93]
	ds_read_b128 v[8:11], v6 offset:3072
	v_pk_add_f32 v[26:27], v[12:13], v[90:91]
	v_pk_add_f32 v[28:29], v[18:19], v[88:89]
	ds_read_b128 v[12:15], v6 offset:4096
	v_pk_add_f32 v[34:35], v[16:17], v[86:87]
	ds_read_b128 v[16:19], v6 offset:5120
	s_waitcnt lgkmcnt(2)
	v_pk_add_f32 v[36:37], v[10:11], v[84:85]
	v_pk_add_f32 v[38:39], v[8:9], v[82:83]
	s_waitcnt lgkmcnt(1)
	v_pk_add_f32 v[40:41], v[14:15], v[80:81]
	ds_read_b128 v[8:11], v6 offset:6144
	v_pk_add_f32 v[78:79], v[12:13], v[78:79]
	s_waitcnt lgkmcnt(1)
	v_pk_add_f32 v[76:77], v[18:19], v[76:77]
	ds_read_b128 v[12:15], v6 offset:7168
	v_pk_add_f32 v[74:75], v[16:17], v[74:75]
	ds_read_b128 v[16:19], v6 offset:8192
	s_waitcnt lgkmcnt(2)
	v_pk_add_f32 v[72:73], v[10:11], v[72:73]
	v_pk_add_f32 v[70:71], v[8:9], v[70:71]
	s_waitcnt lgkmcnt(1)
	v_pk_add_f32 v[68:69], v[14:15], v[68:69]
	ds_read_b128 v[8:11], v6 offset:9216
	v_pk_add_f32 v[66:67], v[12:13], v[66:67]
	s_waitcnt lgkmcnt(1)
	v_pk_add_f32 v[60:61], v[18:19], v[60:61]
	ds_read_b128 v[12:15], v6 offset:10240
	v_pk_add_f32 v[58:59], v[16:17], v[58:59]
	ds_read_b128 v[16:19], v6 offset:11264
	s_waitcnt lgkmcnt(2)
	v_pk_add_f32 v[44:45], v[10:11], v[44:45]
	v_pk_add_f32 v[42:43], v[8:9], v[42:43]
	ds_read_b128 v[8:11], v6 offset:12288
	s_waitcnt lgkmcnt(2)
	v_pk_add_f32 v[14:15], v[14:15], v[32:33]
	s_waitcnt lgkmcnt(1)
	v_pk_add_f32 v[18:19], v[18:19], v[4:5]
	v_pk_add_f32 v[16:17], v[16:17], v[2:3]
	ds_read_b128 v[2:5], v6 offset:13312
	v_pk_add_f32 v[30:31], v[12:13], v[30:31]
	s_waitcnt lgkmcnt(1)
	v_pk_add_f32 v[32:33], v[10:11], v[64:65]
	v_pk_add_f32 v[62:63], v[8:9], v[62:63]
	ds_read_b128 v[10:13], v6 offset:14336
	s_waitcnt lgkmcnt(1)
	v_pk_add_f32 v[2:3], v[2:3], v[46:47]
	v_or_b32_e32 v46, s1, v113
	v_lshlrev_b32_e32 v47, 3, v114
	v_mul_u32_u24_e32 v46, 0x90, v46
	s_mov_b32 s1, 0x10000
	v_add3_u32 v46, v46, v47, s1
	v_fma_mixlo_f16 v47, s0, v22, 0
	v_pk_mov_b32 v[22:23], v[22:23], v[20:21] op_sel:[1,0]
	v_fma_mixlo_f16 v21, s0, v21, 0
	v_pk_mul_f32 v[22:23], s[0:1], v[22:23] op_sel_hi:[0,1]
	v_cvt_pk_f16_f32 v22, v22, v23
	v_pack_b32_f16 v20, v47, v22
	v_alignbit_b32 v21, v21, v22, 16
	v_pk_mov_b32 v[22:23], v[26:27], v[24:25] op_sel:[1,0]
	v_fma_mixlo_f16 v47, s0, v26, 0
	v_pk_mul_f32 v[22:23], s[0:1], v[22:23] op_sel_hi:[0,1]
	v_cvt_pk_f16_f32 v23, v22, v23
	v_fma_mixlo_f16 v24, s0, v25, 0
	v_pack_b32_f16 v22, v47, v23
	v_alignbit_b32 v23, v24, v23, 16
	ds_write2_b64 v46, v[20:21], v[22:23] offset1:4
	v_pk_mov_b32 v[20:21], v[34:35], v[28:29] op_sel:[1,0]
	v_fma_mixlo_f16 v22, s0, v34, 0
	v_pk_mul_f32 v[20:21], s[0:1], v[20:21] op_sel_hi:[0,1]
	v_cvt_pk_f16_f32 v21, v20, v21
	v_pack_b32_f16 v20, v22, v21
	v_fma_mixlo_f16 v22, s0, v29, 0
	v_alignbit_b32 v21, v22, v21, 16
	v_pk_mov_b32 v[22:23], v[38:39], v[36:37] op_sel:[1,0]
	v_fma_mixlo_f16 v24, s0, v38, 0
	v_pk_mul_f32 v[22:23], s[0:1], v[22:23] op_sel_hi:[0,1]
	v_cvt_pk_f16_f32 v23, v22, v23
	v_pack_b32_f16 v22, v24, v23
	v_fma_mixlo_f16 v24, s0, v37, 0
	v_alignbit_b32 v23, v24, v23, 16
	ds_write2_b64 v46, v[20:21], v[22:23] offset0:8 offset1:12
	v_pk_mov_b32 v[20:21], v[78:79], v[40:41] op_sel:[1,0]
	v_fma_mixlo_f16 v22, s0, v78, 0
	v_pk_mul_f32 v[20:21], s[0:1], v[20:21] op_sel_hi:[0,1]
	v_cvt_pk_f16_f32 v21, v20, v21
	v_pack_b32_f16 v20, v22, v21
	v_fma_mixlo_f16 v22, s0, v41, 0
	v_alignbit_b32 v21, v22, v21, 16
	v_pk_mov_b32 v[22:23], v[74:75], v[76:77] op_sel:[1,0]
	v_fma_mixlo_f16 v24, s0, v74, 0
	v_pk_mul_f32 v[22:23], s[0:1], v[22:23] op_sel_hi:[0,1]
	v_cvt_pk_f16_f32 v23, v22, v23
	v_pack_b32_f16 v22, v24, v23
	v_fma_mixlo_f16 v24, s0, v77, 0
	v_alignbit_b32 v23, v24, v23, 16
	v_add_u32_e32 v24, 0x800, v46
	ds_write2_b64 v24, v[20:21], v[22:23] offset0:32 offset1:36
	v_pk_mov_b32 v[20:21], v[70:71], v[72:73] op_sel:[1,0]
	v_fma_mixlo_f16 v22, s0, v70, 0
	v_pk_mul_f32 v[20:21], s[0:1], v[20:21] op_sel_hi:[0,1]
	v_cvt_pk_f16_f32 v21, v20, v21
	v_pack_b32_f16 v20, v22, v21
	v_fma_mixlo_f16 v22, s0, v73, 0
	v_alignbit_b32 v21, v22, v21, 16
	v_pk_mov_b32 v[22:23], v[66:67], v[68:69] op_sel:[1,0]
	v_fma_mixlo_f16 v25, s0, v66, 0
	v_pk_mul_f32 v[22:23], s[0:1], v[22:23] op_sel_hi:[0,1]
	v_cvt_pk_f16_f32 v23, v22, v23
	v_pack_b32_f16 v22, v25, v23
	v_fma_mixlo_f16 v25, s0, v69, 0
	v_alignbit_b32 v23, v25, v23, 16
	ds_write2_b64 v24, v[20:21], v[22:23] offset0:40 offset1:44
	v_pk_mov_b32 v[20:21], v[58:59], v[60:61] op_sel:[1,0]
	v_fma_mixlo_f16 v22, s0, v58, 0
	v_pk_mul_f32 v[20:21], s[0:1], v[20:21] op_sel_hi:[0,1]
	v_cvt_pk_f16_f32 v21, v20, v21
	v_pack_b32_f16 v20, v22, v21
	v_fma_mixlo_f16 v22, s0, v61, 0
	v_alignbit_b32 v21, v22, v21, 16
	v_pk_mov_b32 v[22:23], v[42:43], v[44:45] op_sel:[1,0]
	v_fma_mixlo_f16 v24, s0, v42, 0
	v_pk_mul_f32 v[22:23], s[0:1], v[22:23] op_sel_hi:[0,1]
	v_cvt_pk_f16_f32 v23, v22, v23
	v_pack_b32_f16 v22, v24, v23
	v_fma_mixlo_f16 v24, s0, v45, 0
	v_alignbit_b32 v23, v24, v23, 16
	v_add_u32_e32 v24, 0x1000, v46
	ds_write2_b64 v24, v[20:21], v[22:23] offset0:64 offset1:68
	v_pk_mov_b32 v[20:21], v[30:31], v[14:15] op_sel:[1,0]
	v_fma_mixlo_f16 v22, s0, v30, 0
	v_pk_mul_f32 v[20:21], s[0:1], v[20:21] op_sel_hi:[0,1]
	v_cvt_pk_f16_f32 v20, v20, v21
	v_fma_mixlo_f16 v15, s0, v15, 0
	v_pack_b32_f16 v14, v22, v20
	v_alignbit_b32 v15, v15, v20, 16
	v_fma_mixlo_f16 v20, s0, v16, 0
	v_pk_mov_b32 v[16:17], v[16:17], v[18:19] op_sel:[1,0]
	v_fma_mixlo_f16 v18, s0, v19, 0
	v_pk_mul_f32 v[16:17], s[0:1], v[16:17] op_sel_hi:[0,1]
	v_cvt_pk_f16_f32 v17, v16, v17
	v_pack_b32_f16 v16, v20, v17
	v_alignbit_b32 v17, v18, v17, 16
	ds_write2_b64 v24, v[14:15], v[16:17] offset0:72 offset1:76
	v_pk_mov_b32 v[14:15], v[62:63], v[32:33] op_sel:[1,0]
	v_fma_mixlo_f16 v16, s0, v62, 0
	v_pk_mul_f32 v[14:15], s[0:1], v[14:15] op_sel_hi:[0,1]
	v_cvt_pk_f16_f32 v15, v14, v15
	v_pk_add_f32 v[4:5], v[4:5], v[48:49]
	v_pack_b32_f16 v14, v16, v15
	v_fma_mixlo_f16 v16, s0, v33, 0
	v_alignbit_b32 v15, v16, v15, 16
	v_fma_mixlo_f16 v16, s0, v2, 0
	v_pk_mov_b32 v[2:3], v[2:3], v[4:5] op_sel:[1,0]
	ds_read_b128 v[6:9], v6 offset:15360
	v_pk_mul_f32 v[2:3], s[0:1], v[2:3] op_sel_hi:[0,1]
	v_cvt_pk_f16_f32 v3, v2, v3
	v_fma_mixlo_f16 v4, s0, v5, 0
	s_waitcnt lgkmcnt(7)
	v_pk_add_f32 v[12:13], v[12:13], v[56:57]
	v_pk_add_f32 v[10:11], v[10:11], v[54:55]
	v_pack_b32_f16 v2, v16, v3
	v_alignbit_b32 v3, v4, v3, 16
	v_add_u32_e32 v16, 0x1800, v46
	ds_write2_b64 v16, v[14:15], v[2:3] offset0:96 offset1:100
	v_pk_mov_b32 v[2:3], v[10:11], v[12:13] op_sel:[1,0]
	v_fma_mixlo_f16 v4, s0, v10, 0
	v_pk_mul_f32 v[2:3], s[0:1], v[2:3] op_sel_hi:[0,1]
	v_cvt_pk_f16_f32 v3, v2, v3
	s_waitcnt lgkmcnt(1)
	v_pk_add_f32 v[8:9], v[8:9], v[52:53]
	v_pk_add_f32 v[6:7], v[6:7], v[50:51]
	v_pack_b32_f16 v2, v4, v3
	v_fma_mixlo_f16 v4, s0, v13, 0
	v_alignbit_b32 v3, v4, v3, 16
	v_pk_mov_b32 v[4:5], v[6:7], v[8:9] op_sel:[1,0]
	v_fma_mixlo_f16 v10, s0, v6, 0
	v_pk_mul_f32 v[4:5], s[0:1], v[4:5] op_sel_hi:[0,1]
	v_cvt_pk_f16_f32 v5, v4, v5
	v_fma_mixlo_f16 v6, s0, v9, 0
	v_pack_b32_f16 v4, v10, v5
	v_alignbit_b32 v5, v6, v5, 16
	ds_write2_b64 v16, v[2:3], v[4:5] offset0:104 offset1:108

_Z6conv_kILi128ELi64ELi20ELi64ELi4ELi4ELb0EEvPKDF16_S1_PKfS3_PDF16_S4_S1_fS3_S3_S3_S3_:
	v_readfirstlane_b32 s37, v0
	v_bfe_u32 v10, v0, 3, 3
	v_and_b32_e32 v1, 7, v0
	s_and_b32 s36, s2, 3
	s_ashr_i32 s35, s2, 6
	s_lshl_b32 s3, s2, 3
	s_lshr_b32 s42, s37, 6
	s_and_b32 s33, s2, 56
	v_bitop3_b32 v2, v10, v1, 6 bitop3:0x6c
	s_mul_i32 s2, s36, 5
	v_lshlrev_b32_e32 v4, 3, v2
	s_add_i32 s24, s2, s33
	v_lshl_or_b32 v2, s42, 3, v10
	s_mov_b32 s2, 0x28282829
	s_load_dwordx2 s[28:29], s[0:1], 0x0
	s_load_dword s88, s[0:1], 0x38
	s_load_dwordx2 s[84:85], s[0:1], 0x8
	s_load_dwordx2 s[86:87], s[0:1], 0x28
	s_load_dwordx2 s[4:5], s[0:1], 0x30
	v_mul_hi_u32 v3, v2, s2
	s_and_b32 s34, s3, 32
	v_lshrrev_b32_e32 v3, 3, v3
	s_movk_i32 s8, 0xffcd
	s_add_i32 s24, s24, -9
	v_mul_lo_u32 v5, v3, s8
	v_add_u32_e32 v103, s24, v3
	s_add_i32 s25, s34, -9
	s_movk_i32 s9, 0x264
	v_add3_u32 v5, s25, v2, v5
	v_cmp_gt_u32_e32 vcc, s9, v2
	v_cmp_gt_u32_e64 s[2:3], 64, v103
	s_and_b64 s[2:3], vcc, s[2:3]
	v_cmp_gt_u32_e32 vcc, 64, v5
	v_and_b32_e32 v102, 63, v0
	s_and_b64 s[6:7], s[2:3], vcc
	s_waitcnt lgkmcnt(0)
	v_mov_b64_e32 v[6:7], s[4:5]
	v_lshlrev_b32_e32 v2, 1, v4
	s_and_saveexec_b64 s[2:3], s[6:7]
	s_lshl_b32 s10, s35, 13
	v_lshlrev_b32_e32 v3, 6, v103
	v_or3_b32 v6, v3, s10, v5
	v_ashrrev_i32_e32 v7, 31, v6
	v_lshlrev_b64 v[6:7], 7, v[6:7]
	v_lshl_add_u64 v[6:7], s[28:29], 0, v[6:7]
	v_mov_b32_e32 v3, 0
	v_lshl_add_u64 v[6:7], v[6:7], 0, v[2:3]
	s_or_b64 exec, exec, s[2:3]
	s_lshl_b32 s44, s42, 10
	v_lshlrev_b32_e32 v104, 4, v102
	v_or_b32_e32 v3, s44, v104
	s_add_i32 s11, s42, 8
	v_readfirstlane_b32 s2, v3
	s_mov_b32 m0, s2
	v_lshl_or_b32 v3, s11, 3, v10
	global_load_lds_dwordx4 v[6:7], off
	s_mov_b32 s10, 0x50505051
	v_mul_hi_u32 v6, v3, s10
	v_lshrrev_b32_e32 v6, 4, v6
	v_mul_lo_u32 v7, v6, s8
	v_add_u32_e32 v105, s24, v6
	v_add3_u32 v8, s25, v3, v7
	v_cmp_gt_u32_e32 vcc, s9, v3
	v_cmp_gt_u32_e64 s[2:3], 64, v105
	s_and_b64 s[2:3], vcc, s[2:3]
	v_cmp_gt_u32_e32 vcc, 64, v8
	s_and_b64 s[8:9], s[2:3], vcc
	v_mov_b64_e32 v[6:7], s[4:5]
	s_and_saveexec_b64 s[2:3], s[8:9]
	s_lshl_b32 s12, s35, 13
	v_lshlrev_b32_e32 v3, 6, v105
	v_or3_b32 v6, v3, s12, v8
	v_ashrrev_i32_e32 v7, 31, v6
	v_lshlrev_b64 v[6:7], 7, v[6:7]
	v_lshl_add_u64 v[6:7], s[28:29], 0, v[6:7]
	v_mov_b32_e32 v3, 0
	v_lshl_add_u64 v[6:7], v[6:7], 0, v[2:3]
	s_or_b64 exec, exec, s[2:3]
	s_lshl_b32 s45, s11, 10
	v_or_b32_e32 v3, s45, v104
	s_add_i32 s14, s42, 16
	v_readfirstlane_b32 s2, v3
	s_mov_b32 m0, s2
	v_lshl_or_b32 v3, s14, 3, v10
	global_load_lds_dwordx4 v[6:7], off
	v_mul_hi_u32 v6, v3, s10
	v_lshrrev_b32_e32 v6, 4, v6
	s_movk_i32 s12, 0xffcd
	v_mul_lo_u32 v7, v6, s12
	v_add_u32_e32 v106, s24, v6
	s_movk_i32 s13, 0x264
	v_add3_u32 v9, s25, v3, v7
	v_cmp_gt_u32_e32 vcc, s13, v3
	v_cmp_gt_u32_e64 s[2:3], 64, v106
	s_and_b64 s[2:3], vcc, s[2:3]
	v_cmp_gt_u32_e32 vcc, 64, v9
	s_and_b64 s[10:11], s[2:3], vcc
	v_mov_b64_e32 v[6:7], s[4:5]
	s_and_saveexec_b64 s[2:3], s[10:11]
	s_lshl_b32 s15, s35, 13
	v_lshlrev_b32_e32 v3, 6, v106
	v_or3_b32 v6, v3, s15, v9
	v_ashrrev_i32_e32 v7, 31, v6
	v_lshlrev_b64 v[6:7], 7, v[6:7]
	v_lshl_add_u64 v[6:7], s[28:29], 0, v[6:7]
	v_mov_b32_e32 v3, 0
	v_lshl_add_u64 v[6:7], v[6:7], 0, v[2:3]
	s_or_b64 exec, exec, s[2:3]
	s_lshl_b32 s46, s14, 10
	v_or_b32_e32 v3, s46, v104
	s_add_i32 s15, s42, 24
	v_readfirstlane_b32 s2, v3
	s_mov_b32 m0, s2
	v_lshl_or_b32 v3, s15, 3, v10
	global_load_lds_dwordx4 v[6:7], off
	s_mov_b32 s14, 0x50505051
	v_mul_hi_u32 v6, v3, s14
	v_lshrrev_b32_e32 v6, 4, v6
	v_mul_lo_u32 v7, v6, s12
	v_add_u32_e32 v107, s24, v6
	v_add3_u32 v11, s25, v3, v7
	v_cmp_gt_u32_e32 vcc, s13, v3
	v_cmp_gt_u32_e64 s[2:3], 64, v107
	s_and_b64 s[2:3], vcc, s[2:3]
	v_cmp_gt_u32_e32 vcc, 64, v11
	s_and_b64 s[12:13], s[2:3], vcc
	v_mov_b64_e32 v[6:7], s[4:5]
	s_and_saveexec_b64 s[2:3], s[12:13]
	s_lshl_b32 s16, s35, 13
	v_lshlrev_b32_e32 v3, 6, v107
	v_or3_b32 v6, v3, s16, v11
	v_ashrrev_i32_e32 v7, 31, v6
	v_lshlrev_b64 v[6:7], 7, v[6:7]
	v_lshl_add_u64 v[6:7], s[28:29], 0, v[6:7]
	v_mov_b32_e32 v3, 0
	v_lshl_add_u64 v[6:7], v[6:7], 0, v[2:3]
	s_or_b64 exec, exec, s[2:3]
	s_lshl_b32 s47, s15, 10
	v_or_b32_e32 v3, s47, v104
	s_add_i32 s18, s42, 32
	v_readfirstlane_b32 s2, v3
	s_mov_b32 m0, s2
	v_lshl_or_b32 v3, s18, 3, v10
	global_load_lds_dwordx4 v[6:7], off
	v_mul_hi_u32 v6, v3, s14
	v_lshrrev_b32_e32 v6, 4, v6
	s_movk_i32 s16, 0xffcd
	v_mul_lo_u32 v7, v6, s16
	v_add_u32_e32 v108, s24, v6
	s_movk_i32 s17, 0x264
	v_add3_u32 v12, s25, v3, v7
	v_cmp_gt_u32_e32 vcc, s17, v3
	v_cmp_gt_u32_e64 s[2:3], 64, v108
	s_and_b64 s[2:3], vcc, s[2:3]
	v_cmp_gt_u32_e32 vcc, 64, v12
	s_and_b64 s[14:15], s[2:3], vcc
	v_mov_b64_e32 v[6:7], s[4:5]
	s_and_saveexec_b64 s[2:3], s[14:15]
	s_lshl_b32 s19, s35, 13
	v_lshlrev_b32_e32 v3, 6, v108
	v_or3_b32 v6, v3, s19, v12
	v_ashrrev_i32_e32 v7, 31, v6
	v_lshlrev_b64 v[6:7], 7, v[6:7]
	v_lshl_add_u64 v[6:7], s[28:29], 0, v[6:7]
	v_mov_b32_e32 v3, 0
	v_lshl_add_u64 v[6:7], v[6:7], 0, v[2:3]
	s_or_b64 exec, exec, s[2:3]
	s_lshl_b32 s48, s18, 10
	v_or_b32_e32 v3, s48, v104
	s_add_i32 s19, s42, 40
	v_readfirstlane_b32 s2, v3
	s_mov_b32 m0, s2
	v_lshl_or_b32 v3, s19, 3, v10
	global_load_lds_dwordx4 v[6:7], off
	s_mov_b32 s18, 0x50505051
	v_mul_hi_u32 v6, v3, s18
	v_lshrrev_b32_e32 v6, 4, v6
	v_mul_lo_u32 v7, v6, s16
	v_add_u32_e32 v109, s24, v6
	v_add3_u32 v13, s25, v3, v7
	v_cmp_gt_u32_e32 vcc, s17, v3
	v_cmp_gt_u32_e64 s[2:3], 64, v109
	s_and_b64 s[2:3], vcc, s[2:3]
	v_cmp_gt_u32_e32 vcc, 64, v13
	s_and_b64 s[16:17], s[2:3], vcc
	v_mov_b64_e32 v[6:7], s[4:5]
	s_and_saveexec_b64 s[2:3], s[16:17]
	s_lshl_b32 s20, s35, 13
	v_lshlrev_b32_e32 v3, 6, v109
	v_or3_b32 v6, v3, s20, v13
	v_ashrrev_i32_e32 v7, 31, v6
	v_lshlrev_b64 v[6:7], 7, v[6:7]
	v_lshl_add_u64 v[6:7], s[28:29], 0, v[6:7]
	v_mov_b32_e32 v3, 0
	v_lshl_add_u64 v[6:7], v[6:7], 0, v[2:3]
	s_or_b64 exec, exec, s[2:3]
	s_lshl_b32 s49, s19, 10
	v_or_b32_e32 v3, s49, v104
	s_add_i32 s22, s42, 48
	v_readfirstlane_b32 s2, v3
	s_mov_b32 m0, s2
	v_lshl_or_b32 v3, s22, 3, v10
	global_load_lds_dwordx4 v[6:7], off
	v_mul_hi_u32 v6, v3, s18
	v_lshrrev_b32_e32 v6, 4, v6
	s_movk_i32 s20, 0xffcd
	v_mul_lo_u32 v7, v6, s20
	v_add_u32_e32 v110, s24, v6
	s_movk_i32 s21, 0x264
	v_add3_u32 v14, s25, v3, v7
	v_cmp_gt_u32_e32 vcc, s21, v3
	v_cmp_gt_u32_e64 s[2:3], 64, v110
	s_and_b64 s[2:3], vcc, s[2:3]
	v_cmp_gt_u32_e32 vcc, 64, v14
	s_and_b64 s[18:19], s[2:3], vcc
	v_mov_b64_e32 v[6:7], s[4:5]
	s_and_saveexec_b64 s[2:3], s[18:19]
	s_lshl_b32 s23, s35, 13
	v_lshlrev_b32_e32 v3, 6, v110
	v_or3_b32 v6, v3, s23, v14
	v_ashrrev_i32_e32 v7, 31, v6
	v_lshlrev_b64 v[6:7], 7, v[6:7]
	v_lshl_add_u64 v[6:7], s[28:29], 0, v[6:7]
	v_mov_b32_e32 v3, 0
	v_lshl_add_u64 v[6:7], v[6:7], 0, v[2:3]
	s_or_b64 exec, exec, s[2:3]
	s_lshl_b32 s50, s22, 10
	v_or_b32_e32 v3, s50, v104
	s_add_i32 s23, s42, 56
	v_readfirstlane_b32 s2, v3
	s_mov_b32 m0, s2
	v_lshl_or_b32 v3, s23, 3, v10
	global_load_lds_dwordx4 v[6:7], off
	s_mov_b32 s22, 0x50505051
	v_mul_hi_u32 v6, v3, s22
	v_lshrrev_b32_e32 v6, 4, v6
	v_mul_lo_u32 v7, v6, s20
	v_add_u32_e32 v113, s24, v6
	v_add3_u32 v15, s25, v3, v7
	v_cmp_gt_u32_e32 vcc, s21, v3
	v_cmp_gt_u32_e64 s[2:3], 64, v113
	s_and_b64 s[2:3], vcc, s[2:3]
	v_cmp_gt_u32_e32 vcc, 64, v15
	s_and_b64 s[20:21], s[2:3], vcc
	v_mov_b64_e32 v[6:7], s[4:5]
	s_and_saveexec_b64 s[2:3], s[20:21]
	s_lshl_b32 s26, s35, 13
	v_lshlrev_b32_e32 v3, 6, v113
	v_or3_b32 v6, v3, s26, v15
	v_ashrrev_i32_e32 v7, 31, v6
	v_lshlrev_b64 v[6:7], 7, v[6:7]
	v_lshl_add_u64 v[6:7], s[28:29], 0, v[6:7]
	v_mov_b32_e32 v3, 0
	v_lshl_add_u64 v[6:7], v[6:7], 0, v[2:3]
	s_or_b64 exec, exec, s[2:3]
	s_lshl_b32 s51, s23, 10
	v_or_b32_e32 v3, s51, v104
	s_add_i32 s26, s42, 64
	v_readfirstlane_b32 s2, v3
	s_mov_b32 m0, s2
	v_lshl_or_b32 v3, s26, 3, v10
	global_load_lds_dwordx4 v[6:7], off
	v_mul_hi_u32 v6, v3, s22
	v_lshrrev_b32_e32 v6, 4, v6
	s_movk_i32 s2, 0xffcd
	v_mul_lo_u32 v7, v6, s2
	v_add_u32_e32 v114, s24, v6
	s_movk_i32 s2, 0x264
	v_add3_u32 v16, s25, v3, v7
	v_cmp_gt_u32_e32 vcc, s2, v3
	v_cmp_gt_u32_e64 s[2:3], 64, v114
	s_and_b64 s[2:3], vcc, s[2:3]
	v_cmp_gt_u32_e32 vcc, 64, v16
	s_and_b64 s[22:23], s[2:3], vcc
	s_xor_b64 s[2:3], s[22:23], -1
	s_and_saveexec_b64 s[30:31], s[2:3]
	s_xor_b64 s[2:3], exec, s[30:31]
	s_lshl_b32 s27, s35, 13
	s_or_saveexec_b64 s[2:3], s[2:3]
	v_mov_b32_e32 v17, s27
	v_mov_b64_e32 v[6:7], s[4:5]
	s_xor_b64 exec, exec, s[2:3]
	s_lshl_b32 s27, s35, 13
	v_lshlrev_b32_e32 v3, 6, v114
	v_or3_b32 v6, v3, s27, v16
	v_ashrrev_i32_e32 v7, 31, v6
	v_lshlrev_b64 v[6:7], 7, v[6:7]
	v_lshl_add_u64 v[6:7], s[28:29], 0, v[6:7]
	v_mov_b32_e32 v3, 0
	v_lshl_add_u64 v[6:7], v[6:7], 0, v[2:3]
	v_mov_b32_e32 v17, s27
	s_or_b64 exec, exec, s[2:3]
	s_lshl_b32 s38, s26, 10
	v_or_b32_e32 v2, s38, v104
	s_add_i32 s41, s42, 0x48
	v_readfirstlane_b32 s2, v2
	s_mov_b32 m0, s2
	v_lshl_or_b32 v2, s41, 3, v10
	global_load_lds_dwordx4 v[6:7], off
	s_mov_b32 s2, 0x50505051
	v_mul_hi_u32 v3, v2, s2
	v_lshrrev_b32_e32 v3, 4, v3
	s_movk_i32 s2, 0xffcd
	s_mov_b64 s[30:31], s[84:85]
	v_mul_lo_u32 v6, v3, s2
	v_add_u32_e32 v115, s24, v3
	s_movk_i32 s2, 0x264
	v_add3_u32 v6, s25, v2, v6
	v_cmp_gt_u32_e32 vcc, s2, v2
	v_cmp_gt_u32_e64 s[2:3], 64, v115
	s_and_b64 s[2:3], vcc, s[2:3]
	v_cmp_gt_u32_e32 vcc, 64, v6
	s_and_b64 s[24:25], s[2:3], vcc
	s_xor_b64 s[2:3], s[24:25], -1
	s_and_saveexec_b64 s[26:27], s[2:3]
	s_xor_b64 s[2:3], exec, s[26:27]
	s_or_saveexec_b64 s[26:27], s[2:3]
	s_mov_b64 s[2:3], s[86:87]
	v_mov_b64_e32 v[2:3], s[4:5]
	s_xor_b64 exec, exec, s[26:27]
	v_lshlrev_b32_e32 v2, 6, v115
	v_or3_b32 v2, v2, v17, v6
	v_ashrrev_i32_e32 v3, 31, v2
	v_lshlrev_b64 v[2:3], 7, v[2:3]
	v_lshl_add_u64 v[2:3], s[28:29], 0, v[2:3]
	v_lshlrev_b32_e32 v18, 1, v4
	v_mov_b32_e32 v19, 0
	v_lshl_add_u64 v[2:3], v[2:3], 0, v[18:19]
	s_or_b64 exec, exec, s[26:27]
	v_lshrrev_b32_e32 v112, 4, v102
	v_lshl_or_b32 v7, v10, 6, s44
	v_bitop3_b32 v10, v112, v0, 6 bitop3:0x78
	v_and_b32_e32 v111, 15, v0
	v_lshlrev_b32_e32 v10, 4, v10
	s_lshr_b32 s40, s37, 8
	v_lshl_or_b32 v10, v111, 7, v10
	v_lshl_or_b32 v10, s40, 13, v10
	s_lshl_b32 s41, s41, 10
	s_movk_i32 s26, 0xdc0
	v_add_u32_e32 v118, 0x14000, v10
	v_or_b32_e32 v10, s41, v104
	v_and_or_b32 v7, v7, s26, v4
	v_readfirstlane_b32 s26, v10
	s_mov_b32 m0, s26
	s_lshl_b32 s55, s42, 11
	s_mul_hi_u32 s26, s37, 0x51eb851f
	s_and_b32 s39, s42, 3
	s_add_i32 s42, s55, 0x14000
	s_lshr_b32 s27, s26, 13
	s_lshr_b32 s52, s26, 14
	s_bitcmp1_b32 s26, 13
	s_cselect_b32 s26, 0x190, 0
	s_sub_i32 s27, s36, s27
	s_add_i32 s27, s27, s52
	s_mulk_i32 s27, 0x64
	s_add_i32 s26, s26, s40
	s_add_i32 s26, s26, s27
	s_ashr_i32 s27, s26, 31
	s_lshl_b64 s[26:27], s[26:27], 13
	s_waitcnt lgkmcnt(0)
	s_add_u32 s26, s30, s26
	s_addc_u32 s27, s31, s27
	s_add_i32 s52, s40, 20
	global_load_lds_dwordx4 v[2:3], off
	v_lshlrev_b32_e32 v2, 1, v7
	s_mov_b32 m0, s42
	s_mul_hi_u32 s53, s52, 0x28f5c29
	global_load_lds_dwordx4 v2, s[26:27]
	s_add_i32 m0, s55, 0x14400
	s_lshr_b32 s56, s53, 1
	s_bitcmp1_b32 s53, 0
	s_cselect_b32 s57, 0x190, 0
	s_sub_i32 s53, s36, s53
	s_add_i32 s53, s53, s56
	s_mulk_i32 s53, 0x64
	s_add_i32 s52, s57, s52
	s_add_i32 s52, s52, s53
	v_mov_b32_e32 v3, 0
	s_ashr_i32 s53, s52, 31
	v_lshl_add_u64 v[18:19], s[26:27], 0, v[2:3]
	s_mov_b64 s[26:27], 0x400
	s_lshl_b64 s[52:53], s[52:53], 13
	v_lshl_add_u64 v[18:19], v[18:19], 0, s[26:27]
	s_add_u32 s52, s30, s52
	global_load_lds_dwordx4 v[18:19], off
	s_addc_u32 s53, s31, s53
	s_add_i32 m0, s55, 0x18000
	v_lshl_add_u64 v[18:19], s[52:53], 0, v[2:3]
	global_load_lds_dwordx4 v2, s[52:53]
	s_add_i32 s52, s40, 40
	s_mul_hi_u32 s53, s52, 0x28f5c29
	s_add_i32 m0, s55, 0x18400
	s_lshr_b32 s56, s53, 1
	s_bitcmp1_b32 s53, 0
	s_cselect_b32 s57, 0x190, 0
	s_sub_i32 s53, s36, s53
	s_add_i32 s53, s53, s56
	s_mulk_i32 s53, 0x64
	s_add_i32 s52, s57, s52
	s_add_i32 s52, s52, s53
	s_ashr_i32 s53, s52, 31
	s_lshl_b64 s[52:53], s[52:53], 13
	s_add_u32 s52, s30, s52
	v_lshl_add_u64 v[18:19], v[18:19], 0, s[26:27]
	s_addc_u32 s53, s31, s53
	global_load_lds_dwordx4 v[18:19], off
	s_add_i32 m0, s55, 0x1c000
	v_lshl_add_u64 v[18:19], s[52:53], 0, v[2:3]
	global_load_lds_dwordx4 v2, s[52:53]
	v_lshl_add_u64 v[18:19], v[18:19], 0, s[26:27]
	s_add_i32 m0, s55, 0x1c400
	s_mul_hi_u32 s52, s40, 0x28f5c29
	global_load_lds_dwordx4 v[18:19], off
	s_mulk_i32 s52, 0x64
	s_sub_i32 s52, s40, s52
	s_mul_i32 s53, s52, 0x67
	s_bfe_u32 s53, s53, 0x5000b
	s_mul_i32 s53, s53, 31
	s_mul_i32 s54, s39, 0x66
	s_and_b32 s53, s53, 0xff
	v_add_u32_e32 v116, s54, v111
	s_add_i32 s52, s52, s53
	s_waitcnt vmcnt(4) lgkmcnt(0)
	s_barrier
	ds_read_b128 v[66:69], v118
	v_add_u32_e32 v7, s52, v116
	v_add_u32_e32 v117, 51, v116
	ds_read_b128 v[70:73], v118 offset:2048
	v_lshlrev_b32_e32 v10, 7, v7
	v_bitop3_b32 v7, v7, v112, 6 bitop3:0x6c
	v_lshl_or_b32 v139, v7, 4, v10
	ds_read_b128 v[74:77], v139
	v_add_u32_e32 v7, s52, v117
	ds_read_b128 v[78:81], v139 offset:2048
	v_lshlrev_b32_e32 v10, 7, v7
	v_bitop3_b32 v7, v7, v112, 6 bitop3:0x6c
	v_lshl_or_b32 v140, v7, 4, v10
	ds_read_b128 v[86:89], v140
	ds_read_b128 v[82:85], v140 offset:2048
	ds_read_b128 v[94:97], v118 offset:4096
	ds_read_b128 v[90:93], v118 offset:6144
	v_add_u32_e32 v120, v17, v5
	v_lshlrev_b32_e32 v4, 1, v4
	v_mov_b32_e32 v5, v3
	v_lshl_add_u64 v[98:99], s[28:29], 0, v[4:5]
	s_add_i32 s28, s40, s54
	v_xor_b32_e32 v119, 64, v118
	s_mov_b32 s43, 0
	v_add_u32_e32 v121, v17, v8
	v_add_u32_e32 v122, v17, v9
	v_add_u32_e32 v123, v17, v11
	v_add_u32_e32 v124, v17, v12
	v_add_u32_e32 v125, v17, v13
	v_add_u32_e32 v126, v17, v14
	v_add_u32_e32 v127, v17, v15
	v_add_u32_e32 v128, v17, v16
	v_add_u32_e32 v129, v17, v6
	v_lshl_add_u64 v[100:101], s[30:31], 0, v[2:3]
	v_add_u32_e32 v130, s28, v111
	v_add_u32_e32 v131, s44, v104
	v_add_u32_e32 v132, s45, v104
	v_add_u32_e32 v133, s46, v104
	v_add_u32_e32 v134, s47, v104
	v_add_u32_e32 v135, s48, v104
	v_add_u32_e32 v136, s49, v104
	v_add_u32_e32 v137, s50, v104
	v_add_u32_e32 v138, s51, v104
	s_mov_b32 s30, s40
	s_mov_b32 s31, s40
	s_mov_b32 s44, 0
	s_mov_b32 s45, 0
	v_mov_b32_e32 v2, v3
	v_mov_b32_e32 v4, v3
	v_mov_b32_e32 v6, v3
	v_mov_b32_e32 v7, v3
	v_mov_b32_e32 v8, v3
	v_mov_b32_e32 v9, v3
	v_mov_b32_e32 v14, v3
	v_mov_b32_e32 v15, v3
	v_mov_b32_e32 v16, v3
	v_mov_b32_e32 v17, v3
	v_mov_b32_e32 v30, v3
	v_mov_b32_e32 v31, v3
	v_mov_b32_e32 v32, v3
	v_mov_b32_e32 v33, v3
	v_mov_b32_e32 v34, v3
	v_mov_b32_e32 v35, v3
	v_mov_b32_e32 v36, v3
	v_mov_b32_e32 v37, v3
	v_mov_b32_e32 v38, v3
	v_mov_b32_e32 v39, v3
	v_mov_b32_e32 v40, v3
	v_mov_b32_e32 v41, v3
	v_mov_b32_e32 v42, v3
	v_mov_b32_e32 v43, v3
	v_mov_b32_e32 v44, v3
	v_mov_b32_e32 v45, v3
	v_mov_b32_e32 v46, v3
	v_mov_b32_e32 v47, v3
	v_mov_b32_e32 v48, v3
	v_mov_b32_e32 v49, v3
	v_mov_b32_e32 v50, v3
	v_mov_b32_e32 v51, v3
	v_mov_b32_e32 v52, v3
	v_mov_b32_e32 v53, v3
	v_mov_b32_e32 v54, v3
	v_mov_b32_e32 v55, v3
	v_mov_b32_e32 v56, v3
	v_mov_b32_e32 v57, v3
	v_mov_b32_e32 v58, v3
	v_mov_b32_e32 v59, v3
	v_mov_b32_e32 v60, v3
	v_mov_b32_e32 v61, v3
	v_mov_b32_e32 v62, v3
	v_mov_b32_e32 v63, v3
	v_mov_b32_e32 v64, v3
	v_mov_b32_e32 v65, v3
	v_mov_b32_e32 v26, v3
	v_mov_b32_e32 v27, v3
	v_mov_b32_e32 v28, v3
	v_mov_b32_e32 v29, v3
	v_mov_b32_e32 v18, v3
	v_mov_b32_e32 v19, v3
	v_mov_b32_e32 v20, v3
	v_mov_b32_e32 v21, v3
	v_mov_b32_e32 v22, v3
	v_mov_b32_e32 v23, v3
	v_mov_b32_e32 v24, v3
	v_mov_b32_e32 v25, v3
	v_mov_b32_e32 v10, v3
	v_mov_b32_e32 v11, v3
	v_mov_b32_e32 v12, v3
	v_mov_b32_e32 v13, v3
	s_mov_b32 s60, 0
	s_mov_b32 s61, 5
	s_mov_b32 s62, 0
	s_mov_b32 s65, 0
	s_mov_b32 s66, 0
	s_mul_i32 s73, s36, 0x64
	s_add_i32 s73, s73, s40
	s_mov_b32 s68, s73
	s_mov_b32 s74, s40
	v_mov_b32_e32 v183, v119
	s_waitcnt lgkmcnt(0)

.LBB10_51:
	s_cmpk_gt_u32 s37, 0xff
	s_waitcnt vmcnt(0) lgkmcnt(0)
	s_barrier
	s_cbranch_scc1 .LBB10_53
	ds_read_b128 v[68:71], v66
	ds_read_b128 v[72:75], v66 offset:1024
	ds_read_b128 v[76:79], v66 offset:2048
	s_mov_b32 s0, s88
	s_and_b32 s1, s37, 0xc0
	s_waitcnt lgkmcnt(0)
	v_pk_add_f32 v[64:65], v[70:71], v[64:65]
	v_pk_add_f32 v[68:69], v[68:69], v[62:63]
	v_pk_add_f32 v[70:71], v[74:75], v[60:61]
	ds_read_b128 v[60:63], v66 offset:3072
	v_pk_add_f32 v[72:73], v[72:73], v[58:59]
	v_pk_add_f32 v[74:75], v[78:79], v[56:57]
	ds_read_b128 v[56:59], v66 offset:4096
	v_pk_add_f32 v[76:77], v[76:77], v[54:55]
	s_waitcnt lgkmcnt(1)
	v_pk_add_f32 v[62:63], v[62:63], v[52:53]
	ds_read_b128 v[52:55], v66 offset:5120
	v_pk_add_f32 v[60:61], v[60:61], v[50:51]
	s_waitcnt lgkmcnt(1)
	v_pk_add_f32 v[58:59], v[58:59], v[48:49]
	ds_read_b128 v[48:51], v66 offset:6144
	v_pk_add_f32 v[56:57], v[56:57], v[46:47]
	s_waitcnt lgkmcnt(1)
	v_pk_add_f32 v[54:55], v[54:55], v[44:45]
	ds_read_b128 v[44:47], v66 offset:7168
	v_pk_add_f32 v[52:53], v[52:53], v[42:43]
	s_waitcnt lgkmcnt(1)
	v_pk_add_f32 v[50:51], v[50:51], v[40:41]
	ds_read_b128 v[40:43], v66 offset:8192
	v_pk_add_f32 v[48:49], v[48:49], v[38:39]
	s_waitcnt lgkmcnt(1)
	v_pk_add_f32 v[46:47], v[46:47], v[36:37]
	ds_read_b128 v[36:39], v66 offset:9216
	v_pk_add_f32 v[44:45], v[44:45], v[34:35]
	s_waitcnt lgkmcnt(1)
	v_pk_add_f32 v[42:43], v[42:43], v[32:33]
	ds_read_b128 v[32:35], v66 offset:10240
	v_pk_add_f32 v[30:31], v[40:41], v[30:31]
	s_waitcnt lgkmcnt(1)
	v_pk_add_f32 v[78:79], v[38:39], v[16:17]
	ds_read_b128 v[38:41], v66 offset:11264
	v_pk_add_f32 v[36:37], v[36:37], v[14:15]
	ds_read_b128 v[14:17], v66 offset:12288
	s_waitcnt lgkmcnt(2)
	v_pk_add_f32 v[34:35], v[34:35], v[8:9]
	v_pk_add_f32 v[32:33], v[32:33], v[6:7]
	s_waitcnt lgkmcnt(1)
	v_pk_add_f32 v[40:41], v[40:41], v[4:5]
	v_pk_add_f32 v[38:39], v[38:39], v[2:3]
	ds_read_b128 v[2:5], v66 offset:13312
	s_waitcnt lgkmcnt(1)
	v_pk_add_f32 v[28:29], v[16:17], v[28:29]
	ds_read_b128 v[6:9], v66 offset:14336
	v_pk_add_f32 v[26:27], v[14:15], v[26:27]
	ds_read_b128 v[14:17], v66 offset:15360
	s_waitcnt lgkmcnt(2)
	v_pk_add_f32 v[2:3], v[2:3], v[18:19]
	v_fma_mixlo_f16 v19, s0, v72, 0
	v_pk_add_f32 v[4:5], v[4:5], v[20:21]
	v_fma_mixlo_f16 v20, s0, v44, 0
	s_waitcnt lgkmcnt(0)
	v_pk_add_f32 v[10:11], v[14:15], v[10:11]
	v_or_b32_e32 v14, s1, v111
	v_lshlrev_b32_e32 v15, 3, v112
	v_mul_u32_u24_e32 v14, 0x90, v14
	s_mov_b32 s1, 0x10000
	v_add3_u32 v18, v14, v15, s1
	v_pk_mov_b32 v[14:15], v[68:69], v[64:65] op_sel:[1,0]
	v_pk_add_f32 v[12:13], v[16:17], v[12:13]
	v_pk_mul_f32 v[14:15], s[0:1], v[14:15] op_sel_hi:[0,1]
	v_fma_mixlo_f16 v16, s0, v68, 0
	v_cvt_pk_f16_f32 v15, v14, v15
	v_pack_b32_f16 v14, v16, v15
	v_fma_mixlo_f16 v16, s0, v65, 0
	v_alignbit_b32 v15, v16, v15, 16
	v_pk_mov_b32 v[16:17], v[72:73], v[70:71] op_sel:[1,0]
	v_pk_add_f32 v[8:9], v[8:9], v[24:25]
	v_pk_mul_f32 v[16:17], s[0:1], v[16:17] op_sel_hi:[0,1]
	v_cvt_pk_f16_f32 v17, v16, v17
	v_pack_b32_f16 v16, v19, v17
	v_fma_mixlo_f16 v19, s0, v71, 0
	v_alignbit_b32 v17, v19, v17, 16
	ds_write2_b64 v18, v[14:15], v[16:17] offset1:4
	v_pk_mov_b32 v[14:15], v[76:77], v[74:75] op_sel:[1,0]
	v_fma_mixlo_f16 v16, s0, v76, 0
	v_pk_mul_f32 v[14:15], s[0:1], v[14:15] op_sel_hi:[0,1]
	v_cvt_pk_f16_f32 v15, v14, v15
	v_pack_b32_f16 v14, v16, v15
	v_fma_mixlo_f16 v16, s0, v75, 0
	v_alignbit_b32 v15, v16, v15, 16
	v_pk_mov_b32 v[16:17], v[60:61], v[62:63] op_sel:[1,0]
	v_fma_mixlo_f16 v19, s0, v60, 0
	v_pk_mul_f32 v[16:17], s[0:1], v[16:17] op_sel_hi:[0,1]
	v_cvt_pk_f16_f32 v17, v16, v17
	v_pack_b32_f16 v16, v19, v17
	v_fma_mixlo_f16 v19, s0, v63, 0
	v_alignbit_b32 v17, v19, v17, 16
	ds_write2_b64 v18, v[14:15], v[16:17] offset0:8 offset1:12
	v_pk_mov_b32 v[14:15], v[56:57], v[58:59] op_sel:[1,0]
	v_fma_mixlo_f16 v16, s0, v56, 0
	v_pk_mul_f32 v[14:15], s[0:1], v[14:15] op_sel_hi:[0,1]
	v_cvt_pk_f16_f32 v15, v14, v15
	v_pack_b32_f16 v14, v16, v15
	v_fma_mixlo_f16 v16, s0, v59, 0
	v_alignbit_b32 v15, v16, v15, 16
	v_pk_mov_b32 v[16:17], v[52:53], v[54:55] op_sel:[1,0]
	v_fma_mixlo_f16 v19, s0, v52, 0
	v_pk_mul_f32 v[16:17], s[0:1], v[16:17] op_sel_hi:[0,1]
	v_cvt_pk_f16_f32 v17, v16, v17
	v_pack_b32_f16 v16, v19, v17
	v_fma_mixlo_f16 v19, s0, v55, 0
	v_alignbit_b32 v17, v19, v17, 16
	v_add_u32_e32 v19, 0x800, v18
	ds_write2_b64 v19, v[14:15], v[16:17] offset0:32 offset1:36
	v_pk_mov_b32 v[14:15], v[48:49], v[50:51] op_sel:[1,0]
	v_fma_mixlo_f16 v16, s0, v48, 0
	v_pk_mul_f32 v[14:15], s[0:1], v[14:15] op_sel_hi:[0,1]
	v_cvt_pk_f16_f32 v15, v14, v15
	v_pack_b32_f16 v14, v16, v15
	v_fma_mixlo_f16 v16, s0, v51, 0
	v_alignbit_b32 v15, v16, v15, 16
	v_pk_mov_b32 v[16:17], v[44:45], v[46:47] op_sel:[1,0]
	v_pk_add_f32 v[6:7], v[6:7], v[22:23]
	v_pk_mul_f32 v[16:17], s[0:1], v[16:17] op_sel_hi:[0,1]
	v_cvt_pk_f16_f32 v17, v16, v17
	v_pack_b32_f16 v16, v20, v17
	v_fma_mixlo_f16 v20, s0, v47, 0
	v_alignbit_b32 v17, v20, v17, 16
	ds_write2_b64 v19, v[14:15], v[16:17] offset0:40 offset1:44
	v_pk_mov_b32 v[14:15], v[30:31], v[42:43] op_sel:[1,0]
	v_fma_mixlo_f16 v16, s0, v30, 0
	v_pk_mul_f32 v[14:15], s[0:1], v[14:15] op_sel_hi:[0,1]
	v_cvt_pk_f16_f32 v15, v14, v15
	v_pack_b32_f16 v14, v16, v15
	v_fma_mixlo_f16 v16, s0, v43, 0
	v_alignbit_b32 v15, v16, v15, 16
	v_pk_mov_b32 v[16:17], v[36:37], v[78:79] op_sel:[1,0]
	v_fma_mixlo_f16 v19, s0, v36, 0
	v_pk_mul_f32 v[16:17], s[0:1], v[16:17] op_sel_hi:[0,1]
	v_cvt_pk_f16_f32 v17, v16, v17
	v_pack_b32_f16 v16, v19, v17
	v_fma_mixlo_f16 v19, s0, v79, 0
	v_alignbit_b32 v17, v19, v17, 16
	v_add_u32_e32 v19, 0x1000, v18
	ds_write2_b64 v19, v[14:15], v[16:17] offset0:64 offset1:68
	v_pk_mov_b32 v[14:15], v[32:33], v[34:35] op_sel:[1,0]
	v_fma_mixlo_f16 v16, s0, v32, 0
	v_pk_mul_f32 v[14:15], s[0:1], v[14:15] op_sel_hi:[0,1]
	v_cvt_pk_f16_f32 v15, v14, v15
	v_pack_b32_f16 v14, v16, v15
	v_fma_mixlo_f16 v16, s0, v35, 0
	v_alignbit_b32 v15, v16, v15, 16
	v_pk_mov_b32 v[16:17], v[38:39], v[40:41] op_sel:[1,0]
	v_fma_mixlo_f16 v20, s0, v38, 0
	v_pk_mul_f32 v[16:17], s[0:1], v[16:17] op_sel_hi:[0,1]
	v_cvt_pk_f16_f32 v17, v16, v17
	v_pack_b32_f16 v16, v20, v17
	v_fma_mixlo_f16 v20, s0, v41, 0
	v_alignbit_b32 v17, v20, v17, 16
	ds_write2_b64 v19, v[14:15], v[16:17] offset0:72 offset1:76
	v_pk_mov_b32 v[14:15], v[26:27], v[28:29] op_sel:[1,0]
	v_fma_mixlo_f16 v16, s0, v26, 0
	v_pk_mul_f32 v[14:15], s[0:1], v[14:15] op_sel_hi:[0,1]
	v_cvt_pk_f16_f32 v15, v14, v15
	v_pack_b32_f16 v14, v16, v15
	v_fma_mixlo_f16 v16, s0, v29, 0
	v_alignbit_b32 v15, v16, v15, 16
	v_fma_mixlo_f16 v16, s0, v2, 0
	v_pk_mov_b32 v[2:3], v[2:3], v[4:5] op_sel:[1,0]
	v_fma_mixlo_f16 v4, s0, v5, 0
	v_pk_mul_f32 v[2:3], s[0:1], v[2:3] op_sel_hi:[0,1]
	v_cvt_pk_f16_f32 v3, v2, v3
	v_pack_b32_f16 v2, v16, v3
	v_alignbit_b32 v3, v4, v3, 16
	v_add_u32_e32 v16, 0x1800, v18
	ds_write2_b64 v16, v[14:15], v[2:3] offset0:96 offset1:100
	v_pk_mov_b32 v[2:3], v[6:7], v[8:9] op_sel:[1,0]
	v_fma_mixlo_f16 v4, s0, v6, 0
	v_pk_mul_f32 v[2:3], s[0:1], v[2:3] op_sel_hi:[0,1]
	v_cvt_pk_f16_f32 v3, v2, v3
	v_pack_b32_f16 v2, v4, v3
	v_fma_mixlo_f16 v4, s0, v9, 0
	v_alignbit_b32 v3, v4, v3, 16
	v_pk_mov_b32 v[4:5], v[10:11], v[12:13] op_sel:[1,0]
	v_fma_mixlo_f16 v6, s0, v10, 0
	v_pk_mul_f32 v[4:5], s[0:1], v[4:5] op_sel_hi:[0,1]
	v_cvt_pk_f16_f32 v5, v4, v5
	v_pack_b32_f16 v4, v6, v5
	v_fma_mixlo_f16 v6, s0, v13, 0
	v_alignbit_b32 v5, v6, v5, 16
	ds_write2_b64 v16, v[2:3], v[4:5] offset0:104 offset1:108

amdhsa.kernels:
  - .agpr_count:     0
    .args:
      - .actual_access:  read_only
        .address_space:  global
        .offset:         0
        .size:           8
        .value_kind:     global_buffer
      - .actual_access:  read_only
        .address_space:  global
        .offset:         8
        .size:           8
        .value_kind:     global_buffer
      - .actual_access:  read_only
        .address_space:  global
        .offset:         16
        .size:           8
        .value_kind:     global_buffer
      - .actual_access:  read_only
        .address_space:  global
        .offset:         24
        .size:           8
        .value_kind:     global_buffer
      - .actual_access:  read_only
        .address_space:  global
        .offset:         32
        .size:           8
        .value_kind:     global_buffer
      - .actual_access:  read_only
        .address_space:  global
        .offset:         40
        .size:           8
        .value_kind:     global_buffer
      - .actual_access:  write_only
        .address_space:  global
        .offset:         48
        .size:           8
        .value_kind:     global_buffer
      - .actual_access:  write_only
        .address_space:  global
        .offset:         56
        .size:           8
        .value_kind:     global_buffer
      - .actual_access:  write_only
        .address_space:  global
        .offset:         64
        .size:           8
        .value_kind:     global_buffer
      - .actual_access:  write_only
        .address_space:  global
        .offset:         72
        .size:           8
        .value_kind:     global_buffer
      - .actual_access:  write_only
        .address_space:  global
        .offset:         80
        .size:           8
        .value_kind:     global_buffer
      - .actual_access:  write_only
        .address_space:  global
        .offset:         88
        .size:           8
        .value_kind:     global_buffer
      - .actual_access:  read_only
        .address_space:  global
        .offset:         96
        .size:           8
        .value_kind:     global_buffer
      - .actual_access:  read_only
        .address_space:  global
        .offset:         104
        .size:           8
        .value_kind:     global_buffer
      - .actual_access:  read_only
        .address_space:  global
        .offset:         112
        .size:           8
        .value_kind:     global_buffer
      - .actual_access:  read_only
        .address_space:  global
        .offset:         120
        .size:           8
        .value_kind:     global_buffer
      - .actual_access:  write_only
        .address_space:  global
        .offset:         128
        .size:           8
        .value_kind:     global_buffer
      - .actual_access:  write_only
        .address_space:  global
        .offset:         136
        .size:           8
        .value_kind:     global_buffer
    .group_segment_fixed_size: 14400
    .kernarg_segment_align: 8
    .kernarg_segment_size: 144
    .language:       OpenCL C
    .language_version:
      - 2
      - 0
    .max_flat_workgroup_size: 256
    .name:           _Z10prep_all_kPKfS0_S0_S0_S0_S0_PDF16_S1_S1_S1_S1_S1_S0_S0_S0_S0_S1_Pj
    .private_segment_fixed_size: 0
    .sgpr_count:     27
    .sgpr_spill_count: 0
    .symbol:         _Z10prep_all_kPKfS0_S0_S0_S0_S0_PDF16_S1_S1_S1_S1_S1_S0_S0_S0_S0_S1_Pj.kd
    .uniform_work_group_size: 1
    .uses_dynamic_stack: false
    .vgpr_count:     64
    .vgpr_spill_count: 0
    .wavefront_size: 64
  - .agpr_count:     0
    .args:
      - .actual_access:  read_only
        .address_space:  global
        .offset:         0
        .size:           8
        .value_kind:     global_buffer
      - .actual_access:  read_only
        .address_space:  global
        .offset:         8
        .size:           8
        .value_kind:     global_buffer
      - .actual_access:  read_only
        .address_space:  global
        .offset:         16
        .size:           8
        .value_kind:     global_buffer
      - .actual_access:  read_only
        .address_space:  global
        .offset:         24
        .size:           8
        .value_kind:     global_buffer
      - .actual_access:  read_only
        .address_space:  global
        .offset:         32
        .size:           8
        .value_kind:     global_buffer
      - .actual_access:  read_only
        .address_space:  global
        .offset:         40
        .size:           8
        .value_kind:     global_buffer
      - .actual_access:  write_only
        .address_space:  global
        .offset:         48
        .size:           8
        .value_kind:     global_buffer
    .group_segment_fixed_size: 0
    .kernarg_segment_align: 8
    .kernarg_segment_size: 56
    .language:       OpenCL C
    .language_version:
      - 2
      - 0
    .max_flat_workgroup_size: 256
    .name:           _Z9finish6_kPKDF16_PKfS2_S2_S2_S2_Pf
    .private_segment_fixed_size: 0
    .sgpr_count:     26
    .sgpr_spill_count: 0
    .symbol:         _Z9finish6_kPKDF16_PKfS2_S2_S2_S2_Pf.kd
    .uniform_work_group_size: 1
    .uses_dynamic_stack: false
    .vgpr_count:     51
    .vgpr_spill_count: 0
    .wavefront_size: 64
  - .agpr_count:     0
    .args:
      - .actual_access:  read_only
        .address_space:  global
        .offset:         0
        .size:           8
        .value_kind:     global_buffer
      - .actual_access:  write_only
        .address_space:  global
        .offset:         8
        .size:           8
        .value_kind:     global_buffer
    .group_segment_fixed_size: 16640
    .kernarg_segment_align: 8
    .kernarg_segment_size: 16
    .language:       OpenCL C
    .language_version:
      - 2
      - 0
    .max_flat_workgroup_size: 256
    .name:           _Z6gram_kPKfPf
    .private_segment_fixed_size: 0
    .sgpr_count:     16
    .sgpr_spill_count: 0
    .symbol:         _Z6gram_kPKfPf.kd
    .uniform_work_group_size: 1
    .uses_dynamic_stack: false
    .vgpr_count:     38
    .vgpr_spill_count: 0
    .wavefront_size: 64
  - .agpr_count:     0
    .args:
      - .actual_access:  read_only
        .address_space:  global
        .offset:         0
        .size:           8
        .value_kind:     global_buffer
      - .address_space:  global
        .offset:         8
        .size:           8
        .value_kind:     global_buffer
      - .actual_access:  read_only
        .address_space:  global
        .offset:         16
        .size:           8
        .value_kind:     global_buffer
      - .actual_access:  read_only
        .address_space:  global
        .offset:         24
        .size:           8
        .value_kind:     global_buffer
      - .actual_access:  read_only
        .address_space:  global
        .offset:         32
        .size:           8
        .value_kind:     global_buffer
      - .actual_access:  write_only
        .address_space:  global
        .offset:         40
        .size:           8
        .value_kind:     global_buffer
      - .actual_access:  read_only
        .address_space:  global
        .offset:         48
        .size:           8
        .value_kind:     global_buffer
      - .offset:         56
        .size:           4
        .value_kind:     by_value
      - .actual_access:  read_only
        .address_space:  global
        .offset:         64
        .size:           8
        .value_kind:     global_buffer
      - .actual_access:  read_only
        .address_space:  global
        .offset:         72
        .size:           8
        .value_kind:     global_buffer
      - .actual_access:  read_only
        .address_space:  global
        .offset:         80
        .size:           8
        .value_kind:     global_buffer
      - .actual_access:  read_only
        .address_space:  global
        .offset:         88
        .size:           8
        .value_kind:     global_buffer
    .group_segment_fixed_size: 147456
    .kernarg_segment_align: 8
    .kernarg_segment_size: 96
    .language:       OpenCL C
    .language_version:
      - 2
      - 0
    .max_flat_workgroup_size: 512
    .name:           _Z6conv_kILi64ELi128ELi20ELi128ELi4ELi4ELb1EEvPKDF16_S1_PKfS3_PDF16_S4_S1_fS3_S3_S3_S3_
    .private_segment_fixed_size: 0
    .sgpr_count:     43
    .sgpr_spill_count: 0
    .symbol:         _Z6conv_kILi64ELi128ELi20ELi128ELi4ELi4ELb1EEvPKDF16_S1_PKfS3_PDF16_S4_S1_fS3_S3_S3_S3_.kd
    .uniform_work_group_size: 1
    .uses_dynamic_stack: false
    .vgpr_count:     160
    .vgpr_spill_count: 0
    .wavefront_size: 64
  - .agpr_count:     0
    .args:
      - .actual_access:  read_only
        .address_space:  global
        .offset:         0
        .size:           8
        .value_kind:     global_buffer
      - .actual_access:  read_only
        .address_space:  global
        .offset:         8
        .size:           8
        .value_kind:     global_buffer
      - .actual_access:  read_only
        .address_space:  global
        .offset:         16
        .size:           8
        .value_kind:     global_buffer
      - .actual_access:  write_only
        .address_space:  global
        .offset:         24
        .size:           8
        .value_kind:     global_buffer
    .group_segment_fixed_size: 0
    .kernarg_segment_align: 8
    .kernarg_segment_size: 32
    .language:       OpenCL C
    .language_version:
      - 2
      - 0
    .max_flat_workgroup_size: 256
    .name:           _Z8finish_kILi128ELi4EEvPKDF16_PKfS3_PDF16_
    .private_segment_fixed_size: 0
    .sgpr_count:     18
    .sgpr_spill_count: 0
    .symbol:         _Z8finish_kILi128ELi4EEvPKDF16_PKfS3_PDF16_.kd
    .uniform_work_group_size: 1
    .uses_dynamic_stack: false
    .vgpr_count:     44
    .vgpr_spill_count: 0
    .wavefront_size: 64
  - .agpr_count:     0
    .args:
      - .address_space:  global
        .offset:         0
        .size:           8
        .value_kind:     global_buffer
      - .address_space:  global
        .offset:         8
        .size:           8
        .value_kind:     global_buffer
      - .address_space:  global
        .offset:         16
        .size:           8
        .value_kind:     global_buffer
      - .actual_access:  read_only
        .address_space:  global
        .offset:         24
        .size:           8
        .value_kind:     global_buffer
      - .actual_access:  write_only
        .address_space:  global
        .offset:         32
        .size:           8
        .value_kind:     global_buffer
      - .actual_access:  read_only
        .address_space:  global
        .offset:         40
        .size:           8
        .value_kind:     global_buffer
      - .address_space:  global
        .offset:         48
        .size:           8
        .value_kind:     global_buffer
      - .offset:         56
        .size:           4
        .value_kind:     by_value
      - .actual_access:  read_only
        .address_space:  global
        .offset:         64
        .size:           8
        .value_kind:     global_buffer
      - .actual_access:  read_only
        .address_space:  global
        .offset:         72
        .size:           8
        .value_kind:     global_buffer
      - .actual_access:  read_only
        .address_space:  global
        .offset:         80
        .size:           8
        .value_kind:     global_buffer
      - .actual_access:  read_only
        .address_space:  global
        .offset:         88
        .size:           8
        .value_kind:     global_buffer
    .group_segment_fixed_size: 163840
    .kernarg_segment_align: 8
    .kernarg_segment_size: 96
    .language:       OpenCL C
    .language_version:
      - 2
      - 0
    .max_flat_workgroup_size: 512
    .name:           _Z6conv_kILi128ELi256ELi3ELi64ELi1ELi1ELb0EEvPKDF16_S1_PKfS3_PDF16_S4_S1_fS3_S3_S3_S3_
    .private_segment_fixed_size: 0
    .sgpr_count:     51
    .sgpr_spill_count: 0
    .symbol:         _Z6conv_kILi128ELi256ELi3ELi64ELi1ELi1ELb0EEvPKDF16_S1_PKfS3_PDF16_S4_S1_fS3_S3_S3_S3_.kd
    .uniform_work_group_size: 1
    .uses_dynamic_stack: false
    .vgpr_count:     184
    .vgpr_spill_count: 0
    .wavefront_size: 64
  - .agpr_count:     0
    .args:
      - .address_space:  global
        .offset:         0
        .size:           8
        .value_kind:     global_buffer
      - .address_space:  global
        .offset:         8
        .size:           8
        .value_kind:     global_buffer
      - .address_space:  global
        .offset:         16
        .size:           8
        .value_kind:     global_buffer
      - .actual_access:  read_only
        .address_space:  global
        .offset:         24
        .size:           8
        .value_kind:     global_buffer
      - .actual_access:  write_only
        .address_space:  global
        .offset:         32
        .size:           8
        .value_kind:     global_buffer
      - .actual_access:  read_only
        .address_space:  global
        .offset:         40
        .size:           8
        .value_kind:     global_buffer
      - .address_space:  global
        .offset:         48
        .size:           8
        .value_kind:     global_buffer
      - .offset:         56
        .size:           4
        .value_kind:     by_value
      - .actual_access:  read_only
        .address_space:  global
        .offset:         64
        .size:           8
        .value_kind:     global_buffer
      - .actual_access:  read_only
        .address_space:  global
        .offset:         72
        .size:           8
        .value_kind:     global_buffer
      - .actual_access:  read_only
        .address_space:  global
        .offset:         80
        .size:           8
        .value_kind:     global_buffer
      - .actual_access:  read_only
        .address_space:  global
        .offset:         88
        .size:           8
        .value_kind:     global_buffer
    .group_segment_fixed_size: 163840
    .kernarg_segment_align: 8
    .kernarg_segment_size: 96
    .language:       OpenCL C
    .language_version:
      - 2
      - 0
    .max_flat_workgroup_size: 512
    .name:           _Z6conv_kILi256ELi512ELi3ELi128ELi1ELi1ELb0EEvPKDF16_S1_PKfS3_PDF16_S4_S1_fS3_S3_S3_S3_
    .private_segment_fixed_size: 0
    .sgpr_count:     64
    .sgpr_spill_count: 0
    .symbol:         _Z6conv_kILi256ELi512ELi3ELi128ELi1ELi1ELb0EEvPKDF16_S1_PKfS3_PDF16_S4_S1_fS3_S3_S3_S3_.kd
    .uniform_work_group_size: 1
    .uses_dynamic_stack: false
    .vgpr_count:     184
    .vgpr_spill_count: 0
    .wavefront_size: 64
  - .agpr_count:     0
    .args:
      - .address_space:  global
        .offset:         0
        .size:           8
        .value_kind:     global_buffer
      - .address_space:  global
        .offset:         8
        .size:           8
        .value_kind:     global_buffer
      - .address_space:  global
        .offset:         16
        .size:           8
        .value_kind:     global_buffer
      - .actual_access:  read_only
        .address_space:  global
        .offset:         24
        .size:           8
        .value_kind:     global_buffer
      - .actual_access:  write_only
        .address_space:  global
        .offset:         32
        .size:           8
        .value_kind:     global_buffer
      - .actual_access:  read_only
        .address_space:  global
        .offset:         40
        .size:           8
        .value_kind:     global_buffer
      - .address_space:  global
        .offset:         48
        .size:           8
        .value_kind:     global_buffer
      - .offset:         56
        .size:           4
        .value_kind:     by_value
      - .actual_access:  read_only
        .address_space:  global
        .offset:         64
        .size:           8
        .value_kind:     global_buffer
      - .actual_access:  read_only
        .address_space:  global
        .offset:         72
        .size:           8
        .value_kind:     global_buffer
      - .actual_access:  read_only
        .address_space:  global
        .offset:         80
        .size:           8
        .value_kind:     global_buffer
      - .actual_access:  read_only
        .address_space:  global
        .offset:         88
        .size:           8
        .value_kind:     global_buffer
    .group_segment_fixed_size: 163840
    .kernarg_segment_align: 8
    .kernarg_segment_size: 96
    .language:       OpenCL C
    .language_version:
      - 2
      - 0
    .max_flat_workgroup_size: 512
    .name:           _Z6conv_kILi512ELi256ELi3ELi64ELi1ELi1ELb0EEvPKDF16_S1_PKfS3_PDF16_S4_S1_fS3_S3_S3_S3_
    .private_segment_fixed_size: 0
    .sgpr_count:     66
    .sgpr_spill_count: 0
    .symbol:         _Z6conv_kILi512ELi256ELi3ELi64ELi1ELi1ELb0EEvPKDF16_S1_PKfS3_PDF16_S4_S1_fS3_S3_S3_S3_.kd
    .uniform_work_group_size: 1
    .uses_dynamic_stack: false
    .vgpr_count:     208
    .vgpr_spill_count: 0
    .wavefront_size: 64
  - .agpr_count:     0
    .args:
      - .address_space:  global
        .offset:         0
        .size:           8
        .value_kind:     global_buffer
      - .address_space:  global
        .offset:         8
        .size:           8
        .value_kind:     global_buffer
      - .actual_access:  read_only
        .address_space:  global
        .offset:         16
        .size:           8
        .value_kind:     global_buffer
      - .actual_access:  read_only
        .address_space:  global
        .offset:         24
        .size:           8
        .value_kind:     global_buffer
      - .actual_access:  read_only
        .address_space:  global
        .offset:         32
        .size:           8
        .value_kind:     global_buffer
      - .actual_access:  write_only
        .address_space:  global
        .offset:         40
        .size:           8
        .value_kind:     global_buffer
      - .address_space:  global
        .offset:         48
        .size:           8
        .value_kind:     global_buffer
      - .offset:         56
        .size:           4
        .value_kind:     by_value
      - .actual_access:  read_only
        .address_space:  global
        .offset:         64
        .size:           8
        .value_kind:     global_buffer
      - .actual_access:  read_only
        .address_space:  global
        .offset:         72
        .size:           8
        .value_kind:     global_buffer
      - .actual_access:  read_only
        .address_space:  global
        .offset:         80
        .size:           8
        .value_kind:     global_buffer
      - .actual_access:  read_only
        .address_space:  global
        .offset:         88
        .size:           8
        .value_kind:     global_buffer
    .group_segment_fixed_size: 163840
    .kernarg_segment_align: 8
    .kernarg_segment_size: 96
    .language:       OpenCL C
    .language_version:
      - 2
      - 0
    .max_flat_workgroup_size: 512
    .name:           _Z6conv_kILi256ELi128ELi3ELi64ELi1ELi2ELb0EEvPKDF16_S1_PKfS3_PDF16_S4_S1_fS3_S3_S3_S3_
    .private_segment_fixed_size: 0
    .sgpr_count:     55
    .sgpr_spill_count: 0
    .symbol:         _Z6conv_kILi256ELi128ELi3ELi64ELi1ELi2ELb0EEvPKDF16_S1_PKfS3_PDF16_S4_S1_fS3_S3_S3_S3_.kd
    .uniform_work_group_size: 1
    .uses_dynamic_stack: false
    .vgpr_count:     172
    .vgpr_spill_count: 0
    .wavefront_size: 64
  - .agpr_count:     0
    .args:
      - .actual_access:  read_only
        .address_space:  global
        .offset:         0
        .size:           8
        .value_kind:     global_buffer
      - .actual_access:  read_only
        .address_space:  global
        .offset:         8
        .size:           8
        .value_kind:     global_buffer
      - .actual_access:  read_only
        .address_space:  global
        .offset:         16
        .size:           8
        .value_kind:     global_buffer
      - .actual_access:  write_only
        .address_space:  global
        .offset:         24
        .size:           8
        .value_kind:     global_buffer
    .group_segment_fixed_size: 0
    .kernarg_segment_align: 8
    .kernarg_segment_size: 32
    .language:       OpenCL C
    .language_version:
      - 2
      - 0
    .max_flat_workgroup_size: 256
    .name:           _Z8finish_kILi128ELi2EEvPKDF16_PKfS3_PDF16_
    .private_segment_fixed_size: 0
    .sgpr_count:     18
    .sgpr_spill_count: 0
    .symbol:         _Z8finish_kILi128ELi2EEvPKDF16_PKfS3_PDF16_.kd
    .uniform_work_group_size: 1
    .uses_dynamic_stack: false
    .vgpr_count:     28
    .vgpr_spill_count: 0
    .wavefront_size: 64
  - .agpr_count:     0
    .args:
      - .address_space:  global
        .offset:         0
        .size:           8
        .value_kind:     global_buffer
      - .address_space:  global
        .offset:         8
        .size:           8
        .value_kind:     global_buffer
      - .actual_access:  read_only
        .address_space:  global
        .offset:         16
        .size:           8
        .value_kind:     global_buffer
      - .actual_access:  read_only
        .address_space:  global
        .offset:         24
        .size:           8
        .value_kind:     global_buffer
      - .actual_access:  read_only
        .address_space:  global
        .offset:         32
        .size:           8
        .value_kind:     global_buffer
      - .actual_access:  write_only
        .address_space:  global
        .offset:         40
        .size:           8
        .value_kind:     global_buffer
      - .address_space:  global
        .offset:         48
        .size:           8
        .value_kind:     global_buffer
      - .offset:         56
        .size:           4
        .value_kind:     by_value
      - .actual_access:  read_only
        .address_space:  global
        .offset:         64
        .size:           8
        .value_kind:     global_buffer
      - .actual_access:  read_only
        .address_space:  global
        .offset:         72
        .size:           8
        .value_kind:     global_buffer
      - .actual_access:  read_only
        .address_space:  global
        .offset:         80
        .size:           8
        .value_kind:     global_buffer
      - .actual_access:  read_only
        .address_space:  global
        .offset:         88
        .size:           8
        .value_kind:     global_buffer
    .group_segment_fixed_size: 147456
    .kernarg_segment_align: 8
    .kernarg_segment_size: 96
    .language:       OpenCL C
    .language_version:
      - 2
      - 0
    .max_flat_workgroup_size: 512
    .name:           _Z6conv_kILi128ELi64ELi20ELi64ELi4ELi4ELb0EEvPKDF16_S1_PKfS3_PDF16_S4_S1_fS3_S3_S3_S3_
    .private_segment_fixed_size: 0
    .sgpr_count:     64
    .sgpr_spill_count: 0
    .symbol:         _Z6conv_kILi128ELi64ELi20ELi64ELi4ELi4ELb0EEvPKDF16_S1_PKfS3_PDF16_S4_S1_fS3_S3_S3_S3_.kd
    .uniform_work_group_size: 1
    .uses_dynamic_stack: false
    .vgpr_count:     184
    .vgpr_spill_count: 0
    .wavefront_size: 64
